# stack on v6: SGU gain hoist + Vl swizzle, H router LDS pipelining, M gate loads batched, attention counted lgkmcnt, conv rows 4 per trip
# speedup vs baseline: 1.0107x; 1.0079x over previous
; __device__ __forceinline__ int opaque_tid() { int t = threadIdx.x; asm volatile("" : "+v"(t)); return t; }
; __device__ __forceinline__ unsigned char* opaque_ptr(unsigned char* q) { long z = 0; asm volatile("" : "+s"(z)); return q + z; }
; template <bool MAIN, bool CONV>
; __device__ __forceinline__ void b_row(const Params& p, unsigned char* ws, int l, int row, int lane) {
;     ...
;     if (CONV) {
;         ca = *(const u32x4*)(pr + C_CVC + c0); ch = *(const u32x4*)(pr + C_CVH + c0); bg = *(const u32x4*)(pr + C_CVB + c0);
;         if (t > 0) { pa = *(const u32x4*)(pr - INP + C_CVC + c0); ph = *(const u32x4*)(pr - INP + C_CVH + c0); }
;         if (t < seqlen - 1) { na = *(const u32x4*)(pr + INP + C_CVC + c0); nh = *(const u32x4*)(pr + INP + C_CVH + c0); }
;         const float* cw = p.in[I_CONVW] + (size_t)l * 3 * 512 + c0;
;         cw0a = *(const f32x4*)cw; cw0b = *(const f32x4*)(cw + 4); cw1a = *(const f32x4*)(cw + 512); cw1b = *(const f32x4*)(cw + 516); cw2a = *(const f32x4*)(cw + 1024); cw2b = *(const f32x4*)(cw + 1028);
;     }
; __global__ void __launch_bounds__(512, 2) fwd(Params p) {
;     ...
;             if (G == 256) { const int j = c < 112 ? c : (c >= 208 ? 112 + (c - 208) : -1);
;                 if (j >= 0) { unsigned char* wsq = opaque_ptr(p.ws); const int t_ = opaque_tid(); const int nit = (l == 0 ? MT : NLAT) / 8;
;                     for (int it = j; it < nit; it += 160) b_row<false, true>(p, wsq, l, it * 8 + (t_ >> 6), t_ & 63); } }
.LBB0_725:
	v_readlane_b32 s0, v254, 24
	v_readlane_b32 s1, v254, 25
	s_andn2_b64 vcc, exec, s[0:1]
	s_cbranch_vccnz .LBB0_733
	s_lshr_b32 s2, s62, 3
	v_readlane_b32 s0, v255, 35
	s_cmp_ge_i32 s0, s2
	s_mov_b64 s[0:1], 0
	v_mov_b32_e32 v2, v0
	s_cbranch_scc1 .LBB0_733
	v_readlane_b32 s36, v251, 32
	v_readlane_b32 s12, v252, 5
	v_readlane_b32 s40, v251, 36
	v_readlane_b32 s41, v251, 37
	v_readlane_b32 s13, v252, 6
	s_mul_i32 s4, s12, 0x600
	v_readlane_b32 s42, v251, 38
	v_readlane_b32 s43, v251, 39
	v_readlane_b32 s44, v251, 40
	v_readlane_b32 s45, v251, 41
	v_readlane_b32 s46, v251, 42
	v_readlane_b32 s47, v251, 43
	v_readlane_b32 s48, v251, 44
	v_readlane_b32 s49, v251, 45
	v_readlane_b32 s50, v251, 46
	v_readlane_b32 s51, v251, 47
	s_mov_b64 s[16:17], s[40:41]
	s_lshl_b64 s[12:13], s[4:5], 2
	s_mov_b64 s[18:19], s[42:43]
	s_add_u32 s12, s18, s12
	v_lshlrev_b32_e32 v3, 5, v2
	s_addc_u32 s13, s19, s13
	v_and_b32_e32 v206, 0x7e0, v3
	v_lshl_add_u64 v[42:43], s[12:13], 0, v[206:207]
	s_mov_b64 s[12:13], 0x1000
	v_ashrrev_i32_e32 v4, 6, v2
	v_lshl_add_u64 v[44:45], v[42:43], 0, s[12:13]
	v_readlane_b32 s12, v255, 38
	v_readlane_b32 s13, v255, 39
	v_and_b32_e32 v2, 63, v2
	v_ashrrev_i32_e32 v5, 31, v4
	v_readlane_b32 s3, v255, 36
	v_add_u32_e32 v52, s12, v4
	v_lshlrev_b32_e32 v206, 4, v2
	v_lshl_add_u64 v[2:3], s[12:13], 0, v[4:5]
	s_add_u32 s12, s3, s0
	v_readlane_b32 s3, v255, 37
	s_addc_u32 s13, s3, s1
	s_add_u32 s0, s84, s0
	v_lshlrev_b64 v[4:5], 12, v[2:3]
	s_addc_u32 s1, s85, s1
	v_lshl_add_u64 v[46:47], s[12:13], 0, v[4:5]
	v_mov_b64_e32 v[4:5], s[0:1]
	s_movk_i32 s3, 0x1e00
	v_mad_u64_u32 v[48:49], s[0:1], v2, s3, v[4:5]
	v_mad_i32_i24 v49, v3, s3, v49
	v_readlane_b32 s3, v255, 35
	v_readlane_b32 s37, v251, 33
	v_readlane_b32 s38, v251, 34
	v_readlane_b32 s39, v251, 35
	s_mov_b64 s[20:21], s[44:45]
	s_mov_b64 s[22:23], s[46:47]
	s_mov_b64 s[24:25], s[48:49]
	s_mov_b64 s[26:27], s[50:51]
	global_load_dwordx4 v[72:75], v[42:43], off offset:16
	global_load_dwordx4 v[76:79], v[42:43], off
	global_load_dwordx4 v[80:83], v[42:43], off offset:2064
	global_load_dwordx4 v[84:87], v[42:43], off offset:2048
	global_load_dwordx4 v[88:91], v[44:45], off offset:16
	global_load_dwordx4 v[92:95], v[44:45], off
	v_mov_b32_e32 v228, v48
	v_mov_b32_e32 v229, v49
	v_mov_b32_e32 v230, v52
	s_mov_b32 s12, s3
.Lcv_trip:
	v_lshl_add_u64 v[212:213], v[228:229], 0, v[206:207]
	v_add_co_u32_e32 v214, vcc, 0x1f1b9000, v212
	s_movk_i32 s0, 0x2000
	s_nop 0
	v_addc_co_u32_e32 v215, vcc, 0, v213, vcc
	global_load_dwordx4 v[96:99], v[214:215], off offset:2432
	global_load_dwordx4 v[100:103], v[214:215], off offset:1408
	global_load_dwordx4 v[104:107], v[214:215], off offset:384
	v_add_co_u32_e32 v216, vcc, 0x1f1b7000, v212
	s_nop 1
	v_addc_co_u32_e32 v217, vcc, 0, v213, vcc
	global_load_dwordx4 v[108:111], v[216:217], off offset:1920
	global_load_dwordx4 v[112:115], v[216:217], off offset:2944
	v_add_co_u32_e32 v218, vcc, 0x1f1bb000, v212
	s_nop 1
	v_addc_co_u32_e32 v219, vcc, 0, v213, vcc
	global_load_dwordx4 v[116:119], v[218:219], off offset:896
	global_load_dwordx4 v[120:123], v[218:219], off offset:1920
	v_cmp_gt_i32_e32 vcc, s0, v230
	v_mov_b32_e32 v221, 0xff
	v_mov_b32_e32 v220, 0x7ff
	s_nop 0
	v_cndmask_b32_e32 v221, v221, v220, vcc
	v_and_b32_e32 v220, v221, v230
	s_add_i32 s12, s12, 0xa0
	s_cmp_lt_i32 s12, s2
	s_cselect_b32 s0, 0x960000, 0
	s_cselect_b32 s13, 0x500, 0
	s_mov_b32 s1, 0
	v_lshl_add_u64 v[228:229], v[228:229], 0, s[0:1]
	v_add_u32_e32 v230, s13, v230
	v_lshl_add_u64 v[212:213], v[228:229], 0, v[206:207]
	v_add_co_u32_e32 v214, vcc, 0x1f1b9000, v212
	s_movk_i32 s0, 0x2000
	s_nop 0
	v_addc_co_u32_e32 v215, vcc, 0, v213, vcc
	global_load_dwordx4 v[124:127], v[214:215], off offset:2432
	global_load_dwordx4 v[128:131], v[214:215], off offset:1408
	global_load_dwordx4 v[132:135], v[214:215], off offset:384
	v_add_co_u32_e32 v216, vcc, 0x1f1b7000, v212
	s_nop 1
	v_addc_co_u32_e32 v217, vcc, 0, v213, vcc
	global_load_dwordx4 v[136:139], v[216:217], off offset:1920
	global_load_dwordx4 v[140:143], v[216:217], off offset:2944
	v_add_co_u32_e32 v218, vcc, 0x1f1bb000, v212
	s_nop 1
	v_addc_co_u32_e32 v219, vcc, 0, v213, vcc
	global_load_dwordx4 v[144:147], v[218:219], off offset:896
	global_load_dwordx4 v[148:151], v[218:219], off offset:1920
	v_cmp_gt_i32_e32 vcc, s0, v230
	v_mov_b32_e32 v223, 0xff
	v_mov_b32_e32 v222, 0x7ff
	s_nop 0
	v_cndmask_b32_e32 v223, v223, v222, vcc
	v_and_b32_e32 v222, v223, v230
	s_add_i32 s12, s12, 0xa0
	s_cmp_lt_i32 s12, s2
	s_cselect_b32 s0, 0x960000, 0
	s_cselect_b32 s13, 0x500, 0
	s_mov_b32 s1, 0
	v_lshl_add_u64 v[228:229], v[228:229], 0, s[0:1]
	v_add_u32_e32 v230, s13, v230
	v_lshl_add_u64 v[212:213], v[228:229], 0, v[206:207]
	v_add_co_u32_e32 v214, vcc, 0x1f1b9000, v212
	s_movk_i32 s0, 0x2000
	s_nop 0
	v_addc_co_u32_e32 v215, vcc, 0, v213, vcc
	global_load_dwordx4 v[152:155], v[214:215], off offset:2432
	global_load_dwordx4 v[156:159], v[214:215], off offset:1408
	global_load_dwordx4 v[160:163], v[214:215], off offset:384
	v_add_co_u32_e32 v216, vcc, 0x1f1b7000, v212
	s_nop 1
	v_addc_co_u32_e32 v217, vcc, 0, v213, vcc
	global_load_dwordx4 v[164:167], v[216:217], off offset:1920
	global_load_dwordx4 v[168:171], v[216:217], off offset:2944
	v_add_co_u32_e32 v218, vcc, 0x1f1bb000, v212
	s_nop 1
	v_addc_co_u32_e32 v219, vcc, 0, v213, vcc
	global_load_dwordx4 v[172:175], v[218:219], off offset:896
	global_load_dwordx4 v[176:179], v[218:219], off offset:1920
	v_cmp_gt_i32_e32 vcc, s0, v230
	v_mov_b32_e32 v225, 0xff
	v_mov_b32_e32 v224, 0x7ff
	s_nop 0
	v_cndmask_b32_e32 v225, v225, v224, vcc
	v_and_b32_e32 v224, v225, v230
	s_add_i32 s12, s12, 0xa0
	s_cmp_lt_i32 s12, s2
	s_cselect_b32 s0, 0x960000, 0
	s_cselect_b32 s13, 0x500, 0
	s_mov_b32 s1, 0
	v_lshl_add_u64 v[228:229], v[228:229], 0, s[0:1]
	v_add_u32_e32 v230, s13, v230
	v_lshl_add_u64 v[212:213], v[228:229], 0, v[206:207]
	v_add_co_u32_e32 v214, vcc, 0x1f1b9000, v212
	s_movk_i32 s0, 0x2000
	s_nop 0
	v_addc_co_u32_e32 v215, vcc, 0, v213, vcc
	global_load_dwordx4 v[180:183], v[214:215], off offset:2432
	global_load_dwordx4 v[184:187], v[214:215], off offset:1408
	global_load_dwordx4 v[188:191], v[214:215], off offset:384
	v_add_co_u32_e32 v216, vcc, 0x1f1b7000, v212
	s_nop 1
	v_addc_co_u32_e32 v217, vcc, 0, v213, vcc
	global_load_dwordx4 v[192:195], v[216:217], off offset:1920
	global_load_dwordx4 v[196:199], v[216:217], off offset:2944
	v_add_co_u32_e32 v218, vcc, 0x1f1bb000, v212
	s_nop 1
	v_addc_co_u32_e32 v219, vcc, 0, v213, vcc
	global_load_dwordx4 v[200:203], v[218:219], off offset:896
	global_load_dwordx4 v[208:211], v[218:219], off offset:1920
	v_cmp_gt_i32_e32 vcc, s0, v230
	v_mov_b32_e32 v227, 0xff
	v_mov_b32_e32 v226, 0x7ff
	s_nop 0
	v_cndmask_b32_e32 v227, v227, v226, vcc
	v_and_b32_e32 v226, v227, v230
	s_add_i32 s12, s12, 0xa0
	s_cmp_lt_i32 s12, s2
	s_cselect_b32 s0, 0x960000, 0
	s_cselect_b32 s13, 0x500, 0
	s_mov_b32 s1, 0
	v_lshl_add_u64 v[228:229], v[228:229], 0, s[0:1]
	v_add_u32_e32 v230, s13, v230
	s_waitcnt vmcnt(0)
; __device__ __forceinline__ unsigned cvt_pk_bf16(float lo, float hi) { const f32x2 v = {lo, hi}; const bf16x2_t b = __builtin_convertvector(v, bf16x2_t); return __builtin_bit_cast(unsigned, b); }
; __device__ __forceinline__ float bflo(unsigned w) { return __uint_as_float(w << 16); }
; __device__ __forceinline__ float bfhi(unsigned w) { return __uint_as_float(w & 0xffff0000u); }
;     #define CONV_Z(dst, a_, h_) do { \
;               dst[0] = bflo(a_.x) * bflo(h_.x); dst[1] = bfhi(a_.x) * bfhi(h_.x); dst[2] = bflo(a_.y) * bflo(h_.y); dst[3] = bfhi(a_.y) * bfhi(h_.y); \
;               dst[4] = bflo(a_.z) * bflo(h_.z); dst[5] = bfhi(a_.z) * bfhi(h_.z); dst[6] = bflo(a_.w) * bflo(h_.w); dst[7] = bfhi(a_.w) * bfhi(h_.w); } while (0)
; template <bool MAIN, bool CONV>
; __device__ __forceinline__ void b_row(const Params& p, unsigned char* ws, int l, int row, int lane) {
;     ...
;     if (CONV) {
;         ca = *(const u32x4*)(pr + C_CVC + c0); ch = *(const u32x4*)(pr + C_CVH + c0); bg = *(const u32x4*)(pr + C_CVB + c0);
;         if (t > 0) { pa = *(const u32x4*)(pr - INP + C_CVC + c0); ph = *(const u32x4*)(pr - INP + C_CVH + c0); }
;         if (t < seqlen - 1) { na = *(const u32x4*)(pr + INP + C_CVC + c0); nh = *(const u32x4*)(pr + INP + C_CVH + c0); }
;     ...
;     if (CONV) {
;         { float zp[8], zc[8], zn[8];
;     ...
;           CONV_Z(zc, ca, ch); CONV_Z(zp, pa, ph); CONV_Z(zn, na, nh);
;     ...
;           float bgf[8] = {bflo(bg.x), bfhi(bg.x), bflo(bg.y), bfhi(bg.y), bflo(bg.z), bfhi(bg.z), bflo(bg.w), bfhi(bg.w)};
;           const float w0[8] = {cw0a[0], cw0a[1], cw0a[2], cw0a[3], cw0b[0], cw0b[1], cw0b[2], cw0b[3]}, w1[8] = {cw1a[0], cw1a[1], cw1a[2], cw1a[3], cw1b[0], cw1b[1], cw1b[2], cw1b[3]},
;                       w2[8] = {cw2a[0], cw2a[1], cw2a[2], cw2a[3], cw2b[0], cw2b[1], cw2b[2], cw2b[3]};
;           float o[8];
;     #pragma unroll
;           for (int j = 0; j < 8; ++j) o[j] = bgf[j] * (w0[j] * zp[j] + w1[j] * zc[j] + w2[j] * zn[j]);
;           u32x4 w; w.x = cvt_pk_bf16(o[0], o[1]); w.y = cvt_pk_bf16(o[2], o[3]); w.z = cvt_pk_bf16(o[4], o[5]); w.w = cvt_pk_bf16(o[6], o[7]);
;           *(u32x4*)(CAT + (size_t)row * DM + 1536 + c0) = w; }
	v_cmp_ne_u32_e32 vcc, 0, v220
	v_mov_b32_e32 v22, v96
	v_mov_b32_e32 v23, v97
	v_mov_b32_e32 v24, v98
	v_mov_b32_e32 v25, v99
	v_mov_b32_e32 v30, v100
	v_mov_b32_e32 v31, v101
	v_mov_b32_e32 v32, v102
	v_mov_b32_e32 v33, v103
	v_mov_b32_e32 v2, v104
	v_mov_b32_e32 v3, v105
	v_mov_b32_e32 v4, v106
	v_mov_b32_e32 v5, v107
	v_cndmask_b32_e32 v34, 0, v108, vcc
	v_cndmask_b32_e32 v35, 0, v109, vcc
	v_cndmask_b32_e32 v36, 0, v110, vcc
	v_cndmask_b32_e32 v37, 0, v111, vcc
	v_cndmask_b32_e32 v26, 0, v112, vcc
	v_cndmask_b32_e32 v27, 0, v113, vcc
	v_cndmask_b32_e32 v28, 0, v114, vcc
	v_cndmask_b32_e32 v29, 0, v115, vcc
	v_cmp_ne_u32_e32 vcc, v220, v221
	s_nop 1
	v_cndmask_b32_e32 v38, 0, v116, vcc
	v_cndmask_b32_e32 v39, 0, v117, vcc
	v_cndmask_b32_e32 v40, 0, v118, vcc
	v_cndmask_b32_e32 v41, 0, v119, vcc
	v_cndmask_b32_e32 v18, 0, v120, vcc
	v_cndmask_b32_e32 v19, 0, v121, vcc
	v_cndmask_b32_e32 v20, 0, v122, vcc
	v_cndmask_b32_e32 v21, 0, v123, vcc
	v_lshlrev_b32_e32 v50, 16, v30
	v_and_b32_e32 v51, 0xffff0000, v30
	v_lshlrev_b32_e32 v66, 16, v22
	v_and_b32_e32 v67, 0xffff0000, v22
	v_lshlrev_b32_e32 v30, 16, v31
	v_and_b32_e32 v31, 0xffff0000, v31
	v_lshlrev_b32_e32 v22, 16, v23
	v_and_b32_e32 v23, 0xffff0000, v23
	v_lshlrev_b32_e32 v68, 16, v26
	v_and_b32_e32 v69, 0xffff0000, v26
	v_pk_mul_f32 v[22:23], v[30:31], v[22:23]
	v_lshlrev_b32_e32 v30, 16, v35
	v_and_b32_e32 v31, 0xffff0000, v35
	v_lshlrev_b32_e32 v26, 16, v27
	v_and_b32_e32 v27, 0xffff0000, v27
	v_pk_mul_f32 v[50:51], v[50:51], v[66:67]
	v_lshlrev_b32_e32 v66, 16, v34
	v_and_b32_e32 v67, 0xffff0000, v34
	v_lshlrev_b32_e32 v70, 16, v18
	v_and_b32_e32 v71, 0xffff0000, v18
	v_pk_mul_f32 v[26:27], v[26:27], v[30:31]
	v_lshlrev_b32_e32 v30, 16, v39
	v_and_b32_e32 v31, 0xffff0000, v39
	v_lshlrev_b32_e32 v18, 16, v19
	v_and_b32_e32 v19, 0xffff0000, v19
	v_pk_mul_f32 v[66:67], v[68:69], v[66:67]
	v_lshlrev_b32_e32 v68, 16, v38
	v_and_b32_e32 v69, 0xffff0000, v38
	v_pk_mul_f32 v[18:19], v[18:19], v[30:31]
	v_pk_mul_f32 v[68:69], v[70:71], v[68:69]
	v_lshlrev_b32_e32 v70, 16, v2
	v_and_b32_e32 v71, 0xffff0000, v2
	v_lshlrev_b32_e32 v2, 16, v3
	v_and_b32_e32 v3, 0xffff0000, v3
	v_lshlrev_b32_e32 v30, 16, v20
	v_and_b32_e32 v31, 0xffff0000, v20
	v_lshlrev_b32_e32 v20, 16, v21
	v_and_b32_e32 v21, 0xffff0000, v21
	s_addk_i32 s3, 0xa0
	s_cmp_lt_i32 s3, s2
	s_cselect_b32 s0, 0x500000, 0
	s_mov_b32 s1, 0
	v_pk_mul_f32 v[22:23], v[22:23], v[86:87]
	s_nop 0
	v_pk_fma_f32 v[22:23], v[26:27], v[78:79], v[22:23]
	v_lshlrev_b32_e32 v26, 16, v28
	v_pk_fma_f32 v[18:19], v[18:19], v[94:95], v[22:23]
	v_lshlrev_b32_e32 v22, 16, v24
	v_pk_mul_f32 v[18:19], v[18:19], v[2:3]
	v_lshlrev_b32_e32 v2, 16, v32
	v_and_b32_e32 v3, 0xffff0000, v32
	v_and_b32_e32 v23, 0xffff0000, v24
	v_pk_mul_f32 v[2:3], v[2:3], v[22:23]
	v_lshlrev_b32_e32 v22, 16, v36
	v_and_b32_e32 v23, 0xffff0000, v36
	v_and_b32_e32 v27, 0xffff0000, v28
	v_pk_mul_f32 v[22:23], v[26:27], v[22:23]
	v_lshlrev_b32_e32 v26, 16, v40
	v_and_b32_e32 v27, 0xffff0000, v40
	v_pk_mul_f32 v[2:3], v[2:3], v[80:81]
	v_pk_mul_f32 v[26:27], v[30:31], v[26:27]
	v_pk_fma_f32 v[2:3], v[22:23], v[72:73], v[2:3]
	v_lshlrev_b32_e32 v30, 16, v4
	v_and_b32_e32 v31, 0xffff0000, v4
	v_pk_fma_f32 v[2:3], v[26:27], v[88:89], v[2:3]
	v_lshlrev_b32_e32 v10, 16, v25
	v_pk_mul_f32 v[6:7], v[2:3], v[30:31]
	v_lshlrev_b32_e32 v2, 16, v33
	v_and_b32_e32 v3, 0xffff0000, v33
	v_and_b32_e32 v11, 0xffff0000, v25
	v_pk_mul_f32 v[2:3], v[2:3], v[10:11]
	v_lshlrev_b32_e32 v10, 16, v37
	v_and_b32_e32 v11, 0xffff0000, v37
	v_lshlrev_b32_e32 v14, 16, v29
	v_and_b32_e32 v15, 0xffff0000, v29
	v_pk_mul_f32 v[50:51], v[50:51], v[84:85]
	v_pk_mul_f32 v[10:11], v[14:15], v[10:11]
	v_lshlrev_b32_e32 v14, 16, v41
	v_and_b32_e32 v15, 0xffff0000, v41
	v_pk_mul_f32 v[2:3], v[2:3], v[82:83]
	v_pk_fma_f32 v[50:51], v[66:67], v[76:77], v[50:51]
	v_pk_mul_f32 v[14:15], v[20:21], v[14:15]
	v_pk_fma_f32 v[2:3], v[10:11], v[74:75], v[2:3]
	v_pk_fma_f32 v[50:51], v[68:69], v[92:93], v[50:51]
	v_lshlrev_b32_e32 v4, 16, v5
	v_and_b32_e32 v5, 0xffff0000, v5
	v_pk_fma_f32 v[2:3], v[14:15], v[90:91], v[2:3]
	v_pk_mul_f32 v[50:51], v[50:51], v[70:71]
	v_pk_mul_f32 v[8:9], v[2:3], v[4:5]
	v_cvt_pk_bf16_f32 v4, v6, v7
	v_lshl_add_u64 v[6:7], v[46:47], 0, v[206:207]
	v_lshl_add_u64 v[46:47], v[46:47], 0, s[0:1]
	v_cvt_pk_bf16_f32 v2, v50, v51
	v_cvt_pk_bf16_f32 v3, v18, v19
	v_cvt_pk_bf16_f32 v5, v8, v9
	global_store_dwordx4 v[6:7], v[2:5], off
	s_nop 1
	v_cmp_ne_u32_e32 vcc, 0, v222
	v_mov_b32_e32 v22, v124
	v_mov_b32_e32 v23, v125
	v_mov_b32_e32 v24, v126
	v_mov_b32_e32 v25, v127
	v_mov_b32_e32 v30, v128
	v_mov_b32_e32 v31, v129
	v_mov_b32_e32 v32, v130
	v_mov_b32_e32 v33, v131
	v_mov_b32_e32 v2, v132
	v_mov_b32_e32 v3, v133
	v_mov_b32_e32 v4, v134
	v_mov_b32_e32 v5, v135
	v_cndmask_b32_e32 v34, 0, v136, vcc
	v_cndmask_b32_e32 v35, 0, v137, vcc
	v_cndmask_b32_e32 v36, 0, v138, vcc
	v_cndmask_b32_e32 v37, 0, v139, vcc
	v_cndmask_b32_e32 v26, 0, v140, vcc
	v_cndmask_b32_e32 v27, 0, v141, vcc
	v_cndmask_b32_e32 v28, 0, v142, vcc
	v_cndmask_b32_e32 v29, 0, v143, vcc
	v_cmp_ne_u32_e32 vcc, v222, v223
	s_nop 1
	v_cndmask_b32_e32 v38, 0, v144, vcc
	v_cndmask_b32_e32 v39, 0, v145, vcc
	v_cndmask_b32_e32 v40, 0, v146, vcc
	v_cndmask_b32_e32 v41, 0, v147, vcc
	v_cndmask_b32_e32 v18, 0, v148, vcc
	v_cndmask_b32_e32 v19, 0, v149, vcc
	v_cndmask_b32_e32 v20, 0, v150, vcc
	v_cndmask_b32_e32 v21, 0, v151, vcc
	v_lshlrev_b32_e32 v50, 16, v30
	v_and_b32_e32 v51, 0xffff0000, v30
	v_lshlrev_b32_e32 v66, 16, v22
	v_and_b32_e32 v67, 0xffff0000, v22
	v_lshlrev_b32_e32 v30, 16, v31
	v_and_b32_e32 v31, 0xffff0000, v31
	v_lshlrev_b32_e32 v22, 16, v23
; __device__ __forceinline__ unsigned cvt_pk_bf16(float lo, float hi) { const f32x2 v = {lo, hi}; const bf16x2_t b = __builtin_convertvector(v, bf16x2_t); return __builtin_bit_cast(unsigned, b); }
; __device__ __forceinline__ float bflo(unsigned w) { return __uint_as_float(w << 16); }
; __device__ __forceinline__ float bfhi(unsigned w) { return __uint_as_float(w & 0xffff0000u); }
;     #define CONV_Z(dst, a_, h_) do { \
;               dst[0] = bflo(a_.x) * bflo(h_.x); dst[1] = bfhi(a_.x) * bfhi(h_.x); dst[2] = bflo(a_.y) * bflo(h_.y); dst[3] = bfhi(a_.y) * bfhi(h_.y); \
;               dst[4] = bflo(a_.z) * bflo(h_.z); dst[5] = bfhi(a_.z) * bfhi(h_.z); dst[6] = bflo(a_.w) * bflo(h_.w); dst[7] = bfhi(a_.w) * bfhi(h_.w); } while (0)
; template <bool MAIN, bool CONV>
; __device__ __forceinline__ void b_row(const Params& p, unsigned char* ws, int l, int row, int lane) {
;     ...
;     if (CONV) {
;         { float zp[8], zc[8], zn[8];
;     ...
;           CONV_Z(zc, ca, ch); CONV_Z(zp, pa, ph); CONV_Z(zn, na, nh);
;     ...
;           float bgf[8] = {bflo(bg.x), bfhi(bg.x), bflo(bg.y), bfhi(bg.y), bflo(bg.z), bfhi(bg.z), bflo(bg.w), bfhi(bg.w)};
;           const float w0[8] = {cw0a[0], cw0a[1], cw0a[2], cw0a[3], cw0b[0], cw0b[1], cw0b[2], cw0b[3]}, w1[8] = {cw1a[0], cw1a[1], cw1a[2], cw1a[3], cw1b[0], cw1b[1], cw1b[2], cw1b[3]},
;                       w2[8] = {cw2a[0], cw2a[1], cw2a[2], cw2a[3], cw2b[0], cw2b[1], cw2b[2], cw2b[3]};
;           float o[8];
;     #pragma unroll
;           for (int j = 0; j < 8; ++j) o[j] = bgf[j] * (w0[j] * zp[j] + w1[j] * zc[j] + w2[j] * zn[j]);
;           u32x4 w; w.x = cvt_pk_bf16(o[0], o[1]); w.y = cvt_pk_bf16(o[2], o[3]); w.z = cvt_pk_bf16(o[4], o[5]); w.w = cvt_pk_bf16(o[6], o[7]);
;           *(u32x4*)(CAT + (size_t)row * DM + 1536 + c0) = w; }
	v_and_b32_e32 v23, 0xffff0000, v23
	v_lshlrev_b32_e32 v68, 16, v26
	v_and_b32_e32 v69, 0xffff0000, v26
	v_pk_mul_f32 v[22:23], v[30:31], v[22:23]
	v_lshlrev_b32_e32 v30, 16, v35
	v_and_b32_e32 v31, 0xffff0000, v35
	v_lshlrev_b32_e32 v26, 16, v27
	v_and_b32_e32 v27, 0xffff0000, v27
	v_pk_mul_f32 v[50:51], v[50:51], v[66:67]
	v_lshlrev_b32_e32 v66, 16, v34
	v_and_b32_e32 v67, 0xffff0000, v34
	v_lshlrev_b32_e32 v70, 16, v18
	v_and_b32_e32 v71, 0xffff0000, v18
	v_pk_mul_f32 v[26:27], v[26:27], v[30:31]
	v_lshlrev_b32_e32 v30, 16, v39
	v_and_b32_e32 v31, 0xffff0000, v39
	v_lshlrev_b32_e32 v18, 16, v19
	v_and_b32_e32 v19, 0xffff0000, v19
	v_pk_mul_f32 v[66:67], v[68:69], v[66:67]
	v_lshlrev_b32_e32 v68, 16, v38
	v_and_b32_e32 v69, 0xffff0000, v38
	v_pk_mul_f32 v[18:19], v[18:19], v[30:31]
	v_pk_mul_f32 v[68:69], v[70:71], v[68:69]
	v_lshlrev_b32_e32 v70, 16, v2
	v_and_b32_e32 v71, 0xffff0000, v2
	v_lshlrev_b32_e32 v2, 16, v3
	v_and_b32_e32 v3, 0xffff0000, v3
	v_lshlrev_b32_e32 v30, 16, v20
	v_and_b32_e32 v31, 0xffff0000, v20
	v_lshlrev_b32_e32 v20, 16, v21
	v_and_b32_e32 v21, 0xffff0000, v21
	s_addk_i32 s3, 0xa0
	s_cmp_lt_i32 s3, s2
	s_cselect_b32 s0, 0x500000, 0
	s_mov_b32 s1, 0
	v_pk_mul_f32 v[22:23], v[22:23], v[86:87]
	s_nop 0
	v_pk_fma_f32 v[22:23], v[26:27], v[78:79], v[22:23]
	v_lshlrev_b32_e32 v26, 16, v28
	v_pk_fma_f32 v[18:19], v[18:19], v[94:95], v[22:23]
	v_lshlrev_b32_e32 v22, 16, v24
	v_pk_mul_f32 v[18:19], v[18:19], v[2:3]
	v_lshlrev_b32_e32 v2, 16, v32
	v_and_b32_e32 v3, 0xffff0000, v32
	v_and_b32_e32 v23, 0xffff0000, v24
	v_pk_mul_f32 v[2:3], v[2:3], v[22:23]
	v_lshlrev_b32_e32 v22, 16, v36
	v_and_b32_e32 v23, 0xffff0000, v36
	v_and_b32_e32 v27, 0xffff0000, v28
	v_pk_mul_f32 v[22:23], v[26:27], v[22:23]
	v_lshlrev_b32_e32 v26, 16, v40
	v_and_b32_e32 v27, 0xffff0000, v40
	v_pk_mul_f32 v[2:3], v[2:3], v[80:81]
	v_pk_mul_f32 v[26:27], v[30:31], v[26:27]
	v_pk_fma_f32 v[2:3], v[22:23], v[72:73], v[2:3]
	v_lshlrev_b32_e32 v30, 16, v4
	v_and_b32_e32 v31, 0xffff0000, v4
	v_pk_fma_f32 v[2:3], v[26:27], v[88:89], v[2:3]
	v_lshlrev_b32_e32 v10, 16, v25
	v_pk_mul_f32 v[6:7], v[2:3], v[30:31]
	v_lshlrev_b32_e32 v2, 16, v33
	v_and_b32_e32 v3, 0xffff0000, v33
	v_and_b32_e32 v11, 0xffff0000, v25
	v_pk_mul_f32 v[2:3], v[2:3], v[10:11]
	v_lshlrev_b32_e32 v10, 16, v37
	v_and_b32_e32 v11, 0xffff0000, v37
	v_lshlrev_b32_e32 v14, 16, v29
	v_and_b32_e32 v15, 0xffff0000, v29
	v_pk_mul_f32 v[50:51], v[50:51], v[84:85]
	v_pk_mul_f32 v[10:11], v[14:15], v[10:11]
	v_lshlrev_b32_e32 v14, 16, v41
	v_and_b32_e32 v15, 0xffff0000, v41
	v_pk_mul_f32 v[2:3], v[2:3], v[82:83]
	v_pk_fma_f32 v[50:51], v[66:67], v[76:77], v[50:51]
	v_pk_mul_f32 v[14:15], v[20:21], v[14:15]
	v_pk_fma_f32 v[2:3], v[10:11], v[74:75], v[2:3]
	v_pk_fma_f32 v[50:51], v[68:69], v[92:93], v[50:51]
	v_lshlrev_b32_e32 v4, 16, v5
	v_and_b32_e32 v5, 0xffff0000, v5
	v_pk_fma_f32 v[2:3], v[14:15], v[90:91], v[2:3]
	v_pk_mul_f32 v[50:51], v[50:51], v[70:71]
	v_pk_mul_f32 v[8:9], v[2:3], v[4:5]
	v_cvt_pk_bf16_f32 v4, v6, v7
	v_lshl_add_u64 v[6:7], v[46:47], 0, v[206:207]
	v_lshl_add_u64 v[46:47], v[46:47], 0, s[0:1]
	v_cvt_pk_bf16_f32 v2, v50, v51
	v_cvt_pk_bf16_f32 v3, v18, v19
	v_cvt_pk_bf16_f32 v5, v8, v9
	global_store_dwordx4 v[6:7], v[2:5], off
	s_nop 1
	v_cmp_ne_u32_e32 vcc, 0, v224
	v_mov_b32_e32 v22, v152
	v_mov_b32_e32 v23, v153
	v_mov_b32_e32 v24, v154
	v_mov_b32_e32 v25, v155
	v_mov_b32_e32 v30, v156
	v_mov_b32_e32 v31, v157
	v_mov_b32_e32 v32, v158
	v_mov_b32_e32 v33, v159
	v_mov_b32_e32 v2, v160
	v_mov_b32_e32 v3, v161
	v_mov_b32_e32 v4, v162
	v_mov_b32_e32 v5, v163
	v_cndmask_b32_e32 v34, 0, v164, vcc
	v_cndmask_b32_e32 v35, 0, v165, vcc
	v_cndmask_b32_e32 v36, 0, v166, vcc
	v_cndmask_b32_e32 v37, 0, v167, vcc
	v_cndmask_b32_e32 v26, 0, v168, vcc
	v_cndmask_b32_e32 v27, 0, v169, vcc
	v_cndmask_b32_e32 v28, 0, v170, vcc
	v_cndmask_b32_e32 v29, 0, v171, vcc
	v_cmp_ne_u32_e32 vcc, v224, v225
	s_nop 1
	v_cndmask_b32_e32 v38, 0, v172, vcc
	v_cndmask_b32_e32 v39, 0, v173, vcc
	v_cndmask_b32_e32 v40, 0, v174, vcc
	v_cndmask_b32_e32 v41, 0, v175, vcc
	v_cndmask_b32_e32 v18, 0, v176, vcc
	v_cndmask_b32_e32 v19, 0, v177, vcc
	v_cndmask_b32_e32 v20, 0, v178, vcc
	v_cndmask_b32_e32 v21, 0, v179, vcc
	v_lshlrev_b32_e32 v50, 16, v30
	v_and_b32_e32 v51, 0xffff0000, v30
	v_lshlrev_b32_e32 v66, 16, v22
	v_and_b32_e32 v67, 0xffff0000, v22
	v_lshlrev_b32_e32 v30, 16, v31
	v_and_b32_e32 v31, 0xffff0000, v31
	v_lshlrev_b32_e32 v22, 16, v23
	v_and_b32_e32 v23, 0xffff0000, v23
	v_lshlrev_b32_e32 v68, 16, v26
	v_and_b32_e32 v69, 0xffff0000, v26
	v_pk_mul_f32 v[22:23], v[30:31], v[22:23]
	v_lshlrev_b32_e32 v30, 16, v35
	v_and_b32_e32 v31, 0xffff0000, v35
	v_lshlrev_b32_e32 v26, 16, v27
	v_and_b32_e32 v27, 0xffff0000, v27
	v_pk_mul_f32 v[50:51], v[50:51], v[66:67]
	v_lshlrev_b32_e32 v66, 16, v34
	v_and_b32_e32 v67, 0xffff0000, v34
	v_lshlrev_b32_e32 v70, 16, v18
	v_and_b32_e32 v71, 0xffff0000, v18
	v_pk_mul_f32 v[26:27], v[26:27], v[30:31]
	v_lshlrev_b32_e32 v30, 16, v39
	v_and_b32_e32 v31, 0xffff0000, v39
	v_lshlrev_b32_e32 v18, 16, v19
	v_and_b32_e32 v19, 0xffff0000, v19
	v_pk_mul_f32 v[66:67], v[68:69], v[66:67]
	v_lshlrev_b32_e32 v68, 16, v38
	v_and_b32_e32 v69, 0xffff0000, v38
	v_pk_mul_f32 v[18:19], v[18:19], v[30:31]
	v_pk_mul_f32 v[68:69], v[70:71], v[68:69]
	v_lshlrev_b32_e32 v70, 16, v2
	v_and_b32_e32 v71, 0xffff0000, v2
	v_lshlrev_b32_e32 v2, 16, v3
	v_and_b32_e32 v3, 0xffff0000, v3
	v_lshlrev_b32_e32 v30, 16, v20
	v_and_b32_e32 v31, 0xffff0000, v20
	v_lshlrev_b32_e32 v20, 16, v21
	v_and_b32_e32 v21, 0xffff0000, v21
	s_addk_i32 s3, 0xa0
	s_cmp_lt_i32 s3, s2
	s_cselect_b32 s0, 0x500000, 0
; __device__ __forceinline__ unsigned cvt_pk_bf16(float lo, float hi) { const f32x2 v = {lo, hi}; const bf16x2_t b = __builtin_convertvector(v, bf16x2_t); return __builtin_bit_cast(unsigned, b); }
; __device__ __forceinline__ float bflo(unsigned w) { return __uint_as_float(w << 16); }
; __device__ __forceinline__ float bfhi(unsigned w) { return __uint_as_float(w & 0xffff0000u); }
;     #define CONV_Z(dst, a_, h_) do { \
;               dst[0] = bflo(a_.x) * bflo(h_.x); dst[1] = bfhi(a_.x) * bfhi(h_.x); dst[2] = bflo(a_.y) * bflo(h_.y); dst[3] = bfhi(a_.y) * bfhi(h_.y); \
;               dst[4] = bflo(a_.z) * bflo(h_.z); dst[5] = bfhi(a_.z) * bfhi(h_.z); dst[6] = bflo(a_.w) * bflo(h_.w); dst[7] = bfhi(a_.w) * bfhi(h_.w); } while (0)
; template <bool MAIN, bool CONV>
; __device__ __forceinline__ void b_row(const Params& p, unsigned char* ws, int l, int row, int lane) {
;     ...
;     if (CONV) {
;         { float zp[8], zc[8], zn[8];
;     ...
;           CONV_Z(zc, ca, ch); CONV_Z(zp, pa, ph); CONV_Z(zn, na, nh);
;     ...
;           float bgf[8] = {bflo(bg.x), bfhi(bg.x), bflo(bg.y), bfhi(bg.y), bflo(bg.z), bfhi(bg.z), bflo(bg.w), bfhi(bg.w)};
;           const float w0[8] = {cw0a[0], cw0a[1], cw0a[2], cw0a[3], cw0b[0], cw0b[1], cw0b[2], cw0b[3]}, w1[8] = {cw1a[0], cw1a[1], cw1a[2], cw1a[3], cw1b[0], cw1b[1], cw1b[2], cw1b[3]},
;                       w2[8] = {cw2a[0], cw2a[1], cw2a[2], cw2a[3], cw2b[0], cw2b[1], cw2b[2], cw2b[3]};
;           float o[8];
;     #pragma unroll
;           for (int j = 0; j < 8; ++j) o[j] = bgf[j] * (w0[j] * zp[j] + w1[j] * zc[j] + w2[j] * zn[j]);
;           u32x4 w; w.x = cvt_pk_bf16(o[0], o[1]); w.y = cvt_pk_bf16(o[2], o[3]); w.z = cvt_pk_bf16(o[4], o[5]); w.w = cvt_pk_bf16(o[6], o[7]);
;           *(u32x4*)(CAT + (size_t)row * DM + 1536 + c0) = w; }
; __global__ void __launch_bounds__(512, 2) fwd(Params p) {
;     ...
;                     for (int it = j; it < nit; it += 160) b_row<false, true>(p, wsq, l, it * 8 + (t_ >> 6), t_ & 63); } }
	s_mov_b32 s1, 0
	v_pk_mul_f32 v[22:23], v[22:23], v[86:87]
	s_nop 0
	v_pk_fma_f32 v[22:23], v[26:27], v[78:79], v[22:23]
	v_lshlrev_b32_e32 v26, 16, v28
	v_pk_fma_f32 v[18:19], v[18:19], v[94:95], v[22:23]
	v_lshlrev_b32_e32 v22, 16, v24
	v_pk_mul_f32 v[18:19], v[18:19], v[2:3]
	v_lshlrev_b32_e32 v2, 16, v32
	v_and_b32_e32 v3, 0xffff0000, v32
	v_and_b32_e32 v23, 0xffff0000, v24
	v_pk_mul_f32 v[2:3], v[2:3], v[22:23]
	v_lshlrev_b32_e32 v22, 16, v36
	v_and_b32_e32 v23, 0xffff0000, v36
	v_and_b32_e32 v27, 0xffff0000, v28
	v_pk_mul_f32 v[22:23], v[26:27], v[22:23]
	v_lshlrev_b32_e32 v26, 16, v40
	v_and_b32_e32 v27, 0xffff0000, v40
	v_pk_mul_f32 v[2:3], v[2:3], v[80:81]
	v_pk_mul_f32 v[26:27], v[30:31], v[26:27]
	v_pk_fma_f32 v[2:3], v[22:23], v[72:73], v[2:3]
	v_lshlrev_b32_e32 v30, 16, v4
	v_and_b32_e32 v31, 0xffff0000, v4
	v_pk_fma_f32 v[2:3], v[26:27], v[88:89], v[2:3]
	v_lshlrev_b32_e32 v10, 16, v25
	v_pk_mul_f32 v[6:7], v[2:3], v[30:31]
	v_lshlrev_b32_e32 v2, 16, v33
	v_and_b32_e32 v3, 0xffff0000, v33
	v_and_b32_e32 v11, 0xffff0000, v25
	v_pk_mul_f32 v[2:3], v[2:3], v[10:11]
	v_lshlrev_b32_e32 v10, 16, v37
	v_and_b32_e32 v11, 0xffff0000, v37
	v_lshlrev_b32_e32 v14, 16, v29
	v_and_b32_e32 v15, 0xffff0000, v29
	v_pk_mul_f32 v[50:51], v[50:51], v[84:85]
	v_pk_mul_f32 v[10:11], v[14:15], v[10:11]
	v_lshlrev_b32_e32 v14, 16, v41
	v_and_b32_e32 v15, 0xffff0000, v41
	v_pk_mul_f32 v[2:3], v[2:3], v[82:83]
	v_pk_fma_f32 v[50:51], v[66:67], v[76:77], v[50:51]
	v_pk_mul_f32 v[14:15], v[20:21], v[14:15]
	v_pk_fma_f32 v[2:3], v[10:11], v[74:75], v[2:3]
	v_pk_fma_f32 v[50:51], v[68:69], v[92:93], v[50:51]
	v_lshlrev_b32_e32 v4, 16, v5
	v_and_b32_e32 v5, 0xffff0000, v5
	v_pk_fma_f32 v[2:3], v[14:15], v[90:91], v[2:3]
	v_pk_mul_f32 v[50:51], v[50:51], v[70:71]
	v_pk_mul_f32 v[8:9], v[2:3], v[4:5]
	v_cvt_pk_bf16_f32 v4, v6, v7
	v_lshl_add_u64 v[6:7], v[46:47], 0, v[206:207]
	v_lshl_add_u64 v[46:47], v[46:47], 0, s[0:1]
	v_cvt_pk_bf16_f32 v2, v50, v51
	v_cvt_pk_bf16_f32 v3, v18, v19
	v_cvt_pk_bf16_f32 v5, v8, v9
	global_store_dwordx4 v[6:7], v[2:5], off
	s_nop 1
	v_cmp_ne_u32_e32 vcc, 0, v226
	v_mov_b32_e32 v22, v180
	v_mov_b32_e32 v23, v181
	v_mov_b32_e32 v24, v182
	v_mov_b32_e32 v25, v183
	v_mov_b32_e32 v30, v184
	v_mov_b32_e32 v31, v185
	v_mov_b32_e32 v32, v186
	v_mov_b32_e32 v33, v187
	v_mov_b32_e32 v2, v188
	v_mov_b32_e32 v3, v189
	v_mov_b32_e32 v4, v190
	v_mov_b32_e32 v5, v191
	v_cndmask_b32_e32 v34, 0, v192, vcc
	v_cndmask_b32_e32 v35, 0, v193, vcc
	v_cndmask_b32_e32 v36, 0, v194, vcc
	v_cndmask_b32_e32 v37, 0, v195, vcc
	v_cndmask_b32_e32 v26, 0, v196, vcc
	v_cndmask_b32_e32 v27, 0, v197, vcc
	v_cndmask_b32_e32 v28, 0, v198, vcc
	v_cndmask_b32_e32 v29, 0, v199, vcc
	v_cmp_ne_u32_e32 vcc, v226, v227
	s_nop 1
	v_cndmask_b32_e32 v38, 0, v200, vcc
	v_cndmask_b32_e32 v39, 0, v201, vcc
	v_cndmask_b32_e32 v40, 0, v202, vcc
	v_cndmask_b32_e32 v41, 0, v203, vcc
	v_cndmask_b32_e32 v18, 0, v208, vcc
	v_cndmask_b32_e32 v19, 0, v209, vcc
	v_cndmask_b32_e32 v20, 0, v210, vcc
	v_cndmask_b32_e32 v21, 0, v211, vcc
	v_lshlrev_b32_e32 v50, 16, v30
	v_and_b32_e32 v51, 0xffff0000, v30
	v_lshlrev_b32_e32 v66, 16, v22
	v_and_b32_e32 v67, 0xffff0000, v22
	v_lshlrev_b32_e32 v30, 16, v31
	v_and_b32_e32 v31, 0xffff0000, v31
	v_lshlrev_b32_e32 v22, 16, v23
	v_and_b32_e32 v23, 0xffff0000, v23
	v_lshlrev_b32_e32 v68, 16, v26
	v_and_b32_e32 v69, 0xffff0000, v26
	v_pk_mul_f32 v[22:23], v[30:31], v[22:23]
	v_lshlrev_b32_e32 v30, 16, v35
	v_and_b32_e32 v31, 0xffff0000, v35
	v_lshlrev_b32_e32 v26, 16, v27
	v_and_b32_e32 v27, 0xffff0000, v27
	v_pk_mul_f32 v[50:51], v[50:51], v[66:67]
	v_lshlrev_b32_e32 v66, 16, v34
	v_and_b32_e32 v67, 0xffff0000, v34
	v_lshlrev_b32_e32 v70, 16, v18
	v_and_b32_e32 v71, 0xffff0000, v18
	v_pk_mul_f32 v[26:27], v[26:27], v[30:31]
	v_lshlrev_b32_e32 v30, 16, v39
	v_and_b32_e32 v31, 0xffff0000, v39
	v_lshlrev_b32_e32 v18, 16, v19
	v_and_b32_e32 v19, 0xffff0000, v19
	v_pk_mul_f32 v[66:67], v[68:69], v[66:67]
	v_lshlrev_b32_e32 v68, 16, v38
	v_and_b32_e32 v69, 0xffff0000, v38
	v_pk_mul_f32 v[18:19], v[18:19], v[30:31]
	v_pk_mul_f32 v[68:69], v[70:71], v[68:69]
	v_lshlrev_b32_e32 v70, 16, v2
	v_and_b32_e32 v71, 0xffff0000, v2
	v_lshlrev_b32_e32 v2, 16, v3
	v_and_b32_e32 v3, 0xffff0000, v3
	v_lshlrev_b32_e32 v30, 16, v20
	v_and_b32_e32 v31, 0xffff0000, v20
	v_lshlrev_b32_e32 v20, 16, v21
	v_and_b32_e32 v21, 0xffff0000, v21
	s_addk_i32 s3, 0xa0
	s_cmp_lt_i32 s3, s2
	s_cselect_b32 s0, 0x500000, 0
	s_mov_b32 s1, 0
	v_pk_mul_f32 v[22:23], v[22:23], v[86:87]
	s_nop 0
	v_pk_fma_f32 v[22:23], v[26:27], v[78:79], v[22:23]
	v_lshlrev_b32_e32 v26, 16, v28
	v_pk_fma_f32 v[18:19], v[18:19], v[94:95], v[22:23]
	v_lshlrev_b32_e32 v22, 16, v24
	v_pk_mul_f32 v[18:19], v[18:19], v[2:3]
	v_lshlrev_b32_e32 v2, 16, v32
	v_and_b32_e32 v3, 0xffff0000, v32
	v_and_b32_e32 v23, 0xffff0000, v24
	v_pk_mul_f32 v[2:3], v[2:3], v[22:23]
	v_lshlrev_b32_e32 v22, 16, v36
	v_and_b32_e32 v23, 0xffff0000, v36
	v_and_b32_e32 v27, 0xffff0000, v28
	v_pk_mul_f32 v[22:23], v[26:27], v[22:23]
	v_lshlrev_b32_e32 v26, 16, v40
	v_and_b32_e32 v27, 0xffff0000, v40
	v_pk_mul_f32 v[2:3], v[2:3], v[80:81]
	v_pk_mul_f32 v[26:27], v[30:31], v[26:27]
	v_pk_fma_f32 v[2:3], v[22:23], v[72:73], v[2:3]
	v_lshlrev_b32_e32 v30, 16, v4
	v_and_b32_e32 v31, 0xffff0000, v4
	v_pk_fma_f32 v[2:3], v[26:27], v[88:89], v[2:3]
	v_lshlrev_b32_e32 v10, 16, v25
	v_pk_mul_f32 v[6:7], v[2:3], v[30:31]
	v_lshlrev_b32_e32 v2, 16, v33
	v_and_b32_e32 v3, 0xffff0000, v33
	v_and_b32_e32 v11, 0xffff0000, v25
	v_pk_mul_f32 v[2:3], v[2:3], v[10:11]
	v_lshlrev_b32_e32 v10, 16, v37
	v_and_b32_e32 v11, 0xffff0000, v37
	v_lshlrev_b32_e32 v14, 16, v29
	v_and_b32_e32 v15, 0xffff0000, v29
	v_pk_mul_f32 v[50:51], v[50:51], v[84:85]
	v_pk_mul_f32 v[10:11], v[14:15], v[10:11]
	v_lshlrev_b32_e32 v14, 16, v41
	v_and_b32_e32 v15, 0xffff0000, v41
	v_pk_mul_f32 v[2:3], v[2:3], v[82:83]
	v_pk_fma_f32 v[50:51], v[66:67], v[76:77], v[50:51]
	v_pk_mul_f32 v[14:15], v[20:21], v[14:15]
	v_pk_fma_f32 v[2:3], v[10:11], v[74:75], v[2:3]
	v_pk_fma_f32 v[50:51], v[68:69], v[92:93], v[50:51]
	v_lshlrev_b32_e32 v4, 16, v5
	v_and_b32_e32 v5, 0xffff0000, v5
	v_pk_fma_f32 v[2:3], v[14:15], v[90:91], v[2:3]
	v_pk_mul_f32 v[50:51], v[50:51], v[70:71]
	v_pk_mul_f32 v[8:9], v[2:3], v[4:5]
	v_cvt_pk_bf16_f32 v4, v6, v7
	v_lshl_add_u64 v[6:7], v[46:47], 0, v[206:207]
	v_lshl_add_u64 v[46:47], v[46:47], 0, s[0:1]
	v_cvt_pk_bf16_f32 v2, v50, v51
	v_cvt_pk_bf16_f32 v3, v18, v19
	v_cvt_pk_bf16_f32 v5, v8, v9
	global_store_dwordx4 v[6:7], v[2:5], off
	s_nop 1
	s_cmp_lt_i32 s3, s2
	s_cbranch_scc1 .Lcv_trip

.LBB0_1235:
	s_add_i32 s15, s14, 1
	s_cmp_lg_u32 s14, 2
	s_cselect_b32 s14, s15, 0
	s_mul_i32 s15, s14, 0x6400
	v_add_u32_e32 v70, s15, v185
	ds_read_b128 v[66:69], v70
	ds_read_b128 v[166:169], v70 offset:32
	ds_read_b128 v[170:173], v70 offset:64
	ds_read_b128 v[188:191], v70 offset:96
	ds_read_b128 v[192:195], v70 offset:128
	ds_read_b128 v[196:199], v70 offset:160
	ds_read_b128 v[200:203], v70 offset:192
	ds_read_b128 v[216:219], v70 offset:224
	ds_read_b128 v[220:223], v70 offset:256
	ds_read_b128 v[224:227], v70 offset:288
	ds_read_b128 v[228:231], v70 offset:320
	ds_read_b128 v[146:149], v70 offset:352
	s_waitcnt lgkmcnt(11)
	v_mfma_f32_32x32x16_bf16 v[66:81], v[66:69], v[142:145], 0
	v_sub_f32_e32 v82, v82, v183
	v_exp_f32_e32 v82, v82
	v_sub_f32_e32 v94, v94, v183
	v_exp_f32_e32 v94, v94
	v_add_f32_e32 v165, 0, v82
	v_add_f32_e32 v165, v94, v165
	s_waitcnt lgkmcnt(10)
	v_mfma_f32_32x32x16_bf16 v[66:81], v[166:169], v[138:141], v[66:81]
	v_sub_f32_e32 v83, v83, v183
	v_exp_f32_e32 v83, v83
	v_sub_f32_e32 v95, v95, v183
	v_exp_f32_e32 v95, v95
	v_add_f32_e32 v165, v83, v165
	v_cvt_pk_bf16_f32 v82, v82, v83
	v_add_f32_e32 v165, v95, v165
	v_sub_f32_e32 v83, v84, v183
	s_waitcnt lgkmcnt(9)
	v_mfma_f32_32x32x16_bf16 v[66:81], v[170:173], v[134:137], v[66:81]
	v_exp_f32_e32 v83, v83
	v_sub_f32_e32 v96, v96, v183
	v_add_f32_e32 v84, v83, v165
	v_exp_f32_e32 v165, v96
	s_nop 0
	v_add_f32_e32 v84, v165, v84
	s_waitcnt lgkmcnt(8)
	v_mfma_f32_32x32x16_bf16 v[66:81], v[188:191], v[130:133], v[66:81]
	v_sub_f32_e32 v85, v85, v183
	v_exp_f32_e32 v85, v85
	v_sub_f32_e32 v96, v97, v183
	v_exp_f32_e32 v97, v96
	v_cvt_pk_bf16_f32 v96, v94, v95
	v_add_f32_e32 v84, v85, v84
	v_cvt_pk_bf16_f32 v83, v83, v85
	v_add_f32_e32 v84, v97, v84
	v_cvt_pk_bf16_f32 v97, v165, v97
	s_waitcnt lgkmcnt(7)
	v_mfma_f32_32x32x16_bf16 v[66:81], v[192:195], v[126:129], v[66:81]
	v_sub_f32_e32 v85, v86, v183
	v_exp_f32_e32 v85, v85
	s_nop 0
	v_add_f32_e32 v84, v85, v84
	s_waitcnt lgkmcnt(6)
	v_mfma_f32_32x32x16_bf16 v[66:81], v[196:199], v[122:125], v[66:81]
	v_sub_f32_e32 v86, v87, v183
	v_exp_f32_e32 v86, v86
	s_nop 0
	v_add_f32_e32 v87, v86, v84
	v_cvt_pk_bf16_f32 v84, v85, v86
	s_waitcnt lgkmcnt(5)
	v_mfma_f32_32x32x16_bf16 v[66:81], v[200:203], v[118:121], v[66:81]
	v_sub_f32_e32 v85, v88, v183
	v_exp_f32_e32 v85, v85
	s_nop 0
	v_add_f32_e32 v86, v85, v87
	s_waitcnt lgkmcnt(4)
	v_mfma_f32_32x32x16_bf16 v[66:81], v[216:219], v[114:117], v[66:81]
	v_sub_f32_e32 v87, v89, v183
	v_exp_f32_e32 v87, v87
	s_nop 0
	v_add_f32_e32 v86, v87, v86
	v_cvt_pk_bf16_f32 v85, v85, v87
	v_sub_f32_e32 v87, v90, v183
	v_exp_f32_e32 v90, v87
	s_waitcnt lgkmcnt(3)
	v_mfma_f32_32x32x16_bf16 v[66:81], v[220:223], v[110:113], v[66:81]
	v_add_u32_e32 v165, s13, v187
	v_add_f32_e32 v94, v90, v86
	ds_read_b128 v[86:89], v165
	ds_read_b128 v[166:169], v165 offset:32
	s_waitcnt lgkmcnt(4)
	v_mfma_f32_32x32x16_bf16 v[66:81], v[224:227], v[106:109], v[66:81]
	v_sub_f32_e32 v91, v91, v183
	ds_read_b128 v[170:173], v165 offset:4608
	ds_read_b128 v[188:191], v165 offset:4640
	v_exp_f32_e32 v91, v91
	s_nop 0
	v_add_f32_e32 v95, v91, v94
	v_cvt_pk_bf16_f32 v94, v90, v91
	s_waitcnt lgkmcnt(5)
	v_mfma_f32_32x32x16_bf16 v[66:81], v[228:231], v[102:105], v[66:81]
	v_sub_f32_e32 v90, v92, v183
	ds_read_b128 v[192:195], v165 offset:9216
	ds_read_b128 v[196:199], v165 offset:9248
	v_exp_f32_e32 v90, v90
	s_nop 0
	v_add_f32_e32 v91, v90, v95
	v_sub_f32_e32 v92, v93, v183
	v_exp_f32_e32 v92, v92
	s_waitcnt lgkmcnt(6)
	v_mfma_f32_32x32x16_bf16 v[66:81], v[146:149], v[98:101], v[66:81]
	v_add_f32_e32 v186, v92, v91
	v_cvt_pk_bf16_f32 v95, v90, v92
	ds_read_b128 v[90:93], v165 offset:13824
	ds_read_b128 v[146:149], v165 offset:13856
	s_waitcnt lgkmcnt(0)
	v_mfma_f32_32x32x16_bf16 v[50:65], v[86:89], v[82:85], v[50:65]
	v_add_f32_e32 v186, v164, v186
	v_mfma_f32_32x32x16_bf16 v[34:49], v[170:173], v[82:85], v[34:49]
	v_mfma_f32_32x32x16_bf16 v[18:33], v[192:195], v[82:85], v[18:33]
	v_mfma_f32_32x32x16_bf16 v[2:17], v[90:93], v[82:85], v[2:17]
	v_mfma_f32_32x32x16_bf16 v[50:65], v[166:169], v[94:97], v[50:65]
	v_mfma_f32_32x32x16_bf16 v[34:49], v[188:191], v[94:97], v[34:49]
	v_mfma_f32_32x32x16_bf16 v[18:33], v[196:199], v[94:97], v[18:33]
	v_mfma_f32_32x32x16_bf16 v[2:17], v[146:149], v[94:97], v[2:17]
	s_add_i32 s13, s14, 1
	s_cmp_lg_u32 s14, 2
	s_cselect_b32 s14, s13, 0
	s_add_i32 s13, s12, 1
	s_cmp_lg_u32 s12, 2
	s_cselect_b32 s36, s13, 0
	v_lshl_add_u64 v[150:151], v[150:151], 0, s[6:7]
	v_lshl_add_u64 v[152:153], v[152:153], 0, s[6:7]
	v_lshl_add_u64 v[154:155], v[154:155], 0, s[6:7]
	v_lshl_add_u64 v[156:157], v[156:157], 0, s[6:7]
	s_add_i32 s63, s63, 2
	v_lshl_add_u64 v[158:159], v[158:159], 0, s[10:11]
	v_lshl_add_u64 v[160:161], v[160:161], 0, s[10:11]
	s_andn2_b64 vcc, exec, s[0:1]
	v_lshl_add_u64 v[162:163], v[162:163], 0, s[10:11]
	s_cbranch_vccz .LBB0_1250

.LBB0_1240:
	s_mul_i32 s13, s14, 0x6400
	v_add_u32_e32 v86, s13, v185
	ds_read_b128 v[82:85], v86
	ds_read_b128 v[188:191], v86 offset:32
	ds_read_b128 v[192:195], v86 offset:64
	ds_read_b128 v[196:199], v86 offset:96
	ds_read_b128 v[200:203], v86 offset:128
	ds_read_b128 v[216:219], v86 offset:160
	ds_read_b128 v[220:223], v86 offset:192
	ds_read_b128 v[224:227], v86 offset:224
	ds_read_b128 v[228:231], v86 offset:256
	ds_read_b128 v[232:235], v86 offset:288
	ds_read_b128 v[236:239], v86 offset:320
	ds_read_b128 v[240:243], v86 offset:352
	s_waitcnt lgkmcnt(11)
	v_mfma_f32_32x32x16_bf16 v[82:97], v[82:85], v[142:145], 0
	v_sub_f32_e32 v66, v66, v183
	v_sub_f32_e32 v78, v78, v183
	v_exp_f32_e32 v66, v66
	v_exp_f32_e32 v78, v78
	s_waitcnt lgkmcnt(10)
	v_mfma_f32_32x32x16_bf16 v[82:97], v[188:191], v[138:141], v[82:97]
	v_sub_f32_e32 v67, v67, v183
	v_sub_f32_e32 v79, v79, v183
	v_exp_f32_e32 v67, v67
	v_exp_f32_e32 v79, v79
	v_cvt_pk_bf16_f32 v188, v66, v67
	s_waitcnt lgkmcnt(9)
	v_mfma_f32_32x32x16_bf16 v[82:97], v[192:195], v[134:137], v[82:97]
	v_sub_f32_e32 v68, v68, v183
	v_sub_f32_e32 v80, v80, v183
	v_exp_f32_e32 v68, v68
	v_exp_f32_e32 v80, v80
	s_waitcnt lgkmcnt(8)
	v_mfma_f32_32x32x16_bf16 v[82:97], v[196:199], v[130:133], v[82:97]
	v_sub_f32_e32 v69, v69, v183
	v_sub_f32_e32 v81, v81, v183
	v_exp_f32_e32 v69, v69
	v_exp_f32_e32 v81, v81
	v_cvt_pk_bf16_f32 v194, v78, v79
	v_cvt_pk_bf16_f32 v189, v68, v69
	v_cvt_pk_bf16_f32 v195, v80, v81
	s_waitcnt lgkmcnt(7)
	v_mfma_f32_32x32x16_bf16 v[82:97], v[200:203], v[126:129], v[82:97]
	v_sub_f32_e32 v70, v70, v183
	v_exp_f32_e32 v70, v70
	s_waitcnt lgkmcnt(6)
	v_mfma_f32_32x32x16_bf16 v[82:97], v[216:219], v[122:125], v[82:97]
	v_sub_f32_e32 v71, v71, v183
	v_exp_f32_e32 v71, v71
	s_nop 0
	v_cvt_pk_bf16_f32 v190, v70, v71
	s_waitcnt lgkmcnt(5)
	v_mfma_f32_32x32x16_bf16 v[82:97], v[220:223], v[118:121], v[82:97]
	v_sub_f32_e32 v72, v72, v183
	v_exp_f32_e32 v72, v72
	s_waitcnt lgkmcnt(4)
	v_mfma_f32_32x32x16_bf16 v[82:97], v[224:227], v[114:117], v[82:97]
	v_sub_f32_e32 v73, v73, v183
	v_exp_f32_e32 v73, v73
	s_nop 0
	v_cvt_pk_bf16_f32 v191, v72, v73
	s_waitcnt lgkmcnt(3)
	v_mfma_f32_32x32x16_bf16 v[82:97], v[228:231], v[110:113], v[82:97]
	v_add_u32_e32 v204, s12, v187
	v_sub_f32_e32 v74, v74, v183
	ds_read_b128 v[196:199], v204
	ds_read_b128 v[200:203], v204 offset:32
	v_exp_f32_e32 v74, v74
	s_waitcnt lgkmcnt(4)
	v_mfma_f32_32x32x16_bf16 v[82:97], v[232:235], v[106:109], v[82:97]
	v_sub_f32_e32 v75, v75, v183
	ds_read_b128 v[216:219], v204 offset:4608
	ds_read_b128 v[220:223], v204 offset:4640
	v_exp_f32_e32 v75, v75
	s_nop 0
	v_cvt_pk_bf16_f32 v192, v74, v75
	s_waitcnt lgkmcnt(5)
	v_mfma_f32_32x32x16_bf16 v[82:97], v[236:239], v[102:105], v[82:97]
	v_sub_f32_e32 v76, v76, v183
	ds_read_b128 v[224:227], v204 offset:9216
	ds_read_b128 v[228:231], v204 offset:9248
	v_exp_f32_e32 v76, v76
	s_waitcnt lgkmcnt(6)
	v_mfma_f32_32x32x16_bf16 v[82:97], v[240:243], v[98:101], v[82:97]
	v_sub_f32_e32 v77, v77, v183
	ds_read_b128 v[232:235], v204 offset:13824
	ds_read_b128 v[236:239], v204 offset:13856
	v_exp_f32_e32 v77, v77
	s_nop 0
	v_cvt_pk_bf16_f32 v193, v76, v77
	s_waitcnt lgkmcnt(0)
	v_mfma_f32_32x32x16_bf16 v[50:65], v[196:199], v[188:191], v[50:65]
	v_mfma_f32_32x32x16_bf16 v[34:49], v[216:219], v[188:191], v[34:49]
	v_mfma_f32_32x32x16_bf16 v[18:33], v[224:227], v[188:191], v[18:33]
	v_mfma_f32_32x32x16_bf16 v[2:17], v[232:235], v[188:191], v[2:17]
	v_mfma_f32_32x32x16_bf16 v[50:65], v[200:203], v[192:195], v[50:65]
	v_mfma_f32_32x32x16_bf16 v[34:49], v[220:223], v[192:195], v[34:49]
	v_mfma_f32_32x32x16_bf16 v[18:33], v[228:231], v[192:195], v[18:33]
	v_mfma_f32_32x32x16_bf16 v[2:17], v[236:239], v[192:195], v[2:17]
	s_mov_b64 s[12:13], -1
	s_and_b64 vcc, exec, s[0:1]
	s_cbranch_vccz .LBB0_1242
	s_waitcnt vmcnt(0)
	s_mov_b64 s[12:13], 0

; #define ATT_SYNC(full) do { if (full) asm volatile("s_waitcnt vmcnt(7)" ::: "memory"); else asm volatile("s_waitcnt vmcnt(0)" ::: "memory"); \
;         __builtin_amdgcn_s_barrier(); asm volatile("" ::: "memory"); } while (0)
; __device__ __forceinline__ void attn_unit(const bf16_t* Qrows  , const bf16_t* Kbh, const bf16_t* Vbh, int nkeys, bf16_t* Orows, LAS unsigned char* lds) {
;     ...
;     ATT_SYNC(false);
;     ATT_STEP(sA, sB, true, k1, v0);
;     k1 = k1 == 2 ? 0 : k1 + 1; v0 = v0 == 2 ? 0 : v0 + 1;
;     ATT_SYNC(false);
;     ATT_STEP(sB, sA, false, k1, v0);
.LBB0_1252:
	s_mul_i32 s0, s14, 0x6400
	s_add_i32 s0, s0, 0
	v_add3_u32 v86, s0, v184, v206
	ds_read_b128 v[82:85], v86
	ds_read_b128 v[152:155], v86 offset:32
	ds_read_b128 v[156:159], v86 offset:64
	ds_read_b128 v[160:163], v86 offset:96
	ds_read_b128 v[164:167], v86 offset:128
	ds_read_b128 v[168:171], v86 offset:160
	ds_read_b128 v[188:191], v86 offset:192
	ds_read_b128 v[192:195], v86 offset:224
	ds_read_b128 v[196:199], v86 offset:256
	ds_read_b128 v[200:203], v86 offset:288
	ds_read_b128 v[216:219], v86 offset:320
	ds_read_b128 v[146:149], v86 offset:352
	s_mul_i32 s0, s36, 0x4800
	s_add_i32 s1, s0, 0
	s_add_i32 s1, s1, 0x12c00
	s_waitcnt lgkmcnt(11)
	v_mfma_f32_32x32x16_bf16 v[82:97], v[82:85], v[142:145], 0
	v_sub_f32_e32 v66, v66, v183
	v_exp_f32_e32 v66, v66
	v_sub_f32_e32 v78, v78, v183
	v_exp_f32_e32 v78, v78
	v_add_u32_e32 v151, s1, v181
	v_add_f32_e32 v142, 0, v66
	v_add_f32_e32 v142, v78, v142
	s_waitcnt lgkmcnt(10)
	v_mfma_f32_32x32x16_bf16 v[82:97], v[152:155], v[138:141], v[82:97]
	v_sub_f32_e32 v67, v67, v183
	v_exp_f32_e32 v67, v67
	v_sub_f32_e32 v79, v79, v183
	v_exp_f32_e32 v79, v79
	v_add_f32_e32 v138, v67, v142
	v_cvt_pk_bf16_f32 v66, v66, v67
	v_add_f32_e32 v138, v79, v138
	s_waitcnt lgkmcnt(9)
	v_mfma_f32_32x32x16_bf16 v[82:97], v[156:159], v[134:137], v[82:97]
	v_sub_f32_e32 v67, v68, v183
	v_exp_f32_e32 v67, v67
	v_sub_f32_e32 v80, v80, v183
	v_exp_f32_e32 v134, v80
	v_add_f32_e32 v68, v67, v138
	v_add_f32_e32 v68, v134, v68
	s_waitcnt lgkmcnt(8)
	v_mfma_f32_32x32x16_bf16 v[82:97], v[160:163], v[130:133], v[82:97]
	v_sub_f32_e32 v69, v69, v183
	v_exp_f32_e32 v69, v69
	v_sub_f32_e32 v80, v81, v183
	v_exp_f32_e32 v81, v80
	v_cvt_pk_bf16_f32 v80, v78, v79
	v_add_f32_e32 v68, v69, v68
	v_cvt_pk_bf16_f32 v67, v67, v69
	v_add_f32_e32 v68, v81, v68
	v_cvt_pk_bf16_f32 v81, v134, v81
	s_waitcnt lgkmcnt(7)
	v_mfma_f32_32x32x16_bf16 v[82:97], v[164:167], v[126:129], v[82:97]
	v_sub_f32_e32 v69, v70, v183
	v_exp_f32_e32 v69, v69
	s_nop 0
	v_add_f32_e32 v68, v69, v68
	s_waitcnt lgkmcnt(6)
	v_mfma_f32_32x32x16_bf16 v[82:97], v[168:171], v[122:125], v[82:97]
	v_sub_f32_e32 v70, v71, v183
	v_exp_f32_e32 v70, v70
	s_nop 0
	v_add_f32_e32 v71, v70, v68
	v_cvt_pk_bf16_f32 v68, v69, v70
	s_waitcnt lgkmcnt(5)
	v_mfma_f32_32x32x16_bf16 v[82:97], v[188:191], v[118:121], v[82:97]
	v_sub_f32_e32 v69, v72, v183
	v_exp_f32_e32 v69, v69
	s_nop 0
	v_add_f32_e32 v70, v69, v71
	s_waitcnt lgkmcnt(4)
	v_mfma_f32_32x32x16_bf16 v[82:97], v[192:195], v[114:117], v[82:97]
	v_sub_f32_e32 v71, v73, v183
	v_exp_f32_e32 v71, v71
	s_nop 0
	v_add_f32_e32 v70, v71, v70
	v_cvt_pk_bf16_f32 v69, v69, v71
	v_sub_f32_e32 v71, v74, v183
	v_exp_f32_e32 v74, v71
	s_waitcnt lgkmcnt(3)
	v_mfma_f32_32x32x16_bf16 v[82:97], v[196:199], v[110:113], v[82:97]
	v_add3_u32 v122, v151, v206, v182
	v_add_f32_e32 v78, v74, v70
	ds_read_b128 v[70:73], v122
	ds_read_b128 v[110:113], v122 offset:32
	s_waitcnt lgkmcnt(4)
	v_mfma_f32_32x32x16_bf16 v[82:97], v[200:203], v[106:109], v[82:97]
	v_sub_f32_e32 v75, v75, v183
	ds_read_b128 v[106:109], v122 offset:4608
	ds_read_b128 v[114:117], v122 offset:4640
	v_exp_f32_e32 v75, v75
	s_nop 0
	v_add_f32_e32 v79, v75, v78
	v_cvt_pk_bf16_f32 v78, v74, v75
	s_waitcnt lgkmcnt(5)
	v_mfma_f32_32x32x16_bf16 v[82:97], v[216:219], v[102:105], v[82:97]
	v_sub_f32_e32 v74, v76, v183
	ds_read_b128 v[102:105], v122 offset:9216
	ds_read_b128 v[118:121], v122 offset:9248
	v_exp_f32_e32 v74, v74
	s_nop 0
	v_add_f32_e32 v75, v74, v79
	v_sub_f32_e32 v76, v77, v183
	v_exp_f32_e32 v76, v76
	s_waitcnt lgkmcnt(6)
	v_mfma_f32_32x32x16_bf16 v[82:97], v[146:149], v[98:101], v[82:97]
	v_add_f32_e32 v123, v76, v75
	v_cvt_pk_bf16_f32 v79, v74, v76
	ds_read_b128 v[74:77], v122 offset:13824
	ds_read_b128 v[98:101], v122 offset:13856
	s_waitcnt lgkmcnt(0)
	v_mfma_f32_32x32x16_bf16 v[50:65], v[70:73], v[66:69], v[50:65]
	v_mfma_f32_32x32x16_bf16 v[34:49], v[106:109], v[66:69], v[34:49]
	v_mfma_f32_32x32x16_bf16 v[18:33], v[102:105], v[66:69], v[18:33]
	v_mfma_f32_32x32x16_bf16 v[2:17], v[74:77], v[66:69], v[2:17]
	v_mfma_f32_32x32x16_bf16 v[50:65], v[110:113], v[78:81], v[50:65]
	v_mfma_f32_32x32x16_bf16 v[34:49], v[114:117], v[78:81], v[34:49]
	v_mfma_f32_32x32x16_bf16 v[18:33], v[118:121], v[78:81], v[18:33]
	v_mfma_f32_32x32x16_bf16 v[2:17], v[98:101], v[78:81], v[2:17]
	v_max_f32_e32 v66, v83, v83
	v_max_f32_e32 v67, v82, v82
	v_max_f32_e32 v66, v67, v66
	v_max3_f32 v66, v66, v84, v85
	v_max3_f32 v66, v66, v86, v87
	v_max3_f32 v66, v66, v88, v89
	v_max3_f32 v66, v66, v90, v91
	v_max3_f32 v66, v66, v92, v93
	v_max3_f32 v66, v66, v94, v95
	v_max3_f32 v67, v66, v96, v97
	v_mov_b32_e32 v68, v67
	s_nop 1
	v_permlane32_swap_b32_e32 v68, v67
	s_waitcnt vmcnt(0)
	s_barrier
	v_add_f32_e32 v66, v186, v123
	s_waitcnt lgkmcnt(0)
	v_max_f32_e32 v68, v68, v68
	v_max_f32_e32 v67, v67, v68
	v_cmp_gt_f32_e32 vcc, v67, v150
	s_cbranch_vccz .LBB0_1254
	v_max_f32_e32 v67, v67, v67
	v_max_f32_e32 v68, v183, v183
	v_max_f32_e32 v67, v68, v67
	v_sub_f32_e32 v68, v183, v67
	v_exp_f32_e32 v68, v68
	v_mov_b32_e32 v183, v67
	v_pk_mul_f32 v[64:65], v[64:65], v[68:69] op_sel_hi:[1,0]
	v_pk_mul_f32 v[62:63], v[62:63], v[68:69] op_sel_hi:[1,0]
	v_pk_mul_f32 v[60:61], v[60:61], v[68:69] op_sel_hi:[1,0]
	v_pk_mul_f32 v[58:59], v[58:59], v[68:69] op_sel_hi:[1,0]
	v_pk_mul_f32 v[56:57], v[56:57], v[68:69] op_sel_hi:[1,0]
	v_pk_mul_f32 v[54:55], v[54:55], v[68:69] op_sel_hi:[1,0]
	v_pk_mul_f32 v[52:53], v[52:53], v[68:69] op_sel_hi:[1,0]
	v_pk_mul_f32 v[50:51], v[50:51], v[68:69] op_sel_hi:[1,0]
	v_pk_mul_f32 v[48:49], v[48:49], v[68:69] op_sel_hi:[1,0]
	v_pk_mul_f32 v[46:47], v[46:47], v[68:69] op_sel_hi:[1,0]
	v_pk_mul_f32 v[44:45], v[44:45], v[68:69] op_sel_hi:[1,0]
	v_pk_mul_f32 v[42:43], v[42:43], v[68:69] op_sel_hi:[1,0]
	v_pk_mul_f32 v[40:41], v[40:41], v[68:69] op_sel_hi:[1,0]
	v_pk_mul_f32 v[38:39], v[38:39], v[68:69] op_sel_hi:[1,0]
	v_pk_mul_f32 v[36:37], v[36:37], v[68:69] op_sel_hi:[1,0]
	v_pk_mul_f32 v[34:35], v[34:35], v[68:69] op_sel_hi:[1,0]
	v_pk_mul_f32 v[32:33], v[32:33], v[68:69] op_sel_hi:[1,0]
	v_pk_mul_f32 v[30:31], v[30:31], v[68:69] op_sel_hi:[1,0]
	v_pk_mul_f32 v[28:29], v[28:29], v[68:69] op_sel_hi:[1,0]
	v_pk_mul_f32 v[26:27], v[26:27], v[68:69] op_sel_hi:[1,0]
	v_pk_mul_f32 v[24:25], v[24:25], v[68:69] op_sel_hi:[1,0]
	v_pk_mul_f32 v[22:23], v[22:23], v[68:69] op_sel_hi:[1,0]
	v_pk_mul_f32 v[20:21], v[20:21], v[68:69] op_sel_hi:[1,0]
	v_pk_mul_f32 v[18:19], v[18:19], v[68:69] op_sel_hi:[1,0]
	v_pk_mul_f32 v[16:17], v[16:17], v[68:69] op_sel_hi:[1,0]
	v_pk_mul_f32 v[14:15], v[14:15], v[68:69] op_sel_hi:[1,0]
	v_pk_mul_f32 v[12:13], v[12:13], v[68:69] op_sel_hi:[1,0]
	v_pk_mul_f32 v[10:11], v[10:11], v[68:69] op_sel_hi:[1,0]
	v_pk_mul_f32 v[8:9], v[8:9], v[68:69] op_sel_hi:[1,0]
	v_pk_mul_f32 v[6:7], v[6:7], v[68:69] op_sel_hi:[1,0]
	v_pk_mul_f32 v[4:5], v[4:5], v[68:69] op_sel_hi:[1,0]
	v_pk_mul_f32 v[2:3], v[2:3], v[68:69] op_sel_hi:[1,0]
	v_mul_f32_e32 v66, v66, v68

; #define LAS __attribute__((address_space(3)))
; __device__ __forceinline__ void sgu_unit(const Params& p, int l, int un, LAS unsigned char* lds) {
;     ...
;     const int cc = un >> 2, h = un & 3; const int row0 = cc * 128;
;     LAS bf16_t* Wl = (LAS bf16_t*)lds;
;     LAS bf16_t* Vl = (LAS bf16_t*)(lds + 128 * 136 * 2);
;     const float* Wg = p.in[I_SGUW] + ((size_t)l * 4 + h) * 128 * 128;
;     f32x4 wq[8]; u32x4 vv[16];
; #pragma unroll
;     for (int i = 0; i < 8; ++i) wq[i] = *(const f32x4*)(Wg + (i * 512 + tid) * 4);
; #pragma unroll
;     for (int qi = 0; qi < 16; ++qi) vv[qi] = *(const u32x4*)(P + (size_t)(row0 + wave * 16 + qi) * INP + C_SGU_V + lane * 8);
; __global__ void __launch_bounds__(512, 2) fwd(Params p) {
;     ...
;               pg8::Unit u0; if (S.next(0, u0)) { carry_wait(p, l); pg8::gemm_phase(lds, pg8::Desc{512, 512, 512}, S, E); }
;               else if (G == 256) { const int un = c - (l == 0 ? 128 : 96); if (un >= 0) sgu_unit(p, l, un, lds); } }
.LBB0_1258:
	v_readlane_b32 s0, v251, 50
	v_readlane_b32 s2, v252, 20
	v_readlane_b32 s1, v251, 51
	v_readlane_b32 s3, v252, 21
	s_and_b64 s[0:1], s[0:1], s[2:3]
	s_and_b64 s[0:1], s[0:1], exec
	s_cselect_b32 s0, 32, 0
	v_readlane_b32 s2, v255, 11
	s_mul_hi_u32 s1, s0, s2
	v_readlane_b32 s3, v255, 12
	s_mul_i32 s1, s1, s3
	s_sub_i32 s0, s0, s1
	s_sub_i32 s1, s0, s3
	s_cmp_ge_u32 s0, s3
	s_cselect_b32 s0, s1, s0
	s_sub_i32 s1, s0, s3
	s_cmp_ge_u32 s0, s3
	s_cselect_b32 s0, s1, s0
	v_readlane_b32 s1, v255, 42
	s_sub_i32 s0, s1, s0
	s_ashr_i32 s1, s0, 31
	s_abs_i32 s0, s0
	s_mul_hi_u32 s2, s0, s2
	s_mul_i32 s2, s2, s3
	s_sub_i32 s0, s0, s2
	s_sub_i32 s2, s0, s3
	s_cmp_ge_u32 s0, s3
	s_cselect_b32 s0, s2, s0
	s_sub_i32 s2, s0, s3
	s_cmp_ge_u32 s0, s3
	s_cselect_b32 s0, s2, s0
	s_xor_b32 s0, s0, s1
	s_sub_i32 s26, s0, s1
	s_cmpk_gt_i32 s26, 0x5f
	s_mov_b64 s[0:1], -1
	s_barrier
	s_cbranch_scc0 .LBB0_1294
	v_readlane_b32 s0, v252, 20
	v_readlane_b32 s1, v252, 21
	s_and_b64 s[0:1], s[0:1], exec
	s_movk_i32 s0, 0xff80
	s_cselect_b32 s0, s0, 0xffffffa0
	s_add_i32 s0, s0, s92
	v_readlane_b32 s12, v251, 50
	s_cmp_lt_i32 s0, 0
	v_readlane_b32 s13, v251, 51
	s_cselect_b64 s[2:3], -1, 0
	s_xor_b64 s[12:13], s[12:13], -1
	s_or_b64 s[2:3], s[2:3], s[12:13]
	s_and_b64 vcc, exec, s[2:3]
	s_cbranch_vccnz .LBB0_1293
	v_readlane_b32 s2, v252, 5
	v_readlane_b32 s44, v251, 16
	s_lshl_b32 s1, s0, 5
	s_lshl_b32 s0, s2, 9
	v_readlane_b32 s2, v253, 39
	v_readlane_b32 s48, v251, 20
	v_readlane_b32 s49, v251, 21
	v_readlane_b32 s3, v252, 6
	s_or_b32 s40, s0, s2
	s_mov_b32 s41, s5
	v_readlane_b32 s50, v251, 22
	v_readlane_b32 s51, v251, 23
	v_readlane_b32 s52, v251, 24
	v_readlane_b32 s53, v251, 25
	v_readlane_b32 s54, v251, 26
	v_readlane_b32 s55, v251, 27
	s_mov_b64 s[12:13], s[48:49]
	s_lshl_b64 s[2:3], s[40:41], 9
	s_mov_b64 s[14:15], s[50:51]
	v_mov_b32_e32 v64, v0
	s_add_u32 s2, s14, s2
	s_addc_u32 s3, s15, s3
	v_lshlrev_b32_e32 v2, 2, v64
	v_ashrrev_i32_e32 v3, 31, v2
	v_add_u32_e32 v62, 0x800, v2
	s_mov_b64 s[14:15], 0
	v_lshl_add_u64 v[4:5], v[2:3], 2, s[2:3]
	v_ashrrev_i32_e32 v63, 31, v62
	v_lshl_add_u64 v[6:7], v[62:63], 2, s[2:3]
	global_load_dwordx4 v[66:69], v[4:5], off
	global_load_dwordx4 v[70:73], v[6:7], off
	v_add_u32_e32 v102, 0x1000, v2
	v_ashrrev_i32_e32 v103, 31, v102
	v_add_u32_e32 v104, 0x1800, v2
	v_lshl_add_u64 v[4:5], v[102:103], 2, s[2:3]
	v_ashrrev_i32_e32 v105, 31, v104
	s_and_b32 s12, s1, 0x7fffff80
	s_mov_b32 s1, s5
	v_lshl_add_u64 v[6:7], v[104:105], 2, s[2:3]
	global_load_dwordx4 v[74:77], v[4:5], off
	global_load_dwordx4 v[78:81], v[6:7], off
	s_lshl_b64 s[0:1], s[0:1], 2
	v_readlane_b32 s13, v253, 41
	v_add_u32_e32 v106, 0x2000, v2
	s_add_u32 s0, s13, s0
	v_readlane_b32 s13, v253, 42
	v_ashrrev_i32_e32 v107, 31, v106
	v_add_u32_e32 v108, 0x2800, v2
	s_addc_u32 s1, s13, s1
	v_lshl_add_u64 v[4:5], v[106:107], 2, s[2:3]
	v_ashrrev_i32_e32 v109, 31, v108
	s_add_u32 s36, s84, s14
	v_lshl_add_u64 v[6:7], v[108:109], 2, s[2:3]
	global_load_dwordx4 v[82:85], v[4:5], off
	global_load_dwordx4 v[86:89], v[6:7], off
	s_addc_u32 s37, s85, s15
	v_add_u32_e32 v110, 0x3000, v2
	v_add_u32_e32 v112, 0x3800, v2
	s_add_u32 s38, s36, 0x1f1b8000
	v_ashrrev_i32_e32 v111, 31, v110
	v_ashrrev_i32_e32 v113, 31, v112
	v_ashrrev_i32_e32 v103, 6, v64
	s_addc_u32 s39, s37, 0
	v_lshl_add_u64 v[4:5], v[110:111], 2, s[2:3]
	v_lshl_add_u64 v[2:3], v[112:113], 2, s[2:3]
	v_lshlrev_b32_e32 v65, 4, v103
	v_and_b32_e32 v8, 63, v64
	global_load_dwordx4 v[90:93], v[4:5], off
	global_load_dwordx4 v[94:97], v[2:3], off
	v_add_u32_e32 v9, s12, v65
	v_mov_b64_e32 v[2:3], s[38:39]
	s_movk_i32 s13, 0x1e00
	v_mad_i64_i32 v[4:5], s[2:3], v9, s13, v[2:3]
	v_lshlrev_b32_e32 v206, 4, v8
	v_or_b32_e32 v6, 1, v9
	v_lshl_add_u64 v[4:5], v[4:5], 0, v[206:207]
	v_mad_i64_i32 v[6:7], s[2:3], v6, s13, v[2:3]
	v_lshl_add_u64 v[6:7], v[6:7], 0, v[206:207]
	global_load_dwordx4 v[98:101], v[4:5], off offset:1024
	global_load_dwordx4 v[58:61], v[6:7], off offset:1024
	v_or_b32_e32 v4, 2, v9
	v_or_b32_e32 v6, 3, v9
	v_mad_i64_i32 v[4:5], s[2:3], v4, s13, v[2:3]
	v_mad_i64_i32 v[6:7], s[2:3], v6, s13, v[2:3]
	v_lshl_add_u64 v[4:5], v[4:5], 0, v[206:207]
	v_lshl_add_u64 v[6:7], v[6:7], 0, v[206:207]
	global_load_dwordx4 v[54:57], v[4:5], off offset:1024
	global_load_dwordx4 v[50:53], v[6:7], off offset:1024
	v_or_b32_e32 v4, 4, v9
	v_or_b32_e32 v6, 5, v9
	v_mad_i64_i32 v[4:5], s[2:3], v4, s13, v[2:3]
	v_mad_i64_i32 v[6:7], s[2:3], v6, s13, v[2:3]
	v_lshl_add_u64 v[4:5], v[4:5], 0, v[206:207]
	v_lshl_add_u64 v[6:7], v[6:7], 0, v[206:207]
	global_load_dwordx4 v[46:49], v[4:5], off offset:1024
	global_load_dwordx4 v[42:45], v[6:7], off offset:1024
	v_or_b32_e32 v4, 6, v9
	v_or_b32_e32 v6, 7, v9
	v_mad_i64_i32 v[4:5], s[2:3], v4, s13, v[2:3]
	v_mad_i64_i32 v[6:7], s[2:3], v6, s13, v[2:3]
	v_lshl_add_u64 v[4:5], v[4:5], 0, v[206:207]
	v_lshl_add_u64 v[6:7], v[6:7], 0, v[206:207]
	global_load_dwordx4 v[38:41], v[4:5], off offset:1024
	global_load_dwordx4 v[34:37], v[6:7], off offset:1024
	v_or_b32_e32 v4, 8, v9
	v_or_b32_e32 v6, 9, v9
	v_mad_i64_i32 v[4:5], s[2:3], v4, s13, v[2:3]
	v_mad_i64_i32 v[6:7], s[2:3], v6, s13, v[2:3]
	v_lshl_add_u64 v[4:5], v[4:5], 0, v[206:207]
	v_lshl_add_u64 v[6:7], v[6:7], 0, v[206:207]
	global_load_dwordx4 v[30:33], v[4:5], off offset:1024
	global_load_dwordx4 v[26:29], v[6:7], off offset:1024
	v_or_b32_e32 v4, 10, v9
	v_or_b32_e32 v6, 11, v9
	v_mad_i64_i32 v[4:5], s[2:3], v4, s13, v[2:3]
	v_mad_i64_i32 v[6:7], s[2:3], v6, s13, v[2:3]
	v_lshl_add_u64 v[4:5], v[4:5], 0, v[206:207]
	v_lshl_add_u64 v[6:7], v[6:7], 0, v[206:207]
	global_load_dwordx4 v[22:25], v[4:5], off offset:1024
	global_load_dwordx4 v[18:21], v[6:7], off offset:1024
	v_or_b32_e32 v4, 12, v9
	v_or_b32_e32 v6, 13, v9
	v_mad_i64_i32 v[4:5], s[2:3], v4, s13, v[2:3]
	v_mad_i64_i32 v[6:7], s[2:3], v6, s13, v[2:3]
	v_lshl_add_u64 v[4:5], v[4:5], 0, v[206:207]
	v_lshl_add_u64 v[6:7], v[6:7], 0, v[206:207]
	v_lshlrev_b32_e32 v105, 3, v64
	global_load_dwordx4 v[14:17], v[4:5], off offset:1024
	global_load_dwordx4 v[10:13], v[6:7], off offset:1024
	v_or_b32_e32 v4, 14, v9
	v_or_b32_e32 v6, 15, v9
	v_and_b32_e32 v63, 0xf8, v105
	v_mad_i64_i32 v[4:5], s[2:3], v4, s13, v[2:3]
	v_mad_i64_i32 v[2:3], s[2:3], v6, s13, v[2:3]
	v_add_u32_e32 v114, 0, v63
	v_bfe_i32 v63, v64, 5, 25
	s_movk_i32 s13, 0x110
	v_lshl_add_u64 v[4:5], v[4:5], 0, v[206:207]
	v_lshl_add_u64 v[2:3], v[2:3], 0, v[206:207]
	s_waitcnt vmcnt(21)
; #define LAS __attribute__((address_space(3)))
; __device__ __forceinline__ unsigned cvt_pk_bf16(float lo, float hi) { const f32x2 v = {lo, hi}; const bf16x2_t b = __builtin_convertvector(v, bf16x2_t); return __builtin_bit_cast(unsigned, b); }
; __device__ __forceinline__ float bflo(unsigned w) { return __uint_as_float(w << 16); }
; __device__ __forceinline__ float bfhi(unsigned w) { return __uint_as_float(w & 0xffff0000u); }
; __device__ __forceinline__ unsigned short f2bf(float f) { return (unsigned short)(cvt_pk_bf16(f, 0.f) & 0xffffu); }
; __device__ __forceinline__ void sgu_unit(const Params& p, int l, int un, LAS unsigned char* lds) {
;     ...
;     for (int i = 0; i < 8; ++i) { const int e4 = (i * 512 + tid) * 4, r = e4 >> 7, c = e4 & 127; const f32x4 v = wq[i];
;         u32x2 w; w.x = cvt_pk_bf16(v[0], v[1]); w.y = cvt_pk_bf16(v[2], v[3]); *(LAS u32x2*)(Wl + r * 136 + c) = w; }
; #pragma unroll
;     for (int qi = 0; qi < 16; ++qi) { const int q = wave * 16 + qi;
;         const u32x4 v = vv[qi]; float f[8] = {bflo(v.x), bfhi(v.x), bflo(v.y), bfhi(v.y), bflo(v.z), bfhi(v.z), bflo(v.w), bfhi(v.w)}; float ss = 0.f;
; #pragma unroll
;         for (int j = 0; j < 8; ++j) { f[j] = gelu_tanh(f[j]); ss += f[j] * f[j]; }
;         ss = wave_sum(ss); const float rinv = rsqrtf(ss * (1.0f / 512.0f) + EPS);
;         if ((lane >> 4) == h) { const int c0 = (lane & 15) * 8; const float* g = p.in[I_SGUNG] + l * 512 + h * 128 + c0;
; #pragma unroll
;             for (int j = 0; j < 8; ++j) Vl[(c0 + j) * 136 + q] = f2bf(f[j] * rinv * g[j]); } }
	v_cvt_pk_bf16_f32 v66, v66, v67
	v_cvt_pk_bf16_f32 v67, v68, v69
	v_mad_u64_u32 v[68:69], s[2:3], v63, s13, v[114:115]
	global_load_dwordx4 v[6:9], v[4:5], off offset:1024
	s_nop 0
	global_load_dwordx4 v[2:5], v[2:3], off offset:1024
	ds_write_b64 v68, v[66:67]
	v_ashrrev_i32_e32 v66, 7, v62
	s_waitcnt vmcnt(22)
	v_cvt_pk_bf16_f32 v62, v70, v71
	v_cvt_pk_bf16_f32 v63, v72, v73
	v_mad_u64_u32 v[66:67], s[2:3], v66, s13, v[114:115]
	ds_write_b64 v66, v[62:63]
	v_ashrrev_i32_e32 v66, 7, v102
	s_waitcnt vmcnt(21)
	v_cvt_pk_bf16_f32 v62, v74, v75
	v_cvt_pk_bf16_f32 v63, v76, v77
	v_mad_u64_u32 v[66:67], s[2:3], v66, s13, v[114:115]
	ds_write_b64 v66, v[62:63]
	v_ashrrev_i32_e32 v66, 7, v104
	s_waitcnt vmcnt(20)
	v_cvt_pk_bf16_f32 v62, v78, v79
	v_cvt_pk_bf16_f32 v63, v80, v81
	v_mad_u64_u32 v[66:67], s[2:3], v66, s13, v[114:115]
	ds_write_b64 v66, v[62:63]
	v_ashrrev_i32_e32 v66, 7, v106
	s_waitcnt vmcnt(19)
	v_cvt_pk_bf16_f32 v62, v82, v83
	v_cvt_pk_bf16_f32 v63, v84, v85
	v_mad_u64_u32 v[66:67], s[2:3], v66, s13, v[114:115]
	ds_write_b64 v66, v[62:63]
	v_ashrrev_i32_e32 v66, 7, v108
	s_waitcnt vmcnt(18)
	v_cvt_pk_bf16_f32 v62, v86, v87
	v_cvt_pk_bf16_f32 v63, v88, v89
	v_mad_u64_u32 v[66:67], s[2:3], v66, s13, v[114:115]
	ds_write_b64 v66, v[62:63]
	v_ashrrev_i32_e32 v66, 7, v110
	s_waitcnt vmcnt(17)
	v_cvt_pk_bf16_f32 v62, v90, v91
	v_cvt_pk_bf16_f32 v63, v92, v93
	v_mad_u64_u32 v[66:67], s[2:3], v66, s13, v[114:115]
	ds_write_b64 v66, v[62:63]
	v_ashrrev_i32_e32 v66, 7, v112
	v_mad_u64_u32 v[66:67], s[2:3], v66, s13, v[114:115]
	s_waitcnt vmcnt(15)
	v_and_b32_e32 v67, 0xffff0000, v98
	v_mul_f32_e32 v73, 0x3dd2d3e8, v67
	v_fma_f32 v73, -v73, v67, s33
	v_mul_f32_e32 v73, v73, v67
	v_exp_f32_e32 v73, v73
	v_cvt_pk_bf16_f32 v62, v94, v95
	v_cvt_pk_bf16_f32 v63, v96, v97
	ds_write_b64 v66, v[62:63]
	v_lshlrev_b32_e32 v66, 16, v98
	v_add_f32_e32 v73, 1.0, v73
	v_mul_f32_e32 v72, 0x3dd2d3e8, v66
	v_rcp_f32_e32 v73, v73
	v_fma_f32 v72, -v72, v66, s33
	v_mul_f32_e32 v72, v72, v66
	v_lshlrev_b32_e32 v69, 16, v99
	v_exp_f32_e32 v72, v72
	v_mul_f32_e32 v79, v73, v67
	v_mul_f32_e32 v67, 0x3dd2d3e8, v69
	v_fma_f32 v67, -v67, v69, s33
	v_mul_f32_e32 v67, v67, v69
	v_add_f32_e32 v72, 1.0, v72
	v_exp_f32_e32 v67, v67
	v_rcp_f32_e32 v72, v72
	v_lshlrev_b32_e32 v71, 16, v100
	v_and_b32_e32 v70, 0xffff0000, v99
	v_add_f32_e32 v67, 1.0, v67
	v_mul_f32_e32 v73, 0x3dd2d3e8, v71
	v_mul_f32_e32 v81, v72, v66
	v_mul_f32_e32 v72, 0x3dd2d3e8, v70
	v_rcp_f32_e32 v67, v67
	v_fma_f32 v73, -v73, v71, s33
	v_fma_f32 v72, -v72, v70, s33
	v_mul_f32_e32 v73, v73, v71
	v_mul_f32_e32 v72, v72, v70
	v_exp_f32_e32 v73, v73
	v_and_b32_e32 v74, 0xffff0000, v100
	v_exp_f32_e32 v72, v72
	v_mul_f32_e32 v80, v67, v69
	v_mul_f32_e32 v69, 0x3dd2d3e8, v74
	v_fma_f32 v69, -v69, v74, s33
	v_add_f32_e32 v67, 1.0, v73
	v_mul_f32_e32 v69, v69, v74
	v_add_f32_e32 v72, 1.0, v72
	v_rcp_f32_e32 v67, v67
	v_exp_f32_e32 v69, v69
	v_rcp_f32_e32 v72, v72
	v_lshlrev_b32_e32 v75, 16, v101
	v_and_b32_e32 v82, 0xffff0000, v101
	v_mul_f32_e32 v76, v67, v71
	v_add_f32_e32 v67, 1.0, v69
	v_mul_f32_e32 v69, 0x3dd2d3e8, v75
	v_mul_f32_e32 v78, v72, v70
	v_fma_f32 v69, -v69, v75, s33
	v_mul_f32_e32 v70, 0x3dd2d3e8, v82
	v_mul_f32_e32 v69, v69, v75
	v_fma_f32 v70, -v70, v82, s33
	v_rcp_f32_e32 v67, v67
	v_exp_f32_e32 v69, v69
	v_mul_f32_e32 v70, v70, v82
	v_exp_f32_e32 v70, v70
	v_mul_f32_e32 v66, v79, v79
	v_mul_f32_e32 v77, v67, v74
	v_add_f32_e32 v67, 1.0, v69
	v_fmac_f32_e32 v66, v81, v81
	v_rcp_f32_e32 v67, v67
	v_add_f32_e32 v69, 1.0, v70
	v_fmac_f32_e32 v66, v80, v80
	v_rcp_f32_e32 v69, v69
	v_and_b32_e32 v62, 64, v249
	v_fmac_f32_e32 v66, v78, v78
	v_add_u32_e32 v62, 64, v62
	v_xor_b32_e32 v63, 32, v249
	v_fmac_f32_e32 v66, v76, v76
	v_cmp_lt_i32_e32 vcc, v63, v62
	v_fmac_f32_e32 v66, v77, v77
	v_mul_f32_e32 v75, v67, v75
	v_cndmask_b32_e32 v63, v249, v63, vcc
	v_fmac_f32_e32 v66, v75, v75
	v_mul_f32_e32 v74, v69, v82
	v_lshlrev_b32_e32 v68, 2, v63
	v_fmac_f32_e32 v66, v74, v74
	v_mov_b32_e32 v67, v66
	s_nop 1
	v_permlane32_swap_b32_e32 v67, v66
	v_xor_b32_e32 v63, 16, v249
	v_cmp_lt_i32_e32 vcc, v63, v62
	v_and_b32_e32 v84, 0x78, v105
	v_readlane_b32 s2, v253, 40
	v_cndmask_b32_e32 v63, v249, v63, vcc
	v_lshlrev_b32_e32 v69, 2, v63
	s_waitcnt lgkmcnt(0)
	v_add_f32_e32 v66, v66, v67
	v_mov_b32_e32 v67, v66
	s_nop 1
	v_permlane16_swap_b32_e32 v67, v66
	v_xor_b32_e32 v63, 8, v249
	v_cmp_lt_i32_e32 vcc, v63, v62
	v_lshlrev_b32_e32 v206, 2, v84
	v_readlane_b32 s45, v251, 17
	v_cndmask_b32_e32 v63, v249, v63, vcc
	v_lshlrev_b32_e32 v70, 2, v63
	s_waitcnt lgkmcnt(0)
	v_add_f32_e32 v66, v66, v67
	s_nop 1
	v_mov_b32_dpp v67, v66 row_ror:8 row_mask:0xf bank_mask:0xf
	v_xor_b32_e32 v63, 4, v249
	v_cmp_lt_i32_e32 vcc, v63, v62
	v_readlane_b32 s46, v251, 18
	v_readlane_b32 s47, v251, 19
	v_cndmask_b32_e32 v63, v249, v63, vcc
	v_lshlrev_b32_e32 v71, 2, v63
	s_waitcnt lgkmcnt(0)
	v_add_f32_e32 v66, v66, v67
	v_xor_b32_e32 v63, 2, v249
	s_nop 1
	v_mov_b32_dpp v67, v66 row_shl:4 row_mask:0xf bank_mask:0x5
	v_mov_b32_dpp v67, v66 row_shr:4 row_mask:0xf bank_mask:0xa
	v_cmp_lt_i32_e32 vcc, v63, v62
	v_readlane_b32 s56, v251, 28
	v_readlane_b32 s57, v251, 29
	v_cndmask_b32_e32 v63, v249, v63, vcc
	v_lshlrev_b32_e32 v72, 2, v63
	v_xor_b32_e32 v63, 1, v249
	v_cmp_lt_i32_e32 vcc, v63, v62
	v_readlane_b32 s58, v251, 30
	v_readlane_b32 s59, v251, 31
	v_cndmask_b32_e32 v62, v249, v63, vcc
	s_waitcnt lgkmcnt(0)
	v_add_f32_e32 v63, v66, v67
	s_nop 1
	v_mov_b32_dpp v67, v63 quad_perm:[2,3,0,1] row_mask:0xf bank_mask:0xf
	v_lshlrev_b32_e32 v73, 2, v62
	v_bfe_u32 v66, v64, 4, 2
	v_cmp_eq_u32_e32 vcc, s2, v66
	s_mov_b64 s[16:17], s[52:53]
	s_waitcnt lgkmcnt(0)
	v_add_f32_e32 v82, v63, v67
	s_nop 1
	v_mov_b32_dpp v83, v82 quad_perm:[1,0,3,2] row_mask:0xf bank_mask:0xf
	v_lshl_add_u32 v67, v103, 5, 0
	v_lshl_add_u64 v[62:63], s[0:1], 0, v[206:207]
	v_mad_u32_u24 v67, v84, s13, v67
	v_lshrrev_b32_e32 v170, 6, v0
	v_lshlrev_b32_e32 v170, 1, v170
	v_and_b32_e32 v171, 15, v0
	v_xor_b32_e32 v168, v170, v171
	v_sub_u32_e32 v168, v168, v170
	v_lshl_add_u32 v168, v168, 4, v67
	v_or_b32_e32 v170, 1, v170
	v_xor_b32_e32 v169, v170, v171
	v_sub_u32_e32 v169, v169, v170
	v_lshl_add_u32 v169, v169, 4, v67
	s_mov_b64 s[18:19], s[54:55]
	s_and_saveexec_b64 s[0:1], vcc
	s_cbranch_execz .LBB0_1262
; __device__ __forceinline__ float bflo(unsigned w) { return __uint_as_float(w << 16); }
; __device__ __forceinline__ float bfhi(unsigned w) { return __uint_as_float(w & 0xffff0000u); }
; __device__ __forceinline__ unsigned short f2bf(float f) { return (unsigned short)(cvt_pk_bf16(f, 0.f) & 0xffffu); }
; __device__ __forceinline__ void sgu_unit(const Params& p, int l, int un, LAS unsigned char* lds) {
;     ...
;     for (int qi = 0; qi < 16; ++qi) { const int q = wave * 16 + qi;
;         const u32x4 v = vv[qi]; float f[8] = {bflo(v.x), bfhi(v.x), bflo(v.y), bfhi(v.y), bflo(v.z), bfhi(v.z), bflo(v.w), bfhi(v.w)}; float ss = 0.f;
; #pragma unroll
;         for (int j = 0; j < 8; ++j) { f[j] = gelu_tanh(f[j]); ss += f[j] * f[j]; }
;         ss = wave_sum(ss); const float rinv = rsqrtf(ss * (1.0f / 512.0f) + EPS);
;         if ((lane >> 4) == h) { const int c0 = (lane & 15) * 8; const float* g = p.in[I_SGUNG] + l * 512 + h * 128 + c0;
; #pragma unroll
;             for (int j = 0; j < 8; ++j) Vl[(c0 + j) * 136 + q] = f2bf(f[j] * rinv * g[j]); } }
	s_waitcnt lgkmcnt(0)
	v_add_f32_e32 v82, v82, v83
	v_fmamk_f32 v82, v82, 0x3b000000, v246
	s_mov_b32 s2, 0x800000
	v_cmp_gt_f32_e64 s[2:3], s2, v82
	v_mul_f32_e32 v83, 0x4b800000, v82
	s_nop 0
	v_cndmask_b32_e64 v82, v82, v83, s[2:3]
	v_rsq_f32_e32 v82, v82
	s_nop 0
	v_mul_f32_e32 v83, 0x45800000, v82
	v_cndmask_b32_e64 v90, v82, v83, s[2:3]
	global_load_dwordx4 v[82:85], v[62:63], off offset:16
	global_load_dwordx4 v[86:89], v[62:63], off
	v_mul_f32_e32 v79, v79, v90
	v_mul_f32_e32 v76, v76, v90
	v_mul_f32_e32 v81, v81, v90
	v_mul_f32_e32 v78, v78, v90
	v_mul_f32_e32 v75, v75, v90
	v_mul_f32_e32 v74, v74, v90
	s_waitcnt vmcnt(1)
	v_mul_f32_e32 v76, v76, v82
	s_waitcnt vmcnt(0)
	v_mov_b32_e32 v160, v86
	v_mov_b32_e32 v161, v87
	v_mov_b32_e32 v162, v88
	v_mov_b32_e32 v163, v89
	v_mov_b32_e32 v164, v82
	v_mov_b32_e32 v165, v83
	v_mov_b32_e32 v166, v84
	v_mov_b32_e32 v167, v85
	v_mul_f32_e32 v79, v79, v87
	v_cvt_pk_bf16_f32 v79, v79, s0
	v_cvt_pk_bf16_f32 v76, v76, s0
	ds_write_b16 v168, v79 offset:35088
	v_mul_f32_e32 v79, v80, v90
	ds_write_b16 v168, v76 offset:35904
	v_mul_f32_e32 v76, v77, v90
	v_mul_f32_e32 v81, v81, v86
	v_mul_f32_e32 v79, v79, v88
	v_mul_f32_e32 v78, v78, v89
	v_mul_f32_e32 v76, v76, v83
	v_mul_f32_e32 v75, v75, v84
	v_mul_f32_e32 v74, v74, v85
	v_cvt_pk_bf16_f32 v81, v81, s0
	v_cvt_pk_bf16_f32 v79, v79, s0
	v_cvt_pk_bf16_f32 v78, v78, s0
	v_cvt_pk_bf16_f32 v76, v76, s0
	v_cvt_pk_bf16_f32 v75, v75, s0
	v_cvt_pk_bf16_f32 v74, v74, s0
	ds_write_b16 v168, v81 offset:34816
	ds_write_b16 v168, v79 offset:35360
	ds_write_b16 v168, v78 offset:35632
	ds_write_b16 v168, v76 offset:36176
	ds_write_b16 v168, v75 offset:36448
	ds_write_b16 v168, v74 offset:36720
.LBB0_1262:
	s_or_b64 exec, exec, s[0:1]
	s_waitcnt vmcnt(14)
	v_lshlrev_b32_e32 v74, 16, v58
	v_lshlrev_b32_e32 v75, 16, v59
	v_and_b32_e32 v77, 0xffff0000, v59
	v_mul_f32_e32 v59, 0x3dd2d3e8, v74
	v_fma_f32 v59, -v59, v74, s33
	v_mul_f32_e32 v59, v59, v74
	v_exp_f32_e32 v59, v59
	v_and_b32_e32 v58, 0xffff0000, v58
	v_lshlrev_b32_e32 v78, 16, v60
	v_and_b32_e32 v79, 0xffff0000, v60
	v_add_f32_e32 v59, 1.0, v59
	v_rcp_f32_e32 v59, v59
	v_mul_f32_e32 v60, 0x3dd2d3e8, v77
	v_fma_f32 v60, -v60, v77, s33
	v_mul_f32_e32 v60, v60, v77
	v_mul_f32_e32 v76, v59, v74
	v_mul_f32_e32 v59, 0x3dd2d3e8, v58
	v_fma_f32 v59, -v59, v58, s33
	v_mul_f32_e32 v59, v59, v58
	v_exp_f32_e32 v59, v59
	v_exp_f32_e32 v60, v60
	v_lshlrev_b32_e32 v80, 16, v61
	v_and_b32_e32 v81, 0xffff0000, v61
	v_add_f32_e32 v59, 1.0, v59
	v_rcp_f32_e32 v59, v59
	v_add_f32_e32 v60, 1.0, v60
	v_rcp_f32_e32 v60, v60
	v_mul_f32_e32 v61, 0x3dd2d3e8, v78
	v_mul_f32_e32 v59, v59, v58
	v_mul_f32_e32 v58, 0x3dd2d3e8, v75
	v_fma_f32 v58, -v58, v75, s33
	v_mul_f32_e32 v58, v58, v75
	v_exp_f32_e32 v58, v58
	v_fma_f32 v61, -v61, v78, s33
	v_mul_f32_e32 v74, 0x3dd2d3e8, v79
	v_mul_f32_e32 v61, v61, v78
	v_add_f32_e32 v58, 1.0, v58
	v_rcp_f32_e32 v58, v58
	v_fma_f32 v74, -v74, v79, s33
	v_mul_f32_e32 v60, v60, v77
	v_exp_f32_e32 v61, v61
	v_mul_f32_e32 v58, v58, v75
	v_mul_f32_e32 v75, 0x3dd2d3e8, v80
	v_mul_f32_e32 v74, v74, v79
	v_fma_f32 v75, -v75, v80, s33
	v_mul_f32_e32 v77, 0x3dd2d3e8, v81
	v_exp_f32_e32 v74, v74
	v_mul_f32_e32 v75, v75, v80
	v_fma_f32 v77, -v77, v81, s33
	v_exp_f32_e32 v75, v75
	v_mul_f32_e32 v77, v77, v81
	v_exp_f32_e32 v77, v77
	v_add_f32_e32 v61, 1.0, v61
	v_rcp_f32_e32 v61, v61
	v_add_f32_e32 v74, 1.0, v74
	v_mul_f32_e32 v82, v59, v59
	v_rcp_f32_e32 v74, v74
	v_add_f32_e32 v75, 1.0, v75
	v_fmac_f32_e32 v82, v76, v76
	v_rcp_f32_e32 v75, v75
	v_add_f32_e32 v77, 1.0, v77
	v_fmac_f32_e32 v82, v58, v58
	v_rcp_f32_e32 v77, v77
	v_fmac_f32_e32 v82, v60, v60
	v_mul_f32_e32 v61, v61, v78
	v_fmac_f32_e32 v82, v61, v61
	v_mul_f32_e32 v74, v74, v79
	v_fmac_f32_e32 v82, v74, v74
	v_mul_f32_e32 v75, v75, v80
	v_fmac_f32_e32 v82, v75, v75
	v_mul_f32_e32 v77, v77, v81
	v_fmac_f32_e32 v82, v77, v77
	ds_bpermute_b32 v78, v68, v82
	s_waitcnt lgkmcnt(0)
	v_add_f32_e32 v78, v82, v78
	v_mov_b32_e32 v79, v78
	s_nop 1
	v_permlane16_swap_b32_e32 v79, v78
	s_waitcnt lgkmcnt(0)
	v_add_f32_e32 v78, v78, v79
	s_nop 1
	v_mov_b32_dpp v79, v78 row_ror:8 row_mask:0xf bank_mask:0xf
	s_waitcnt lgkmcnt(0)
	v_add_f32_e32 v78, v78, v79
	s_nop 1
	v_mov_b32_dpp v79, v78 row_shl:4 row_mask:0xf bank_mask:0x5
	v_mov_b32_dpp v79, v78 row_shr:4 row_mask:0xf bank_mask:0xa
	s_waitcnt lgkmcnt(0)
	v_add_f32_e32 v78, v78, v79
	s_nop 1
	v_mov_b32_dpp v79, v78 quad_perm:[2,3,0,1] row_mask:0xf bank_mask:0xf
	s_waitcnt lgkmcnt(0)
	v_add_f32_e32 v78, v78, v79
	s_nop 1
	v_mov_b32_dpp v79, v78 quad_perm:[1,0,3,2] row_mask:0xf bank_mask:0xf
	s_and_saveexec_b64 s[0:1], vcc
	s_cbranch_execz .LBB0_1264
	s_waitcnt lgkmcnt(0)
	v_add_f32_e32 v78, v78, v79
	v_fmamk_f32 v78, v78, 0x3b000000, v246
	s_mov_b32 s2, 0x800000
	v_cmp_gt_f32_e64 s[2:3], s2, v78
	v_mul_f32_e32 v79, 0x4b800000, v78
	s_nop 0
	v_cndmask_b32_e64 v78, v78, v79, s[2:3]
	v_rsq_f32_e32 v78, v78
	s_nop 0
	v_mul_f32_e32 v79, 0x45800000, v78
	v_cndmask_b32_e64 v86, v78, v79, s[2:3]
	v_mul_f32_e32 v58, v58, v86
	v_mul_f32_e32 v76, v76, v86
	v_mul_f32_e32 v59, v59, v86
	v_mul_f32_e32 v58, v58, v162
	v_cvt_pk_bf16_f32 v58, v58, s0
	ds_write_b16 v168, v58 offset:35362
	v_mul_f32_e32 v58, v60, v86
	v_mul_f32_e32 v58, v58, v163
	v_cvt_pk_bf16_f32 v58, v58, s0
	ds_write_b16 v168, v58 offset:35634
	v_mul_f32_e32 v58, v61, v86
	v_mul_f32_e32 v58, v58, v164
	v_cvt_pk_bf16_f32 v58, v58, s0
	ds_write_b16 v168, v58 offset:35906
	v_mul_f32_e32 v58, v74, v86
	v_mul_f32_e32 v58, v58, v165
	v_cvt_pk_bf16_f32 v58, v58, s0
	ds_write_b16 v168, v58 offset:36178
	v_mul_f32_e32 v58, v75, v86
	v_mul_f32_e32 v58, v58, v166
	v_cvt_pk_bf16_f32 v58, v58, s0
	ds_write_b16 v168, v58 offset:36450
	v_mul_f32_e32 v58, v77, v86
	v_mul_f32_e32 v76, v76, v160
	v_mul_f32_e32 v59, v59, v161
	v_mul_f32_e32 v58, v58, v167
	v_cvt_pk_bf16_f32 v76, v76, s0
	v_cvt_pk_bf16_f32 v59, v59, s0
	v_cvt_pk_bf16_f32 v58, v58, s0
	ds_write_b16 v168, v76 offset:34818
	ds_write_b16 v168, v59 offset:35090
	ds_write_b16 v168, v58 offset:36722
; __device__ __forceinline__ float bflo(unsigned w) { return __uint_as_float(w << 16); }
; __device__ __forceinline__ float bfhi(unsigned w) { return __uint_as_float(w & 0xffff0000u); }
; __device__ __forceinline__ unsigned short f2bf(float f) { return (unsigned short)(cvt_pk_bf16(f, 0.f) & 0xffffu); }
; __device__ __forceinline__ void sgu_unit(const Params& p, int l, int un, LAS unsigned char* lds) {
;     ...
;     for (int qi = 0; qi < 16; ++qi) { const int q = wave * 16 + qi;
;         const u32x4 v = vv[qi]; float f[8] = {bflo(v.x), bfhi(v.x), bflo(v.y), bfhi(v.y), bflo(v.z), bfhi(v.z), bflo(v.w), bfhi(v.w)}; float ss = 0.f;
; #pragma unroll
;         for (int j = 0; j < 8; ++j) { f[j] = gelu_tanh(f[j]); ss += f[j] * f[j]; }
;         ss = wave_sum(ss); const float rinv = rsqrtf(ss * (1.0f / 512.0f) + EPS);
;         if ((lane >> 4) == h) { const int c0 = (lane & 15) * 8; const float* g = p.in[I_SGUNG] + l * 512 + h * 128 + c0;
; #pragma unroll
;             for (int j = 0; j < 8; ++j) Vl[(c0 + j) * 136 + q] = f2bf(f[j] * rinv * g[j]); } }
.LBB0_1264:
	s_or_b64 exec, exec, s[0:1]
	s_waitcnt vmcnt(13)
	v_lshlrev_b32_e32 v58, 16, v54
	v_lshlrev_b32_e32 v59, 16, v55
	v_and_b32_e32 v61, 0xffff0000, v55
	v_mul_f32_e32 v55, 0x3dd2d3e8, v58
	v_fma_f32 v55, -v55, v58, s33
	v_mul_f32_e32 v55, v55, v58
	v_exp_f32_e32 v55, v55
	v_and_b32_e32 v54, 0xffff0000, v54
	v_lshlrev_b32_e32 v74, 16, v56
	v_and_b32_e32 v75, 0xffff0000, v56
	v_add_f32_e32 v55, 1.0, v55
	v_rcp_f32_e32 v55, v55
	v_mul_f32_e32 v56, 0x3dd2d3e8, v61
	v_fma_f32 v56, -v56, v61, s33
	v_mul_f32_e32 v56, v56, v61
	v_mul_f32_e32 v60, v55, v58
	v_mul_f32_e32 v55, 0x3dd2d3e8, v54
	v_fma_f32 v55, -v55, v54, s33
	v_mul_f32_e32 v55, v55, v54
	v_exp_f32_e32 v55, v55
	v_exp_f32_e32 v56, v56
	v_lshlrev_b32_e32 v76, 16, v57
	v_and_b32_e32 v77, 0xffff0000, v57
	v_add_f32_e32 v55, 1.0, v55
	v_rcp_f32_e32 v55, v55
	v_add_f32_e32 v56, 1.0, v56
	v_rcp_f32_e32 v56, v56
	v_mul_f32_e32 v57, 0x3dd2d3e8, v74
	v_mul_f32_e32 v55, v55, v54
	v_mul_f32_e32 v54, 0x3dd2d3e8, v59
	v_fma_f32 v54, -v54, v59, s33
	v_mul_f32_e32 v54, v54, v59
	v_exp_f32_e32 v54, v54
	v_fma_f32 v57, -v57, v74, s33
	v_mul_f32_e32 v58, 0x3dd2d3e8, v75
	v_mul_f32_e32 v57, v57, v74
	v_add_f32_e32 v54, 1.0, v54
	v_rcp_f32_e32 v54, v54
	v_fma_f32 v58, -v58, v75, s33
	v_mul_f32_e32 v56, v56, v61
	v_exp_f32_e32 v57, v57
	v_mul_f32_e32 v54, v54, v59
	v_mul_f32_e32 v59, 0x3dd2d3e8, v76
	v_mul_f32_e32 v58, v58, v75
	v_fma_f32 v59, -v59, v76, s33
	v_mul_f32_e32 v61, 0x3dd2d3e8, v77
	v_exp_f32_e32 v58, v58
	v_mul_f32_e32 v59, v59, v76
	v_fma_f32 v61, -v61, v77, s33
	v_exp_f32_e32 v59, v59
	v_mul_f32_e32 v61, v61, v77
	v_exp_f32_e32 v61, v61
	v_add_f32_e32 v57, 1.0, v57
	v_rcp_f32_e32 v57, v57
	v_add_f32_e32 v58, 1.0, v58
	v_mul_f32_e32 v78, v55, v55
	v_rcp_f32_e32 v58, v58
	v_add_f32_e32 v59, 1.0, v59
	v_fmac_f32_e32 v78, v60, v60
	v_rcp_f32_e32 v59, v59
	v_add_f32_e32 v61, 1.0, v61
	v_fmac_f32_e32 v78, v54, v54
	v_rcp_f32_e32 v61, v61
	v_fmac_f32_e32 v78, v56, v56
	v_mul_f32_e32 v57, v57, v74
	v_fmac_f32_e32 v78, v57, v57
	v_mul_f32_e32 v58, v58, v75
	v_fmac_f32_e32 v78, v58, v58
	v_mul_f32_e32 v59, v59, v76
	v_fmac_f32_e32 v78, v59, v59
	v_mul_f32_e32 v61, v61, v77
	v_fmac_f32_e32 v78, v61, v61
	ds_bpermute_b32 v74, v68, v78
	s_waitcnt lgkmcnt(0)
	v_add_f32_e32 v74, v78, v74
	v_mov_b32_e32 v75, v74
	s_nop 1
	v_permlane16_swap_b32_e32 v75, v74
	s_waitcnt lgkmcnt(0)
	v_add_f32_e32 v74, v74, v75
	s_nop 1
	v_mov_b32_dpp v75, v74 row_ror:8 row_mask:0xf bank_mask:0xf
	s_waitcnt lgkmcnt(0)
	v_add_f32_e32 v74, v74, v75
	s_nop 1
	v_mov_b32_dpp v75, v74 row_shl:4 row_mask:0xf bank_mask:0x5
	v_mov_b32_dpp v75, v74 row_shr:4 row_mask:0xf bank_mask:0xa
	s_waitcnt lgkmcnt(0)
	v_add_f32_e32 v74, v74, v75
	s_nop 1
	v_mov_b32_dpp v75, v74 quad_perm:[2,3,0,1] row_mask:0xf bank_mask:0xf
	s_waitcnt lgkmcnt(0)
	v_add_f32_e32 v74, v74, v75
	s_nop 1
	v_mov_b32_dpp v75, v74 quad_perm:[1,0,3,2] row_mask:0xf bank_mask:0xf
	s_and_saveexec_b64 s[0:1], vcc
	s_cbranch_execz .LBB0_1266
	s_waitcnt lgkmcnt(0)
	v_add_f32_e32 v74, v74, v75
	v_fmamk_f32 v74, v74, 0x3b000000, v246
	s_mov_b32 s2, 0x800000
	v_cmp_gt_f32_e64 s[2:3], s2, v74
	v_mul_f32_e32 v75, 0x4b800000, v74
	s_nop 0
	v_cndmask_b32_e64 v74, v74, v75, s[2:3]
	v_rsq_f32_e32 v74, v74
	s_nop 0
	v_mul_f32_e32 v75, 0x45800000, v74
	v_cndmask_b32_e64 v82, v74, v75, s[2:3]
	v_mul_f32_e32 v54, v54, v82
	v_mul_f32_e32 v60, v60, v82
	v_mul_f32_e32 v55, v55, v82
	v_mul_f32_e32 v54, v54, v162
	v_cvt_pk_bf16_f32 v54, v54, s0
	ds_write_b16 v168, v54 offset:35364
	v_mul_f32_e32 v54, v56, v82
	v_mul_f32_e32 v54, v54, v163
	v_cvt_pk_bf16_f32 v54, v54, s0
	ds_write_b16 v168, v54 offset:35636
	v_mul_f32_e32 v54, v57, v82
	v_mul_f32_e32 v54, v54, v164
	v_cvt_pk_bf16_f32 v54, v54, s0
	ds_write_b16 v168, v54 offset:35908
	v_mul_f32_e32 v54, v58, v82
	v_mul_f32_e32 v54, v54, v165
	v_cvt_pk_bf16_f32 v54, v54, s0
	ds_write_b16 v168, v54 offset:36180
	v_mul_f32_e32 v54, v59, v82
	v_mul_f32_e32 v54, v54, v166
	v_cvt_pk_bf16_f32 v54, v54, s0
	ds_write_b16 v168, v54 offset:36452
	v_mul_f32_e32 v54, v61, v82
	v_mul_f32_e32 v60, v60, v160
	v_mul_f32_e32 v55, v55, v161
	v_mul_f32_e32 v54, v54, v167
	v_cvt_pk_bf16_f32 v60, v60, s0
	v_cvt_pk_bf16_f32 v55, v55, s0
	v_cvt_pk_bf16_f32 v54, v54, s0
	ds_write_b16 v168, v60 offset:34820
	ds_write_b16 v168, v55 offset:35092
	ds_write_b16 v168, v54 offset:36724
; __device__ __forceinline__ float bflo(unsigned w) { return __uint_as_float(w << 16); }
; __device__ __forceinline__ float bfhi(unsigned w) { return __uint_as_float(w & 0xffff0000u); }
; __device__ __forceinline__ unsigned short f2bf(float f) { return (unsigned short)(cvt_pk_bf16(f, 0.f) & 0xffffu); }
; __device__ __forceinline__ void sgu_unit(const Params& p, int l, int un, LAS unsigned char* lds) {
;     ...
;     for (int qi = 0; qi < 16; ++qi) { const int q = wave * 16 + qi;
;         const u32x4 v = vv[qi]; float f[8] = {bflo(v.x), bfhi(v.x), bflo(v.y), bfhi(v.y), bflo(v.z), bfhi(v.z), bflo(v.w), bfhi(v.w)}; float ss = 0.f;
; #pragma unroll
;         for (int j = 0; j < 8; ++j) { f[j] = gelu_tanh(f[j]); ss += f[j] * f[j]; }
;         ss = wave_sum(ss); const float rinv = rsqrtf(ss * (1.0f / 512.0f) + EPS);
;         if ((lane >> 4) == h) { const int c0 = (lane & 15) * 8; const float* g = p.in[I_SGUNG] + l * 512 + h * 128 + c0;
; #pragma unroll
;             for (int j = 0; j < 8; ++j) Vl[(c0 + j) * 136 + q] = f2bf(f[j] * rinv * g[j]); } }
.LBB0_1266:
	s_or_b64 exec, exec, s[0:1]
	s_waitcnt vmcnt(12)
	v_lshlrev_b32_e32 v54, 16, v50
	v_lshlrev_b32_e32 v55, 16, v51
	v_and_b32_e32 v57, 0xffff0000, v51
	v_mul_f32_e32 v51, 0x3dd2d3e8, v54
	v_fma_f32 v51, -v51, v54, s33
	v_mul_f32_e32 v51, v51, v54
	v_exp_f32_e32 v51, v51
	v_and_b32_e32 v50, 0xffff0000, v50
	v_lshlrev_b32_e32 v58, 16, v52
	v_and_b32_e32 v59, 0xffff0000, v52
	v_add_f32_e32 v51, 1.0, v51
	v_rcp_f32_e32 v51, v51
	v_mul_f32_e32 v52, 0x3dd2d3e8, v57
	v_fma_f32 v52, -v52, v57, s33
	v_mul_f32_e32 v52, v52, v57
	v_mul_f32_e32 v56, v51, v54
	v_mul_f32_e32 v51, 0x3dd2d3e8, v50
	v_fma_f32 v51, -v51, v50, s33
	v_mul_f32_e32 v51, v51, v50
	v_exp_f32_e32 v51, v51
	v_exp_f32_e32 v52, v52
	v_lshlrev_b32_e32 v60, 16, v53
	v_and_b32_e32 v61, 0xffff0000, v53
	v_add_f32_e32 v51, 1.0, v51
	v_rcp_f32_e32 v51, v51
	v_add_f32_e32 v52, 1.0, v52
	v_rcp_f32_e32 v52, v52
	v_mul_f32_e32 v53, 0x3dd2d3e8, v58
	v_mul_f32_e32 v51, v51, v50
	v_mul_f32_e32 v50, 0x3dd2d3e8, v55
	v_fma_f32 v50, -v50, v55, s33
	v_mul_f32_e32 v50, v50, v55
	v_exp_f32_e32 v50, v50
	v_fma_f32 v53, -v53, v58, s33
	v_mul_f32_e32 v54, 0x3dd2d3e8, v59
	v_mul_f32_e32 v53, v53, v58
	v_add_f32_e32 v50, 1.0, v50
	v_rcp_f32_e32 v50, v50
	v_fma_f32 v54, -v54, v59, s33
	v_mul_f32_e32 v52, v52, v57
	v_exp_f32_e32 v53, v53
	v_mul_f32_e32 v50, v50, v55
	v_mul_f32_e32 v55, 0x3dd2d3e8, v60
	v_mul_f32_e32 v54, v54, v59
	v_fma_f32 v55, -v55, v60, s33
	v_mul_f32_e32 v57, 0x3dd2d3e8, v61
	v_exp_f32_e32 v54, v54
	v_mul_f32_e32 v55, v55, v60
	v_fma_f32 v57, -v57, v61, s33
	v_exp_f32_e32 v55, v55
	v_mul_f32_e32 v57, v57, v61
	v_exp_f32_e32 v57, v57
	v_add_f32_e32 v53, 1.0, v53
	v_rcp_f32_e32 v53, v53
	v_add_f32_e32 v54, 1.0, v54
	v_mul_f32_e32 v74, v51, v51
	v_rcp_f32_e32 v54, v54
	v_add_f32_e32 v55, 1.0, v55
	v_fmac_f32_e32 v74, v56, v56
	v_rcp_f32_e32 v55, v55
	v_add_f32_e32 v57, 1.0, v57
	v_fmac_f32_e32 v74, v50, v50
	v_rcp_f32_e32 v57, v57
	v_fmac_f32_e32 v74, v52, v52
	v_mul_f32_e32 v53, v53, v58
	v_fmac_f32_e32 v74, v53, v53
	v_mul_f32_e32 v54, v54, v59
	v_fmac_f32_e32 v74, v54, v54
	v_mul_f32_e32 v55, v55, v60
	v_fmac_f32_e32 v74, v55, v55
	v_mul_f32_e32 v57, v57, v61
	v_fmac_f32_e32 v74, v57, v57
	ds_bpermute_b32 v58, v68, v74
	s_waitcnt lgkmcnt(0)
	v_add_f32_e32 v58, v74, v58
	v_mov_b32_e32 v59, v58
	s_nop 1
	v_permlane16_swap_b32_e32 v59, v58
	s_waitcnt lgkmcnt(0)
	v_add_f32_e32 v58, v58, v59
	s_nop 1
	v_mov_b32_dpp v59, v58 row_ror:8 row_mask:0xf bank_mask:0xf
	s_waitcnt lgkmcnt(0)
	v_add_f32_e32 v58, v58, v59
	s_nop 1
	v_mov_b32_dpp v59, v58 row_shl:4 row_mask:0xf bank_mask:0x5
	v_mov_b32_dpp v59, v58 row_shr:4 row_mask:0xf bank_mask:0xa
	s_waitcnt lgkmcnt(0)
	v_add_f32_e32 v58, v58, v59
	s_nop 1
	v_mov_b32_dpp v59, v58 quad_perm:[2,3,0,1] row_mask:0xf bank_mask:0xf
	s_waitcnt lgkmcnt(0)
	v_add_f32_e32 v58, v58, v59
	s_nop 1
	v_mov_b32_dpp v59, v58 quad_perm:[1,0,3,2] row_mask:0xf bank_mask:0xf
	s_and_saveexec_b64 s[0:1], vcc
	s_cbranch_execz .LBB0_1268
	s_waitcnt lgkmcnt(0)
	v_add_f32_e32 v58, v58, v59
	v_fmamk_f32 v58, v58, 0x3b000000, v246
	s_mov_b32 s2, 0x800000
	v_cmp_gt_f32_e64 s[2:3], s2, v58
	v_mul_f32_e32 v59, 0x4b800000, v58
	s_nop 0
	v_cndmask_b32_e64 v58, v58, v59, s[2:3]
	v_rsq_f32_e32 v58, v58
	s_nop 0
	v_mul_f32_e32 v59, 0x45800000, v58
	v_cndmask_b32_e64 v78, v58, v59, s[2:3]
	v_mul_f32_e32 v50, v50, v78
	v_mul_f32_e32 v56, v56, v78
	v_mul_f32_e32 v51, v51, v78
	v_mul_f32_e32 v50, v50, v162
	v_cvt_pk_bf16_f32 v50, v50, s0
	ds_write_b16 v168, v50 offset:35366
	v_mul_f32_e32 v50, v52, v78
	v_mul_f32_e32 v50, v50, v163
	v_cvt_pk_bf16_f32 v50, v50, s0
	ds_write_b16 v168, v50 offset:35638
	v_mul_f32_e32 v50, v53, v78
	v_mul_f32_e32 v50, v50, v164
	v_cvt_pk_bf16_f32 v50, v50, s0
	ds_write_b16 v168, v50 offset:35910
	v_mul_f32_e32 v50, v54, v78
	v_mul_f32_e32 v50, v50, v165
	v_cvt_pk_bf16_f32 v50, v50, s0
	ds_write_b16 v168, v50 offset:36182
	v_mul_f32_e32 v50, v55, v78
	v_mul_f32_e32 v50, v50, v166
	v_cvt_pk_bf16_f32 v50, v50, s0
	ds_write_b16 v168, v50 offset:36454
	v_mul_f32_e32 v50, v57, v78
	v_mul_f32_e32 v56, v56, v160
	v_mul_f32_e32 v51, v51, v161
	v_mul_f32_e32 v50, v50, v167
	v_cvt_pk_bf16_f32 v56, v56, s0
	v_cvt_pk_bf16_f32 v51, v51, s0
	v_cvt_pk_bf16_f32 v50, v50, s0
	ds_write_b16 v168, v56 offset:34822
	ds_write_b16 v168, v51 offset:35094
	ds_write_b16 v168, v50 offset:36726
; __device__ __forceinline__ float bflo(unsigned w) { return __uint_as_float(w << 16); }
; __device__ __forceinline__ float bfhi(unsigned w) { return __uint_as_float(w & 0xffff0000u); }
; __device__ __forceinline__ unsigned short f2bf(float f) { return (unsigned short)(cvt_pk_bf16(f, 0.f) & 0xffffu); }
; __device__ __forceinline__ void sgu_unit(const Params& p, int l, int un, LAS unsigned char* lds) {
;     ...
;     for (int qi = 0; qi < 16; ++qi) { const int q = wave * 16 + qi;
;         const u32x4 v = vv[qi]; float f[8] = {bflo(v.x), bfhi(v.x), bflo(v.y), bfhi(v.y), bflo(v.z), bfhi(v.z), bflo(v.w), bfhi(v.w)}; float ss = 0.f;
; #pragma unroll
;         for (int j = 0; j < 8; ++j) { f[j] = gelu_tanh(f[j]); ss += f[j] * f[j]; }
;         ss = wave_sum(ss); const float rinv = rsqrtf(ss * (1.0f / 512.0f) + EPS);
;         if ((lane >> 4) == h) { const int c0 = (lane & 15) * 8; const float* g = p.in[I_SGUNG] + l * 512 + h * 128 + c0;
; #pragma unroll
;             for (int j = 0; j < 8; ++j) Vl[(c0 + j) * 136 + q] = f2bf(f[j] * rinv * g[j]); } }
.LBB0_1268:
	s_or_b64 exec, exec, s[0:1]
	s_waitcnt vmcnt(11)
	v_lshlrev_b32_e32 v50, 16, v46
	v_lshlrev_b32_e32 v51, 16, v47
	v_and_b32_e32 v53, 0xffff0000, v47
	v_mul_f32_e32 v47, 0x3dd2d3e8, v50
	v_fma_f32 v47, -v47, v50, s33
	v_mul_f32_e32 v47, v47, v50
	v_exp_f32_e32 v47, v47
	v_and_b32_e32 v46, 0xffff0000, v46
	v_lshlrev_b32_e32 v54, 16, v48
	v_and_b32_e32 v55, 0xffff0000, v48
	v_add_f32_e32 v47, 1.0, v47
	v_rcp_f32_e32 v47, v47
	v_mul_f32_e32 v48, 0x3dd2d3e8, v53
	v_fma_f32 v48, -v48, v53, s33
	v_mul_f32_e32 v48, v48, v53
	v_mul_f32_e32 v52, v47, v50
	v_mul_f32_e32 v47, 0x3dd2d3e8, v46
	v_fma_f32 v47, -v47, v46, s33
	v_mul_f32_e32 v47, v47, v46
	v_exp_f32_e32 v47, v47
	v_exp_f32_e32 v48, v48
	v_lshlrev_b32_e32 v56, 16, v49
	v_and_b32_e32 v57, 0xffff0000, v49
	v_add_f32_e32 v47, 1.0, v47
	v_rcp_f32_e32 v47, v47
	v_add_f32_e32 v48, 1.0, v48
	v_rcp_f32_e32 v48, v48
	v_mul_f32_e32 v49, 0x3dd2d3e8, v54
	v_mul_f32_e32 v47, v47, v46
	v_mul_f32_e32 v46, 0x3dd2d3e8, v51
	v_fma_f32 v46, -v46, v51, s33
	v_mul_f32_e32 v46, v46, v51
	v_exp_f32_e32 v46, v46
	v_fma_f32 v49, -v49, v54, s33
	v_mul_f32_e32 v50, 0x3dd2d3e8, v55
	v_mul_f32_e32 v49, v49, v54
	v_add_f32_e32 v46, 1.0, v46
	v_rcp_f32_e32 v46, v46
	v_fma_f32 v50, -v50, v55, s33
	v_mul_f32_e32 v48, v48, v53
	v_exp_f32_e32 v49, v49
	v_mul_f32_e32 v46, v46, v51
	v_mul_f32_e32 v51, 0x3dd2d3e8, v56
	v_mul_f32_e32 v50, v50, v55
	v_fma_f32 v51, -v51, v56, s33
	v_mul_f32_e32 v53, 0x3dd2d3e8, v57
	v_exp_f32_e32 v50, v50
	v_mul_f32_e32 v51, v51, v56
	v_fma_f32 v53, -v53, v57, s33
	v_exp_f32_e32 v51, v51
	v_mul_f32_e32 v53, v53, v57
	v_exp_f32_e32 v53, v53
	v_add_f32_e32 v49, 1.0, v49
	v_rcp_f32_e32 v49, v49
	v_add_f32_e32 v50, 1.0, v50
	v_mul_f32_e32 v58, v47, v47
	v_rcp_f32_e32 v50, v50
	v_add_f32_e32 v51, 1.0, v51
	v_fmac_f32_e32 v58, v52, v52
	v_rcp_f32_e32 v51, v51
	v_add_f32_e32 v53, 1.0, v53
	v_fmac_f32_e32 v58, v46, v46
	v_rcp_f32_e32 v53, v53
	v_fmac_f32_e32 v58, v48, v48
	v_mul_f32_e32 v49, v49, v54
	v_fmac_f32_e32 v58, v49, v49
	v_mul_f32_e32 v50, v50, v55
	v_fmac_f32_e32 v58, v50, v50
	v_mul_f32_e32 v51, v51, v56
	v_fmac_f32_e32 v58, v51, v51
	v_mul_f32_e32 v53, v53, v57
	v_fmac_f32_e32 v58, v53, v53
	ds_bpermute_b32 v54, v68, v58
	s_waitcnt lgkmcnt(0)
	v_add_f32_e32 v54, v58, v54
	v_mov_b32_e32 v55, v54
	s_nop 1
	v_permlane16_swap_b32_e32 v55, v54
	s_waitcnt lgkmcnt(0)
	v_add_f32_e32 v54, v54, v55
	s_nop 1
	v_mov_b32_dpp v55, v54 row_ror:8 row_mask:0xf bank_mask:0xf
	s_waitcnt lgkmcnt(0)
	v_add_f32_e32 v54, v54, v55
	s_nop 1
	v_mov_b32_dpp v55, v54 row_shl:4 row_mask:0xf bank_mask:0x5
	v_mov_b32_dpp v55, v54 row_shr:4 row_mask:0xf bank_mask:0xa
	s_waitcnt lgkmcnt(0)
	v_add_f32_e32 v54, v54, v55
	s_nop 1
	v_mov_b32_dpp v55, v54 quad_perm:[2,3,0,1] row_mask:0xf bank_mask:0xf
	s_waitcnt lgkmcnt(0)
	v_add_f32_e32 v54, v54, v55
	s_nop 1
	v_mov_b32_dpp v55, v54 quad_perm:[1,0,3,2] row_mask:0xf bank_mask:0xf
	s_and_saveexec_b64 s[0:1], vcc
	s_cbranch_execz .LBB0_1270
	s_waitcnt lgkmcnt(0)
	v_add_f32_e32 v54, v54, v55
	v_fmamk_f32 v54, v54, 0x3b000000, v246
	s_mov_b32 s2, 0x800000
	v_cmp_gt_f32_e64 s[2:3], s2, v54
	v_mul_f32_e32 v55, 0x4b800000, v54
	s_nop 0
	v_cndmask_b32_e64 v54, v54, v55, s[2:3]
	v_rsq_f32_e32 v54, v54
	s_nop 0
	v_mul_f32_e32 v55, 0x45800000, v54
	v_cndmask_b32_e64 v74, v54, v55, s[2:3]
	v_mul_f32_e32 v46, v46, v74
	v_mul_f32_e32 v52, v52, v74
	v_mul_f32_e32 v47, v47, v74
	v_mul_f32_e32 v46, v46, v162
	v_cvt_pk_bf16_f32 v46, v46, s0
	ds_write_b16 v168, v46 offset:35368
	v_mul_f32_e32 v46, v48, v74
	v_mul_f32_e32 v46, v46, v163
	v_cvt_pk_bf16_f32 v46, v46, s0
	ds_write_b16 v168, v46 offset:35640
	v_mul_f32_e32 v46, v49, v74
	v_mul_f32_e32 v46, v46, v164
	v_cvt_pk_bf16_f32 v46, v46, s0
	ds_write_b16 v168, v46 offset:35912
	v_mul_f32_e32 v46, v50, v74
	v_mul_f32_e32 v46, v46, v165
	v_cvt_pk_bf16_f32 v46, v46, s0
	ds_write_b16 v168, v46 offset:36184
	v_mul_f32_e32 v46, v51, v74
	v_mul_f32_e32 v46, v46, v166
	v_cvt_pk_bf16_f32 v46, v46, s0
	ds_write_b16 v168, v46 offset:36456
	v_mul_f32_e32 v46, v53, v74
	v_mul_f32_e32 v52, v52, v160
	v_mul_f32_e32 v47, v47, v161
	v_mul_f32_e32 v46, v46, v167
	v_cvt_pk_bf16_f32 v52, v52, s0
	v_cvt_pk_bf16_f32 v47, v47, s0
	v_cvt_pk_bf16_f32 v46, v46, s0
	ds_write_b16 v168, v52 offset:34824
	ds_write_b16 v168, v47 offset:35096
	ds_write_b16 v168, v46 offset:36728
; __device__ __forceinline__ float bflo(unsigned w) { return __uint_as_float(w << 16); }
; __device__ __forceinline__ float bfhi(unsigned w) { return __uint_as_float(w & 0xffff0000u); }
; __device__ __forceinline__ unsigned short f2bf(float f) { return (unsigned short)(cvt_pk_bf16(f, 0.f) & 0xffffu); }
; __device__ __forceinline__ void sgu_unit(const Params& p, int l, int un, LAS unsigned char* lds) {
;     ...
;     for (int qi = 0; qi < 16; ++qi) { const int q = wave * 16 + qi;
;         const u32x4 v = vv[qi]; float f[8] = {bflo(v.x), bfhi(v.x), bflo(v.y), bfhi(v.y), bflo(v.z), bfhi(v.z), bflo(v.w), bfhi(v.w)}; float ss = 0.f;
; #pragma unroll
;         for (int j = 0; j < 8; ++j) { f[j] = gelu_tanh(f[j]); ss += f[j] * f[j]; }
;         ss = wave_sum(ss); const float rinv = rsqrtf(ss * (1.0f / 512.0f) + EPS);
;         if ((lane >> 4) == h) { const int c0 = (lane & 15) * 8; const float* g = p.in[I_SGUNG] + l * 512 + h * 128 + c0;
; #pragma unroll
;             for (int j = 0; j < 8; ++j) Vl[(c0 + j) * 136 + q] = f2bf(f[j] * rinv * g[j]); } }
.LBB0_1270:
	s_or_b64 exec, exec, s[0:1]
	s_waitcnt vmcnt(10)
	v_lshlrev_b32_e32 v46, 16, v42
	v_lshlrev_b32_e32 v47, 16, v43
	v_and_b32_e32 v49, 0xffff0000, v43
	v_mul_f32_e32 v43, 0x3dd2d3e8, v46
	v_fma_f32 v43, -v43, v46, s33
	v_mul_f32_e32 v43, v43, v46
	v_exp_f32_e32 v43, v43
	v_and_b32_e32 v42, 0xffff0000, v42
	v_lshlrev_b32_e32 v50, 16, v44
	v_and_b32_e32 v51, 0xffff0000, v44
	v_add_f32_e32 v43, 1.0, v43
	v_rcp_f32_e32 v43, v43
	v_mul_f32_e32 v44, 0x3dd2d3e8, v49
	v_fma_f32 v44, -v44, v49, s33
	v_mul_f32_e32 v44, v44, v49
	v_mul_f32_e32 v48, v43, v46
	v_mul_f32_e32 v43, 0x3dd2d3e8, v42
	v_fma_f32 v43, -v43, v42, s33
	v_mul_f32_e32 v43, v43, v42
	v_exp_f32_e32 v43, v43
	v_exp_f32_e32 v44, v44
	v_lshlrev_b32_e32 v52, 16, v45
	v_and_b32_e32 v53, 0xffff0000, v45
	v_add_f32_e32 v43, 1.0, v43
	v_rcp_f32_e32 v43, v43
	v_add_f32_e32 v44, 1.0, v44
	v_rcp_f32_e32 v44, v44
	v_mul_f32_e32 v45, 0x3dd2d3e8, v50
	v_mul_f32_e32 v43, v43, v42
	v_mul_f32_e32 v42, 0x3dd2d3e8, v47
	v_fma_f32 v42, -v42, v47, s33
	v_mul_f32_e32 v42, v42, v47
	v_exp_f32_e32 v42, v42
	v_fma_f32 v45, -v45, v50, s33
	v_mul_f32_e32 v46, 0x3dd2d3e8, v51
	v_mul_f32_e32 v45, v45, v50
	v_add_f32_e32 v42, 1.0, v42
	v_rcp_f32_e32 v42, v42
	v_fma_f32 v46, -v46, v51, s33
	v_mul_f32_e32 v44, v44, v49
	v_exp_f32_e32 v45, v45
	v_mul_f32_e32 v42, v42, v47
	v_mul_f32_e32 v47, 0x3dd2d3e8, v52
	v_mul_f32_e32 v46, v46, v51
	v_fma_f32 v47, -v47, v52, s33
	v_mul_f32_e32 v49, 0x3dd2d3e8, v53
	v_exp_f32_e32 v46, v46
	v_mul_f32_e32 v47, v47, v52
	v_fma_f32 v49, -v49, v53, s33
	v_exp_f32_e32 v47, v47
	v_mul_f32_e32 v49, v49, v53
	v_exp_f32_e32 v49, v49
	v_add_f32_e32 v45, 1.0, v45
	v_rcp_f32_e32 v45, v45
	v_add_f32_e32 v46, 1.0, v46
	v_mul_f32_e32 v54, v43, v43
	v_rcp_f32_e32 v46, v46
	v_add_f32_e32 v47, 1.0, v47
	v_fmac_f32_e32 v54, v48, v48
	v_rcp_f32_e32 v47, v47
	v_add_f32_e32 v49, 1.0, v49
	v_fmac_f32_e32 v54, v42, v42
	v_rcp_f32_e32 v49, v49
	v_fmac_f32_e32 v54, v44, v44
	v_mul_f32_e32 v45, v45, v50
	v_fmac_f32_e32 v54, v45, v45
	v_mul_f32_e32 v46, v46, v51
	v_fmac_f32_e32 v54, v46, v46
	v_mul_f32_e32 v47, v47, v52
	v_fmac_f32_e32 v54, v47, v47
	v_mul_f32_e32 v49, v49, v53
	v_fmac_f32_e32 v54, v49, v49
	v_mov_b32_e32 v50, v54
	s_nop 1
	v_permlane32_swap_b32_e32 v50, v54
	s_waitcnt lgkmcnt(0)
	v_add_f32_e32 v50, v54, v50
	v_mov_b32_e32 v51, v50
	s_nop 1
	v_permlane16_swap_b32_e32 v51, v50
	s_waitcnt lgkmcnt(0)
	v_add_f32_e32 v50, v50, v51
	s_nop 1
	v_mov_b32_dpp v51, v50 row_ror:8 row_mask:0xf bank_mask:0xf
	s_waitcnt lgkmcnt(0)
	v_add_f32_e32 v50, v50, v51
	s_nop 1
	v_mov_b32_dpp v51, v50 row_shl:4 row_mask:0xf bank_mask:0x5
	v_mov_b32_dpp v51, v50 row_shr:4 row_mask:0xf bank_mask:0xa
	s_waitcnt lgkmcnt(0)
	v_add_f32_e32 v50, v50, v51
	s_nop 1
	v_mov_b32_dpp v51, v50 quad_perm:[2,3,0,1] row_mask:0xf bank_mask:0xf
	s_waitcnt lgkmcnt(0)
	v_add_f32_e32 v50, v50, v51
	s_nop 1
	v_mov_b32_dpp v51, v50 quad_perm:[1,0,3,2] row_mask:0xf bank_mask:0xf
	s_and_saveexec_b64 s[0:1], vcc
	s_cbranch_execz .LBB0_1272
	s_waitcnt lgkmcnt(0)
	v_add_f32_e32 v50, v50, v51
	v_fmamk_f32 v50, v50, 0x3b000000, v246
	s_mov_b32 s2, 0x800000
	v_cmp_gt_f32_e64 s[2:3], s2, v50
	v_mul_f32_e32 v51, 0x4b800000, v50
	s_nop 0
	v_cndmask_b32_e64 v50, v50, v51, s[2:3]
	v_rsq_f32_e32 v50, v50
	s_nop 0
	v_mul_f32_e32 v51, 0x45800000, v50
	v_cndmask_b32_e64 v58, v50, v51, s[2:3]
	v_mul_f32_e32 v42, v42, v58
	v_mul_f32_e32 v48, v48, v58
	v_mul_f32_e32 v43, v43, v58
	v_mul_f32_e32 v42, v42, v162
	v_cvt_pk_bf16_f32 v42, v42, s0
	ds_write_b16 v168, v42 offset:35370
	v_mul_f32_e32 v42, v44, v58
	v_mul_f32_e32 v42, v42, v163
	v_cvt_pk_bf16_f32 v42, v42, s0
	ds_write_b16 v168, v42 offset:35642
	v_mul_f32_e32 v42, v45, v58
	v_mul_f32_e32 v42, v42, v164
	v_cvt_pk_bf16_f32 v42, v42, s0
	ds_write_b16 v168, v42 offset:35914
	v_mul_f32_e32 v42, v46, v58
	v_mul_f32_e32 v42, v42, v165
	v_cvt_pk_bf16_f32 v42, v42, s0
	ds_write_b16 v168, v42 offset:36186
	v_mul_f32_e32 v42, v47, v58
	v_mul_f32_e32 v42, v42, v166
	v_cvt_pk_bf16_f32 v42, v42, s0
	ds_write_b16 v168, v42 offset:36458
	v_mul_f32_e32 v42, v49, v58
	v_mul_f32_e32 v48, v48, v160
	v_mul_f32_e32 v43, v43, v161
	v_mul_f32_e32 v42, v42, v167
	v_cvt_pk_bf16_f32 v48, v48, s0
	v_cvt_pk_bf16_f32 v43, v43, s0
	v_cvt_pk_bf16_f32 v42, v42, s0
	ds_write_b16 v168, v48 offset:34826
	ds_write_b16 v168, v43 offset:35098
	ds_write_b16 v168, v42 offset:36730
; __device__ __forceinline__ float bflo(unsigned w) { return __uint_as_float(w << 16); }
; __device__ __forceinline__ float bfhi(unsigned w) { return __uint_as_float(w & 0xffff0000u); }
; __device__ __forceinline__ unsigned short f2bf(float f) { return (unsigned short)(cvt_pk_bf16(f, 0.f) & 0xffffu); }
; __device__ __forceinline__ void sgu_unit(const Params& p, int l, int un, LAS unsigned char* lds) {
;     ...
;     for (int qi = 0; qi < 16; ++qi) { const int q = wave * 16 + qi;
;         const u32x4 v = vv[qi]; float f[8] = {bflo(v.x), bfhi(v.x), bflo(v.y), bfhi(v.y), bflo(v.z), bfhi(v.z), bflo(v.w), bfhi(v.w)}; float ss = 0.f;
; #pragma unroll
;         for (int j = 0; j < 8; ++j) { f[j] = gelu_tanh(f[j]); ss += f[j] * f[j]; }
;         ss = wave_sum(ss); const float rinv = rsqrtf(ss * (1.0f / 512.0f) + EPS);
;         if ((lane >> 4) == h) { const int c0 = (lane & 15) * 8; const float* g = p.in[I_SGUNG] + l * 512 + h * 128 + c0;
; #pragma unroll
;             for (int j = 0; j < 8; ++j) Vl[(c0 + j) * 136 + q] = f2bf(f[j] * rinv * g[j]); } }
.LBB0_1272:
	s_or_b64 exec, exec, s[0:1]
	s_waitcnt vmcnt(9)
	v_lshlrev_b32_e32 v42, 16, v38
	v_lshlrev_b32_e32 v43, 16, v39
	v_and_b32_e32 v45, 0xffff0000, v39
	v_mul_f32_e32 v39, 0x3dd2d3e8, v42
	v_fma_f32 v39, -v39, v42, s33
	v_mul_f32_e32 v39, v39, v42
	v_exp_f32_e32 v39, v39
	v_and_b32_e32 v38, 0xffff0000, v38
	v_lshlrev_b32_e32 v46, 16, v40
	v_and_b32_e32 v47, 0xffff0000, v40
	v_add_f32_e32 v39, 1.0, v39
	v_rcp_f32_e32 v39, v39
	v_mul_f32_e32 v40, 0x3dd2d3e8, v45
	v_fma_f32 v40, -v40, v45, s33
	v_mul_f32_e32 v40, v40, v45
	v_mul_f32_e32 v44, v39, v42
	v_mul_f32_e32 v39, 0x3dd2d3e8, v38
	v_fma_f32 v39, -v39, v38, s33
	v_mul_f32_e32 v39, v39, v38
	v_exp_f32_e32 v39, v39
	v_exp_f32_e32 v40, v40
	v_lshlrev_b32_e32 v48, 16, v41
	v_and_b32_e32 v49, 0xffff0000, v41
	v_add_f32_e32 v39, 1.0, v39
	v_rcp_f32_e32 v39, v39
	v_add_f32_e32 v40, 1.0, v40
	v_rcp_f32_e32 v40, v40
	v_mul_f32_e32 v41, 0x3dd2d3e8, v46
	v_mul_f32_e32 v39, v39, v38
	v_mul_f32_e32 v38, 0x3dd2d3e8, v43
	v_fma_f32 v38, -v38, v43, s33
	v_mul_f32_e32 v38, v38, v43
	v_exp_f32_e32 v38, v38
	v_fma_f32 v41, -v41, v46, s33
	v_mul_f32_e32 v42, 0x3dd2d3e8, v47
	v_mul_f32_e32 v41, v41, v46
	v_add_f32_e32 v38, 1.0, v38
	v_rcp_f32_e32 v38, v38
	v_fma_f32 v42, -v42, v47, s33
	v_mul_f32_e32 v40, v40, v45
	v_exp_f32_e32 v41, v41
	v_mul_f32_e32 v38, v38, v43
	v_mul_f32_e32 v43, 0x3dd2d3e8, v48
	v_mul_f32_e32 v42, v42, v47
	v_fma_f32 v43, -v43, v48, s33
	v_mul_f32_e32 v45, 0x3dd2d3e8, v49
	v_exp_f32_e32 v42, v42
	v_mul_f32_e32 v43, v43, v48
	v_fma_f32 v45, -v45, v49, s33
	v_exp_f32_e32 v43, v43
	v_mul_f32_e32 v45, v45, v49
	v_exp_f32_e32 v45, v45
	v_add_f32_e32 v41, 1.0, v41
	v_rcp_f32_e32 v41, v41
	v_add_f32_e32 v42, 1.0, v42
	v_mul_f32_e32 v50, v39, v39
	v_rcp_f32_e32 v42, v42
	v_add_f32_e32 v43, 1.0, v43
	v_fmac_f32_e32 v50, v44, v44
	v_rcp_f32_e32 v43, v43
	v_add_f32_e32 v45, 1.0, v45
	v_fmac_f32_e32 v50, v38, v38
	v_rcp_f32_e32 v45, v45
	v_fmac_f32_e32 v50, v40, v40
	v_mul_f32_e32 v41, v41, v46
	v_fmac_f32_e32 v50, v41, v41
	v_mul_f32_e32 v42, v42, v47
	v_fmac_f32_e32 v50, v42, v42
	v_mul_f32_e32 v43, v43, v48
	v_fmac_f32_e32 v50, v43, v43
	v_mul_f32_e32 v45, v45, v49
	v_fmac_f32_e32 v50, v45, v45
	v_mov_b32_e32 v46, v50
	s_nop 1
	v_permlane32_swap_b32_e32 v46, v50
	s_waitcnt lgkmcnt(0)
	v_add_f32_e32 v46, v50, v46
	v_mov_b32_e32 v47, v46
	s_nop 1
	v_permlane16_swap_b32_e32 v47, v46
	s_waitcnt lgkmcnt(0)
	v_add_f32_e32 v46, v46, v47
	s_nop 1
	v_mov_b32_dpp v47, v46 row_ror:8 row_mask:0xf bank_mask:0xf
	s_waitcnt lgkmcnt(0)
	v_add_f32_e32 v46, v46, v47
	s_nop 1
	v_mov_b32_dpp v47, v46 row_shl:4 row_mask:0xf bank_mask:0x5
	v_mov_b32_dpp v47, v46 row_shr:4 row_mask:0xf bank_mask:0xa
	s_waitcnt lgkmcnt(0)
	v_add_f32_e32 v46, v46, v47
	s_nop 1
	v_mov_b32_dpp v47, v46 quad_perm:[2,3,0,1] row_mask:0xf bank_mask:0xf
	s_waitcnt lgkmcnt(0)
	v_add_f32_e32 v46, v46, v47
	s_nop 1
	v_mov_b32_dpp v47, v46 quad_perm:[1,0,3,2] row_mask:0xf bank_mask:0xf
	s_and_saveexec_b64 s[0:1], vcc
	s_cbranch_execz .LBB0_1274
	s_waitcnt lgkmcnt(0)
	v_add_f32_e32 v46, v46, v47
	v_fmamk_f32 v46, v46, 0x3b000000, v246
	s_mov_b32 s2, 0x800000
	v_cmp_gt_f32_e64 s[2:3], s2, v46
	v_mul_f32_e32 v47, 0x4b800000, v46
	s_nop 0
	v_cndmask_b32_e64 v46, v46, v47, s[2:3]
	v_rsq_f32_e32 v46, v46
	s_nop 0
	v_mul_f32_e32 v47, 0x45800000, v46
	v_cndmask_b32_e64 v54, v46, v47, s[2:3]
	v_mul_f32_e32 v38, v38, v54
	v_mul_f32_e32 v44, v44, v54
	v_mul_f32_e32 v39, v39, v54
	v_mul_f32_e32 v38, v38, v162
	v_cvt_pk_bf16_f32 v38, v38, s0
	ds_write_b16 v168, v38 offset:35372
	v_mul_f32_e32 v38, v40, v54
	v_mul_f32_e32 v38, v38, v163
	v_cvt_pk_bf16_f32 v38, v38, s0
	ds_write_b16 v168, v38 offset:35644
	v_mul_f32_e32 v38, v41, v54
	v_mul_f32_e32 v38, v38, v164
	v_cvt_pk_bf16_f32 v38, v38, s0
	ds_write_b16 v168, v38 offset:35916
	v_mul_f32_e32 v38, v42, v54
	v_mul_f32_e32 v38, v38, v165
	v_cvt_pk_bf16_f32 v38, v38, s0
	ds_write_b16 v168, v38 offset:36188
	v_mul_f32_e32 v38, v43, v54
	v_mul_f32_e32 v38, v38, v166
	v_cvt_pk_bf16_f32 v38, v38, s0
	ds_write_b16 v168, v38 offset:36460
	v_mul_f32_e32 v38, v45, v54
	v_mul_f32_e32 v44, v44, v160
	v_mul_f32_e32 v39, v39, v161
	v_mul_f32_e32 v38, v38, v167
	v_cvt_pk_bf16_f32 v44, v44, s0
	v_cvt_pk_bf16_f32 v39, v39, s0
	v_cvt_pk_bf16_f32 v38, v38, s0
	ds_write_b16 v168, v44 offset:34828
	ds_write_b16 v168, v39 offset:35100
	ds_write_b16 v168, v38 offset:36732
; __device__ __forceinline__ float bflo(unsigned w) { return __uint_as_float(w << 16); }
; __device__ __forceinline__ float bfhi(unsigned w) { return __uint_as_float(w & 0xffff0000u); }
; __device__ __forceinline__ unsigned short f2bf(float f) { return (unsigned short)(cvt_pk_bf16(f, 0.f) & 0xffffu); }
; __device__ __forceinline__ void sgu_unit(const Params& p, int l, int un, LAS unsigned char* lds) {
;     ...
;     for (int qi = 0; qi < 16; ++qi) { const int q = wave * 16 + qi;
;         const u32x4 v = vv[qi]; float f[8] = {bflo(v.x), bfhi(v.x), bflo(v.y), bfhi(v.y), bflo(v.z), bfhi(v.z), bflo(v.w), bfhi(v.w)}; float ss = 0.f;
; #pragma unroll
;         for (int j = 0; j < 8; ++j) { f[j] = gelu_tanh(f[j]); ss += f[j] * f[j]; }
;         ss = wave_sum(ss); const float rinv = rsqrtf(ss * (1.0f / 512.0f) + EPS);
;         if ((lane >> 4) == h) { const int c0 = (lane & 15) * 8; const float* g = p.in[I_SGUNG] + l * 512 + h * 128 + c0;
; #pragma unroll
;             for (int j = 0; j < 8; ++j) Vl[(c0 + j) * 136 + q] = f2bf(f[j] * rinv * g[j]); } }
.LBB0_1274:
	s_or_b64 exec, exec, s[0:1]
	s_waitcnt vmcnt(8)
	v_lshlrev_b32_e32 v38, 16, v34
	v_lshlrev_b32_e32 v39, 16, v35
	v_and_b32_e32 v41, 0xffff0000, v35
	v_mul_f32_e32 v35, 0x3dd2d3e8, v38
	v_fma_f32 v35, -v35, v38, s33
	v_mul_f32_e32 v35, v35, v38
	v_exp_f32_e32 v35, v35
	v_and_b32_e32 v34, 0xffff0000, v34
	v_lshlrev_b32_e32 v42, 16, v36
	v_and_b32_e32 v43, 0xffff0000, v36
	v_add_f32_e32 v35, 1.0, v35
	v_rcp_f32_e32 v35, v35
	v_mul_f32_e32 v36, 0x3dd2d3e8, v41
	v_fma_f32 v36, -v36, v41, s33
	v_mul_f32_e32 v36, v36, v41
	v_mul_f32_e32 v40, v35, v38
	v_mul_f32_e32 v35, 0x3dd2d3e8, v34
	v_fma_f32 v35, -v35, v34, s33
	v_mul_f32_e32 v35, v35, v34
	v_exp_f32_e32 v35, v35
	v_exp_f32_e32 v36, v36
	v_lshlrev_b32_e32 v44, 16, v37
	v_and_b32_e32 v45, 0xffff0000, v37
	v_add_f32_e32 v35, 1.0, v35
	v_rcp_f32_e32 v35, v35
	v_add_f32_e32 v36, 1.0, v36
	v_rcp_f32_e32 v36, v36
	v_mul_f32_e32 v37, 0x3dd2d3e8, v42
	v_mul_f32_e32 v35, v35, v34
	v_mul_f32_e32 v34, 0x3dd2d3e8, v39
	v_fma_f32 v34, -v34, v39, s33
	v_mul_f32_e32 v34, v34, v39
	v_exp_f32_e32 v34, v34
	v_fma_f32 v37, -v37, v42, s33
	v_mul_f32_e32 v38, 0x3dd2d3e8, v43
	v_mul_f32_e32 v37, v37, v42
	v_add_f32_e32 v34, 1.0, v34
	v_rcp_f32_e32 v34, v34
	v_fma_f32 v38, -v38, v43, s33
	v_mul_f32_e32 v36, v36, v41
	v_exp_f32_e32 v37, v37
	v_mul_f32_e32 v34, v34, v39
	v_mul_f32_e32 v39, 0x3dd2d3e8, v44
	v_mul_f32_e32 v38, v38, v43
	v_fma_f32 v39, -v39, v44, s33
	v_mul_f32_e32 v41, 0x3dd2d3e8, v45
	v_exp_f32_e32 v38, v38
	v_mul_f32_e32 v39, v39, v44
	v_fma_f32 v41, -v41, v45, s33
	v_exp_f32_e32 v39, v39
	v_mul_f32_e32 v41, v41, v45
	v_exp_f32_e32 v41, v41
	v_add_f32_e32 v37, 1.0, v37
	v_rcp_f32_e32 v37, v37
	v_add_f32_e32 v38, 1.0, v38
	v_mul_f32_e32 v46, v35, v35
	v_rcp_f32_e32 v38, v38
	v_add_f32_e32 v39, 1.0, v39
	v_fmac_f32_e32 v46, v40, v40
	v_rcp_f32_e32 v39, v39
	v_add_f32_e32 v41, 1.0, v41
	v_fmac_f32_e32 v46, v34, v34
	v_rcp_f32_e32 v41, v41
	v_fmac_f32_e32 v46, v36, v36
	v_mul_f32_e32 v37, v37, v42
	v_fmac_f32_e32 v46, v37, v37
	v_mul_f32_e32 v38, v38, v43
	v_fmac_f32_e32 v46, v38, v38
	v_mul_f32_e32 v39, v39, v44
	v_fmac_f32_e32 v46, v39, v39
	v_mul_f32_e32 v41, v41, v45
	v_fmac_f32_e32 v46, v41, v41
	v_mov_b32_e32 v42, v46
	s_nop 1
	v_permlane32_swap_b32_e32 v42, v46
	s_waitcnt lgkmcnt(0)
	v_add_f32_e32 v42, v46, v42
	v_mov_b32_e32 v43, v42
	s_nop 1
	v_permlane16_swap_b32_e32 v43, v42
	s_waitcnt lgkmcnt(0)
	v_add_f32_e32 v42, v42, v43
	s_nop 1
	v_mov_b32_dpp v43, v42 row_ror:8 row_mask:0xf bank_mask:0xf
	s_waitcnt lgkmcnt(0)
	v_add_f32_e32 v42, v42, v43
	s_nop 1
	v_mov_b32_dpp v43, v42 row_shl:4 row_mask:0xf bank_mask:0x5
	v_mov_b32_dpp v43, v42 row_shr:4 row_mask:0xf bank_mask:0xa
	s_waitcnt lgkmcnt(0)
	v_add_f32_e32 v42, v42, v43
	s_nop 1
	v_mov_b32_dpp v43, v42 quad_perm:[2,3,0,1] row_mask:0xf bank_mask:0xf
	s_waitcnt lgkmcnt(0)
	v_add_f32_e32 v42, v42, v43
	s_nop 1
	v_mov_b32_dpp v43, v42 quad_perm:[1,0,3,2] row_mask:0xf bank_mask:0xf
	s_and_saveexec_b64 s[0:1], vcc
	s_cbranch_execz .LBB0_1276
	s_waitcnt lgkmcnt(0)
	v_add_f32_e32 v42, v42, v43
	v_fmamk_f32 v42, v42, 0x3b000000, v246
	s_mov_b32 s2, 0x800000
	v_cmp_gt_f32_e64 s[2:3], s2, v42
	v_mul_f32_e32 v43, 0x4b800000, v42
	s_nop 0
	v_cndmask_b32_e64 v42, v42, v43, s[2:3]
	v_rsq_f32_e32 v42, v42
	s_nop 0
	v_mul_f32_e32 v43, 0x45800000, v42
	v_cndmask_b32_e64 v50, v42, v43, s[2:3]
	v_mul_f32_e32 v34, v34, v50
	v_mul_f32_e32 v40, v40, v50
	v_mul_f32_e32 v35, v35, v50
	v_mul_f32_e32 v34, v34, v162
	v_cvt_pk_bf16_f32 v34, v34, s0
	ds_write_b16 v168, v34 offset:35374
	v_mul_f32_e32 v34, v36, v50
	v_mul_f32_e32 v34, v34, v163
	v_cvt_pk_bf16_f32 v34, v34, s0
	ds_write_b16 v168, v34 offset:35646
	v_mul_f32_e32 v34, v37, v50
	v_mul_f32_e32 v34, v34, v164
	v_cvt_pk_bf16_f32 v34, v34, s0
	ds_write_b16 v168, v34 offset:35918
	v_mul_f32_e32 v34, v38, v50
	v_mul_f32_e32 v34, v34, v165
	v_cvt_pk_bf16_f32 v34, v34, s0
	ds_write_b16 v168, v34 offset:36190
	v_mul_f32_e32 v34, v39, v50
	v_mul_f32_e32 v34, v34, v166
	v_cvt_pk_bf16_f32 v34, v34, s0
	ds_write_b16 v168, v34 offset:36462
	v_mul_f32_e32 v34, v41, v50
	v_mul_f32_e32 v40, v40, v160
	v_mul_f32_e32 v35, v35, v161
	v_mul_f32_e32 v34, v34, v167
	v_cvt_pk_bf16_f32 v40, v40, s0
	v_cvt_pk_bf16_f32 v35, v35, s0
	v_cvt_pk_bf16_f32 v34, v34, s0
	ds_write_b16 v168, v40 offset:34830
	ds_write_b16 v168, v35 offset:35102
	ds_write_b16 v168, v34 offset:36734
; __device__ __forceinline__ float bflo(unsigned w) { return __uint_as_float(w << 16); }
; __device__ __forceinline__ float bfhi(unsigned w) { return __uint_as_float(w & 0xffff0000u); }
; __device__ __forceinline__ unsigned short f2bf(float f) { return (unsigned short)(cvt_pk_bf16(f, 0.f) & 0xffffu); }
; __device__ __forceinline__ void sgu_unit(const Params& p, int l, int un, LAS unsigned char* lds) {
;     ...
;     for (int qi = 0; qi < 16; ++qi) { const int q = wave * 16 + qi;
;         const u32x4 v = vv[qi]; float f[8] = {bflo(v.x), bfhi(v.x), bflo(v.y), bfhi(v.y), bflo(v.z), bfhi(v.z), bflo(v.w), bfhi(v.w)}; float ss = 0.f;
; #pragma unroll
;         for (int j = 0; j < 8; ++j) { f[j] = gelu_tanh(f[j]); ss += f[j] * f[j]; }
;         ss = wave_sum(ss); const float rinv = rsqrtf(ss * (1.0f / 512.0f) + EPS);
;         if ((lane >> 4) == h) { const int c0 = (lane & 15) * 8; const float* g = p.in[I_SGUNG] + l * 512 + h * 128 + c0;
; #pragma unroll
;             for (int j = 0; j < 8; ++j) Vl[(c0 + j) * 136 + q] = f2bf(f[j] * rinv * g[j]); } }
.LBB0_1276:
	s_or_b64 exec, exec, s[0:1]
	s_waitcnt vmcnt(7)
	v_lshlrev_b32_e32 v34, 16, v30
	v_lshlrev_b32_e32 v35, 16, v31
	v_and_b32_e32 v37, 0xffff0000, v31
	v_mul_f32_e32 v31, 0x3dd2d3e8, v34
	v_fma_f32 v31, -v31, v34, s33
	v_mul_f32_e32 v31, v31, v34
	v_exp_f32_e32 v31, v31
	v_and_b32_e32 v30, 0xffff0000, v30
	v_lshlrev_b32_e32 v38, 16, v32
	v_and_b32_e32 v39, 0xffff0000, v32
	v_add_f32_e32 v31, 1.0, v31
	v_rcp_f32_e32 v31, v31
	v_mul_f32_e32 v32, 0x3dd2d3e8, v37
	v_fma_f32 v32, -v32, v37, s33
	v_mul_f32_e32 v32, v32, v37
	v_mul_f32_e32 v36, v31, v34
	v_mul_f32_e32 v31, 0x3dd2d3e8, v30
	v_fma_f32 v31, -v31, v30, s33
	v_mul_f32_e32 v31, v31, v30
	v_exp_f32_e32 v31, v31
	v_exp_f32_e32 v32, v32
	v_lshlrev_b32_e32 v40, 16, v33
	v_and_b32_e32 v41, 0xffff0000, v33
	v_add_f32_e32 v31, 1.0, v31
	v_rcp_f32_e32 v31, v31
	v_add_f32_e32 v32, 1.0, v32
	v_rcp_f32_e32 v32, v32
	v_mul_f32_e32 v33, 0x3dd2d3e8, v38
	v_mul_f32_e32 v31, v31, v30
	v_mul_f32_e32 v30, 0x3dd2d3e8, v35
	v_fma_f32 v30, -v30, v35, s33
	v_mul_f32_e32 v30, v30, v35
	v_exp_f32_e32 v30, v30
	v_fma_f32 v33, -v33, v38, s33
	v_mul_f32_e32 v34, 0x3dd2d3e8, v39
	v_mul_f32_e32 v33, v33, v38
	v_add_f32_e32 v30, 1.0, v30
	v_rcp_f32_e32 v30, v30
	v_fma_f32 v34, -v34, v39, s33
	v_mul_f32_e32 v32, v32, v37
	v_exp_f32_e32 v33, v33
	v_mul_f32_e32 v30, v30, v35
	v_mul_f32_e32 v35, 0x3dd2d3e8, v40
	v_mul_f32_e32 v34, v34, v39
	v_fma_f32 v35, -v35, v40, s33
	v_mul_f32_e32 v37, 0x3dd2d3e8, v41
	v_exp_f32_e32 v34, v34
	v_mul_f32_e32 v35, v35, v40
	v_fma_f32 v37, -v37, v41, s33
	v_exp_f32_e32 v35, v35
	v_mul_f32_e32 v37, v37, v41
	v_exp_f32_e32 v37, v37
	v_add_f32_e32 v33, 1.0, v33
	v_rcp_f32_e32 v33, v33
	v_add_f32_e32 v34, 1.0, v34
	v_mul_f32_e32 v42, v31, v31
	v_rcp_f32_e32 v34, v34
	v_add_f32_e32 v35, 1.0, v35
	v_fmac_f32_e32 v42, v36, v36
	v_rcp_f32_e32 v35, v35
	v_add_f32_e32 v37, 1.0, v37
	v_fmac_f32_e32 v42, v30, v30
	v_rcp_f32_e32 v37, v37
	v_fmac_f32_e32 v42, v32, v32
	v_mul_f32_e32 v33, v33, v38
	v_fmac_f32_e32 v42, v33, v33
	v_mul_f32_e32 v34, v34, v39
	v_fmac_f32_e32 v42, v34, v34
	v_mul_f32_e32 v35, v35, v40
	v_fmac_f32_e32 v42, v35, v35
	v_mul_f32_e32 v37, v37, v41
	v_fmac_f32_e32 v42, v37, v37
	v_mov_b32_e32 v38, v42
	s_nop 1
	v_permlane32_swap_b32_e32 v38, v42
	s_waitcnt lgkmcnt(0)
	v_add_f32_e32 v38, v42, v38
	v_mov_b32_e32 v39, v38
	s_nop 1
	v_permlane16_swap_b32_e32 v39, v38
	s_waitcnt lgkmcnt(0)
	v_add_f32_e32 v38, v38, v39
	s_nop 1
	v_mov_b32_dpp v39, v38 row_ror:8 row_mask:0xf bank_mask:0xf
	s_waitcnt lgkmcnt(0)
	v_add_f32_e32 v38, v38, v39
	s_nop 1
	v_mov_b32_dpp v39, v38 row_shl:4 row_mask:0xf bank_mask:0x5
	v_mov_b32_dpp v39, v38 row_shr:4 row_mask:0xf bank_mask:0xa
	s_waitcnt lgkmcnt(0)
	v_add_f32_e32 v38, v38, v39
	s_nop 1
	v_mov_b32_dpp v39, v38 quad_perm:[2,3,0,1] row_mask:0xf bank_mask:0xf
	s_waitcnt lgkmcnt(0)
	v_add_f32_e32 v38, v38, v39
	s_nop 1
	v_mov_b32_dpp v39, v38 quad_perm:[1,0,3,2] row_mask:0xf bank_mask:0xf
	s_and_saveexec_b64 s[0:1], vcc
	s_cbranch_execz .LBB0_1278
	s_waitcnt lgkmcnt(0)
	v_add_f32_e32 v38, v38, v39
	v_fmamk_f32 v38, v38, 0x3b000000, v246
	s_mov_b32 s2, 0x800000
	v_cmp_gt_f32_e64 s[2:3], s2, v38
	v_mul_f32_e32 v39, 0x4b800000, v38
	s_nop 0
	v_cndmask_b32_e64 v38, v38, v39, s[2:3]
	v_rsq_f32_e32 v38, v38
	s_nop 0
	v_mul_f32_e32 v39, 0x45800000, v38
	v_cndmask_b32_e64 v46, v38, v39, s[2:3]
	v_mul_f32_e32 v30, v30, v46
	v_mul_f32_e32 v36, v36, v46
	v_mul_f32_e32 v31, v31, v46
	v_mul_f32_e32 v30, v30, v162
	v_cvt_pk_bf16_f32 v30, v30, s0
	ds_write_b16 v169, v30 offset:35376
	v_mul_f32_e32 v30, v32, v46
	v_mul_f32_e32 v30, v30, v163
	v_cvt_pk_bf16_f32 v30, v30, s0
	ds_write_b16 v169, v30 offset:35648
	v_mul_f32_e32 v30, v33, v46
	v_mul_f32_e32 v30, v30, v164
	v_cvt_pk_bf16_f32 v30, v30, s0
	ds_write_b16 v169, v30 offset:35920
	v_mul_f32_e32 v30, v34, v46
	v_mul_f32_e32 v30, v30, v165
	v_cvt_pk_bf16_f32 v30, v30, s0
	ds_write_b16 v169, v30 offset:36192
	v_mul_f32_e32 v30, v35, v46
	v_mul_f32_e32 v30, v30, v166
	v_cvt_pk_bf16_f32 v30, v30, s0
	ds_write_b16 v169, v30 offset:36464
	v_mul_f32_e32 v30, v37, v46
	v_mul_f32_e32 v36, v36, v160
	v_mul_f32_e32 v31, v31, v161
	v_mul_f32_e32 v30, v30, v167
	v_cvt_pk_bf16_f32 v36, v36, s0
	v_cvt_pk_bf16_f32 v31, v31, s0
	v_cvt_pk_bf16_f32 v30, v30, s0
	ds_write_b16 v169, v36 offset:34832
	ds_write_b16 v169, v31 offset:35104
	ds_write_b16 v169, v30 offset:36736
; __device__ __forceinline__ float bflo(unsigned w) { return __uint_as_float(w << 16); }
; __device__ __forceinline__ float bfhi(unsigned w) { return __uint_as_float(w & 0xffff0000u); }
; __device__ __forceinline__ unsigned short f2bf(float f) { return (unsigned short)(cvt_pk_bf16(f, 0.f) & 0xffffu); }
; __device__ __forceinline__ void sgu_unit(const Params& p, int l, int un, LAS unsigned char* lds) {
;     ...
;     for (int qi = 0; qi < 16; ++qi) { const int q = wave * 16 + qi;
;         const u32x4 v = vv[qi]; float f[8] = {bflo(v.x), bfhi(v.x), bflo(v.y), bfhi(v.y), bflo(v.z), bfhi(v.z), bflo(v.w), bfhi(v.w)}; float ss = 0.f;
; #pragma unroll
;         for (int j = 0; j < 8; ++j) { f[j] = gelu_tanh(f[j]); ss += f[j] * f[j]; }
;         ss = wave_sum(ss); const float rinv = rsqrtf(ss * (1.0f / 512.0f) + EPS);
;         if ((lane >> 4) == h) { const int c0 = (lane & 15) * 8; const float* g = p.in[I_SGUNG] + l * 512 + h * 128 + c0;
; #pragma unroll
;             for (int j = 0; j < 8; ++j) Vl[(c0 + j) * 136 + q] = f2bf(f[j] * rinv * g[j]); } }
.LBB0_1278:
	s_or_b64 exec, exec, s[0:1]
	s_waitcnt vmcnt(6)
	v_lshlrev_b32_e32 v30, 16, v26
	v_lshlrev_b32_e32 v31, 16, v27
	v_and_b32_e32 v33, 0xffff0000, v27
	v_mul_f32_e32 v27, 0x3dd2d3e8, v30
	v_fma_f32 v27, -v27, v30, s33
	v_mul_f32_e32 v27, v27, v30
	v_exp_f32_e32 v27, v27
	v_and_b32_e32 v26, 0xffff0000, v26
	v_lshlrev_b32_e32 v34, 16, v28
	v_and_b32_e32 v35, 0xffff0000, v28
	v_add_f32_e32 v27, 1.0, v27
	v_rcp_f32_e32 v27, v27
	v_mul_f32_e32 v28, 0x3dd2d3e8, v33
	v_fma_f32 v28, -v28, v33, s33
	v_mul_f32_e32 v28, v28, v33
	v_mul_f32_e32 v32, v27, v30
	v_mul_f32_e32 v27, 0x3dd2d3e8, v26
	v_fma_f32 v27, -v27, v26, s33
	v_mul_f32_e32 v27, v27, v26
	v_exp_f32_e32 v27, v27
	v_exp_f32_e32 v28, v28
	v_lshlrev_b32_e32 v36, 16, v29
	v_and_b32_e32 v37, 0xffff0000, v29
	v_add_f32_e32 v27, 1.0, v27
	v_rcp_f32_e32 v27, v27
	v_add_f32_e32 v28, 1.0, v28
	v_rcp_f32_e32 v28, v28
	v_mul_f32_e32 v29, 0x3dd2d3e8, v34
	v_mul_f32_e32 v27, v27, v26
	v_mul_f32_e32 v26, 0x3dd2d3e8, v31
	v_fma_f32 v26, -v26, v31, s33
	v_mul_f32_e32 v26, v26, v31
	v_exp_f32_e32 v26, v26
	v_fma_f32 v29, -v29, v34, s33
	v_mul_f32_e32 v30, 0x3dd2d3e8, v35
	v_mul_f32_e32 v29, v29, v34
	v_add_f32_e32 v26, 1.0, v26
	v_rcp_f32_e32 v26, v26
	v_fma_f32 v30, -v30, v35, s33
	v_mul_f32_e32 v28, v28, v33
	v_exp_f32_e32 v29, v29
	v_mul_f32_e32 v26, v26, v31
	v_mul_f32_e32 v31, 0x3dd2d3e8, v36
	v_mul_f32_e32 v30, v30, v35
	v_fma_f32 v31, -v31, v36, s33
	v_mul_f32_e32 v33, 0x3dd2d3e8, v37
	v_exp_f32_e32 v30, v30
	v_mul_f32_e32 v31, v31, v36
	v_fma_f32 v33, -v33, v37, s33
	v_exp_f32_e32 v31, v31
	v_mul_f32_e32 v33, v33, v37
	v_exp_f32_e32 v33, v33
	v_add_f32_e32 v29, 1.0, v29
	v_rcp_f32_e32 v29, v29
	v_add_f32_e32 v30, 1.0, v30
	v_mul_f32_e32 v38, v27, v27
	v_rcp_f32_e32 v30, v30
	v_add_f32_e32 v31, 1.0, v31
	v_fmac_f32_e32 v38, v32, v32
	v_rcp_f32_e32 v31, v31
	v_add_f32_e32 v33, 1.0, v33
	v_fmac_f32_e32 v38, v26, v26
	v_rcp_f32_e32 v33, v33
	v_fmac_f32_e32 v38, v28, v28
	v_mul_f32_e32 v29, v29, v34
	v_fmac_f32_e32 v38, v29, v29
	v_mul_f32_e32 v30, v30, v35
	v_fmac_f32_e32 v38, v30, v30
	v_mul_f32_e32 v31, v31, v36
	v_fmac_f32_e32 v38, v31, v31
	v_mul_f32_e32 v33, v33, v37
	v_fmac_f32_e32 v38, v33, v33
	v_mov_b32_e32 v34, v38
	s_nop 1
	v_permlane32_swap_b32_e32 v34, v38
	s_waitcnt lgkmcnt(0)
	v_add_f32_e32 v34, v38, v34
	v_mov_b32_e32 v35, v34
	s_nop 1
	v_permlane16_swap_b32_e32 v35, v34
	s_waitcnt lgkmcnt(0)
	v_add_f32_e32 v34, v34, v35
	s_nop 1
	v_mov_b32_dpp v35, v34 row_ror:8 row_mask:0xf bank_mask:0xf
	s_waitcnt lgkmcnt(0)
	v_add_f32_e32 v34, v34, v35
	s_nop 1
	v_mov_b32_dpp v35, v34 row_shl:4 row_mask:0xf bank_mask:0x5
	v_mov_b32_dpp v35, v34 row_shr:4 row_mask:0xf bank_mask:0xa
	s_waitcnt lgkmcnt(0)
	v_add_f32_e32 v34, v34, v35
	s_nop 1
	v_mov_b32_dpp v35, v34 quad_perm:[2,3,0,1] row_mask:0xf bank_mask:0xf
	s_waitcnt lgkmcnt(0)
	v_add_f32_e32 v34, v34, v35
	s_nop 1
	v_mov_b32_dpp v35, v34 quad_perm:[1,0,3,2] row_mask:0xf bank_mask:0xf
	s_and_saveexec_b64 s[0:1], vcc
	s_cbranch_execz .LBB0_1280
	s_waitcnt lgkmcnt(0)
	v_add_f32_e32 v34, v34, v35
	v_fmamk_f32 v34, v34, 0x3b000000, v246
	s_mov_b32 s2, 0x800000
	v_cmp_gt_f32_e64 s[2:3], s2, v34
	v_mul_f32_e32 v35, 0x4b800000, v34
	s_nop 0
	v_cndmask_b32_e64 v34, v34, v35, s[2:3]
	v_rsq_f32_e32 v34, v34
	s_nop 0
	v_mul_f32_e32 v35, 0x45800000, v34
	v_cndmask_b32_e64 v42, v34, v35, s[2:3]
	v_mul_f32_e32 v26, v26, v42
	v_mul_f32_e32 v32, v32, v42
	v_mul_f32_e32 v27, v27, v42
	v_mul_f32_e32 v26, v26, v162
	v_cvt_pk_bf16_f32 v26, v26, s0
	ds_write_b16 v169, v26 offset:35378
	v_mul_f32_e32 v26, v28, v42
	v_mul_f32_e32 v26, v26, v163
	v_cvt_pk_bf16_f32 v26, v26, s0
	ds_write_b16 v169, v26 offset:35650
	v_mul_f32_e32 v26, v29, v42
	v_mul_f32_e32 v26, v26, v164
	v_cvt_pk_bf16_f32 v26, v26, s0
	ds_write_b16 v169, v26 offset:35922
	v_mul_f32_e32 v26, v30, v42
	v_mul_f32_e32 v26, v26, v165
	v_cvt_pk_bf16_f32 v26, v26, s0
	ds_write_b16 v169, v26 offset:36194
	v_mul_f32_e32 v26, v31, v42
	v_mul_f32_e32 v26, v26, v166
	v_cvt_pk_bf16_f32 v26, v26, s0
	ds_write_b16 v169, v26 offset:36466
	v_mul_f32_e32 v26, v33, v42
	v_mul_f32_e32 v32, v32, v160
	v_mul_f32_e32 v27, v27, v161
	v_mul_f32_e32 v26, v26, v167
	v_cvt_pk_bf16_f32 v32, v32, s0
	v_cvt_pk_bf16_f32 v27, v27, s0
	v_cvt_pk_bf16_f32 v26, v26, s0
	ds_write_b16 v169, v32 offset:34834
	ds_write_b16 v169, v27 offset:35106
	ds_write_b16 v169, v26 offset:36738
; __device__ __forceinline__ float bflo(unsigned w) { return __uint_as_float(w << 16); }
; __device__ __forceinline__ float bfhi(unsigned w) { return __uint_as_float(w & 0xffff0000u); }
; __device__ __forceinline__ unsigned short f2bf(float f) { return (unsigned short)(cvt_pk_bf16(f, 0.f) & 0xffffu); }
; __device__ __forceinline__ void sgu_unit(const Params& p, int l, int un, LAS unsigned char* lds) {
;     ...
;     for (int qi = 0; qi < 16; ++qi) { const int q = wave * 16 + qi;
;         const u32x4 v = vv[qi]; float f[8] = {bflo(v.x), bfhi(v.x), bflo(v.y), bfhi(v.y), bflo(v.z), bfhi(v.z), bflo(v.w), bfhi(v.w)}; float ss = 0.f;
; #pragma unroll
;         for (int j = 0; j < 8; ++j) { f[j] = gelu_tanh(f[j]); ss += f[j] * f[j]; }
;         ss = wave_sum(ss); const float rinv = rsqrtf(ss * (1.0f / 512.0f) + EPS);
;         if ((lane >> 4) == h) { const int c0 = (lane & 15) * 8; const float* g = p.in[I_SGUNG] + l * 512 + h * 128 + c0;
; #pragma unroll
;             for (int j = 0; j < 8; ++j) Vl[(c0 + j) * 136 + q] = f2bf(f[j] * rinv * g[j]); } }
.LBB0_1280:
	s_or_b64 exec, exec, s[0:1]
	s_waitcnt vmcnt(5)
	v_lshlrev_b32_e32 v26, 16, v22
	v_lshlrev_b32_e32 v27, 16, v23
	v_and_b32_e32 v29, 0xffff0000, v23
	v_mul_f32_e32 v23, 0x3dd2d3e8, v26
	v_fma_f32 v23, -v23, v26, s33
	v_mul_f32_e32 v23, v23, v26
	v_exp_f32_e32 v23, v23
	v_and_b32_e32 v22, 0xffff0000, v22
	v_lshlrev_b32_e32 v30, 16, v24
	v_and_b32_e32 v31, 0xffff0000, v24
	v_add_f32_e32 v23, 1.0, v23
	v_rcp_f32_e32 v23, v23
	v_mul_f32_e32 v24, 0x3dd2d3e8, v29
	v_fma_f32 v24, -v24, v29, s33
	v_mul_f32_e32 v24, v24, v29
	v_mul_f32_e32 v28, v23, v26
	v_mul_f32_e32 v23, 0x3dd2d3e8, v22
	v_fma_f32 v23, -v23, v22, s33
	v_mul_f32_e32 v23, v23, v22
	v_exp_f32_e32 v23, v23
	v_exp_f32_e32 v24, v24
	v_lshlrev_b32_e32 v32, 16, v25
	v_and_b32_e32 v33, 0xffff0000, v25
	v_add_f32_e32 v23, 1.0, v23
	v_rcp_f32_e32 v23, v23
	v_add_f32_e32 v24, 1.0, v24
	v_rcp_f32_e32 v24, v24
	v_mul_f32_e32 v25, 0x3dd2d3e8, v30
	v_mul_f32_e32 v23, v23, v22
	v_mul_f32_e32 v22, 0x3dd2d3e8, v27
	v_fma_f32 v22, -v22, v27, s33
	v_mul_f32_e32 v22, v22, v27
	v_exp_f32_e32 v22, v22
	v_fma_f32 v25, -v25, v30, s33
	v_mul_f32_e32 v26, 0x3dd2d3e8, v31
	v_mul_f32_e32 v25, v25, v30
	v_add_f32_e32 v22, 1.0, v22
	v_rcp_f32_e32 v22, v22
	v_fma_f32 v26, -v26, v31, s33
	v_mul_f32_e32 v24, v24, v29
	v_exp_f32_e32 v25, v25
	v_mul_f32_e32 v22, v22, v27
	v_mul_f32_e32 v27, 0x3dd2d3e8, v32
	v_mul_f32_e32 v26, v26, v31
	v_fma_f32 v27, -v27, v32, s33
	v_mul_f32_e32 v29, 0x3dd2d3e8, v33
	v_exp_f32_e32 v26, v26
	v_mul_f32_e32 v27, v27, v32
	v_fma_f32 v29, -v29, v33, s33
	v_exp_f32_e32 v27, v27
	v_mul_f32_e32 v29, v29, v33
	v_exp_f32_e32 v29, v29
	v_add_f32_e32 v25, 1.0, v25
	v_rcp_f32_e32 v25, v25
	v_add_f32_e32 v26, 1.0, v26
	v_mul_f32_e32 v34, v23, v23
	v_rcp_f32_e32 v26, v26
	v_add_f32_e32 v27, 1.0, v27
	v_fmac_f32_e32 v34, v28, v28
	v_rcp_f32_e32 v27, v27
	v_add_f32_e32 v29, 1.0, v29
	v_fmac_f32_e32 v34, v22, v22
	v_rcp_f32_e32 v29, v29
	v_fmac_f32_e32 v34, v24, v24
	v_mul_f32_e32 v25, v25, v30
	v_fmac_f32_e32 v34, v25, v25
	v_mul_f32_e32 v26, v26, v31
	v_fmac_f32_e32 v34, v26, v26
	v_mul_f32_e32 v27, v27, v32
	v_fmac_f32_e32 v34, v27, v27
	v_mul_f32_e32 v29, v29, v33
	v_fmac_f32_e32 v34, v29, v29
	v_mov_b32_e32 v30, v34
	s_nop 1
	v_permlane32_swap_b32_e32 v30, v34
	s_waitcnt lgkmcnt(0)
	v_add_f32_e32 v30, v34, v30
	v_mov_b32_e32 v31, v30
	s_nop 1
	v_permlane16_swap_b32_e32 v31, v30
	s_waitcnt lgkmcnt(0)
	v_add_f32_e32 v30, v30, v31
	s_nop 1
	v_mov_b32_dpp v31, v30 row_ror:8 row_mask:0xf bank_mask:0xf
	s_waitcnt lgkmcnt(0)
	v_add_f32_e32 v30, v30, v31
	s_nop 1
	v_mov_b32_dpp v31, v30 row_shl:4 row_mask:0xf bank_mask:0x5
	v_mov_b32_dpp v31, v30 row_shr:4 row_mask:0xf bank_mask:0xa
	s_waitcnt lgkmcnt(0)
	v_add_f32_e32 v30, v30, v31
	s_nop 1
	v_mov_b32_dpp v31, v30 quad_perm:[2,3,0,1] row_mask:0xf bank_mask:0xf
	s_waitcnt lgkmcnt(0)
	v_add_f32_e32 v30, v30, v31
	s_nop 1
	v_mov_b32_dpp v31, v30 quad_perm:[1,0,3,2] row_mask:0xf bank_mask:0xf
	s_and_saveexec_b64 s[0:1], vcc
	s_cbranch_execz .LBB0_1282
	s_waitcnt lgkmcnt(0)
	v_add_f32_e32 v30, v30, v31
	v_fmamk_f32 v30, v30, 0x3b000000, v246
	s_mov_b32 s2, 0x800000
	v_cmp_gt_f32_e64 s[2:3], s2, v30
	v_mul_f32_e32 v31, 0x4b800000, v30
	s_nop 0
	v_cndmask_b32_e64 v30, v30, v31, s[2:3]
	v_rsq_f32_e32 v30, v30
	s_nop 0
	v_mul_f32_e32 v31, 0x45800000, v30
	v_cndmask_b32_e64 v38, v30, v31, s[2:3]
	v_mul_f32_e32 v22, v22, v38
	v_mul_f32_e32 v28, v28, v38
	v_mul_f32_e32 v23, v23, v38
	v_mul_f32_e32 v22, v22, v162
	v_cvt_pk_bf16_f32 v22, v22, s0
	ds_write_b16 v169, v22 offset:35380
	v_mul_f32_e32 v22, v24, v38
	v_mul_f32_e32 v22, v22, v163
	v_cvt_pk_bf16_f32 v22, v22, s0
	ds_write_b16 v169, v22 offset:35652
	v_mul_f32_e32 v22, v25, v38
	v_mul_f32_e32 v22, v22, v164
	v_cvt_pk_bf16_f32 v22, v22, s0
	ds_write_b16 v169, v22 offset:35924
	v_mul_f32_e32 v22, v26, v38
	v_mul_f32_e32 v22, v22, v165
	v_cvt_pk_bf16_f32 v22, v22, s0
	ds_write_b16 v169, v22 offset:36196
	v_mul_f32_e32 v22, v27, v38
	v_mul_f32_e32 v22, v22, v166
	v_cvt_pk_bf16_f32 v22, v22, s0
	ds_write_b16 v169, v22 offset:36468
	v_mul_f32_e32 v22, v29, v38
	v_mul_f32_e32 v28, v28, v160
	v_mul_f32_e32 v23, v23, v161
	v_mul_f32_e32 v22, v22, v167
	v_cvt_pk_bf16_f32 v28, v28, s0
	v_cvt_pk_bf16_f32 v23, v23, s0
	v_cvt_pk_bf16_f32 v22, v22, s0
	ds_write_b16 v169, v28 offset:34836
	ds_write_b16 v169, v23 offset:35108
	ds_write_b16 v169, v22 offset:36740
; __device__ __forceinline__ float bflo(unsigned w) { return __uint_as_float(w << 16); }
; __device__ __forceinline__ float bfhi(unsigned w) { return __uint_as_float(w & 0xffff0000u); }
; __device__ __forceinline__ unsigned short f2bf(float f) { return (unsigned short)(cvt_pk_bf16(f, 0.f) & 0xffffu); }
; __device__ __forceinline__ float gelu_tanh(float x) {
;     const float y = x * (-2.3022081986679503f - 0.10294324069457f * x * x);
;     return x * __builtin_amdgcn_rcpf(1.0f + __builtin_amdgcn_exp2f(y));
; }
; __device__ __forceinline__ void sgu_unit(const Params& p, int l, int un, LAS unsigned char* lds) {
;     ...
;     for (int qi = 0; qi < 16; ++qi) { const int q = wave * 16 + qi;
;         const u32x4 v = vv[qi]; float f[8] = {bflo(v.x), bfhi(v.x), bflo(v.y), bfhi(v.y), bflo(v.z), bfhi(v.z), bflo(v.w), bfhi(v.w)}; float ss = 0.f;
; #pragma unroll
;         for (int j = 0; j < 8; ++j) { f[j] = gelu_tanh(f[j]); ss += f[j] * f[j]; }
;         ss = wave_sum(ss); const float rinv = rsqrtf(ss * (1.0f / 512.0f) + EPS);
;         if ((lane >> 4) == h) { const int c0 = (lane & 15) * 8; const float* g = p.in[I_SGUNG] + l * 512 + h * 128 + c0;
; #pragma unroll
;             for (int j = 0; j < 8; ++j) Vl[(c0 + j) * 136 + q] = f2bf(f[j] * rinv * g[j]); } }
.LBB0_1282:
	s_or_b64 exec, exec, s[0:1]
	s_waitcnt vmcnt(4)
	v_lshlrev_b32_e32 v22, 16, v18
	v_lshlrev_b32_e32 v23, 16, v19
	v_and_b32_e32 v25, 0xffff0000, v19
	v_mul_f32_e32 v19, 0x3dd2d3e8, v22
	v_fma_f32 v19, -v19, v22, s33
	v_mul_f32_e32 v19, v19, v22
	v_exp_f32_e32 v19, v19
	v_and_b32_e32 v18, 0xffff0000, v18
	v_lshlrev_b32_e32 v26, 16, v20
	v_and_b32_e32 v27, 0xffff0000, v20
	v_add_f32_e32 v19, 1.0, v19
	v_rcp_f32_e32 v19, v19
	v_mul_f32_e32 v20, 0x3dd2d3e8, v25
	v_fma_f32 v20, -v20, v25, s33
	v_mul_f32_e32 v20, v20, v25
	v_mul_f32_e32 v24, v19, v22
	v_mul_f32_e32 v19, 0x3dd2d3e8, v18
	v_fma_f32 v19, -v19, v18, s33
	v_mul_f32_e32 v19, v19, v18
	v_exp_f32_e32 v19, v19
	v_exp_f32_e32 v20, v20
	v_lshlrev_b32_e32 v28, 16, v21
	v_and_b32_e32 v29, 0xffff0000, v21
	v_add_f32_e32 v19, 1.0, v19
	v_rcp_f32_e32 v19, v19
	v_add_f32_e32 v20, 1.0, v20
	v_rcp_f32_e32 v20, v20
	v_mul_f32_e32 v21, 0x3dd2d3e8, v26
	v_mul_f32_e32 v19, v19, v18
	v_mul_f32_e32 v18, 0x3dd2d3e8, v23
	v_fma_f32 v18, -v18, v23, s33
	v_mul_f32_e32 v18, v18, v23
	v_exp_f32_e32 v18, v18
	v_fma_f32 v21, -v21, v26, s33
	v_mul_f32_e32 v22, 0x3dd2d3e8, v27
	v_mul_f32_e32 v21, v21, v26
	v_add_f32_e32 v18, 1.0, v18
	v_rcp_f32_e32 v18, v18
	v_fma_f32 v22, -v22, v27, s33
	v_mul_f32_e32 v20, v20, v25
	v_exp_f32_e32 v21, v21
	v_mul_f32_e32 v18, v18, v23
	v_mul_f32_e32 v23, 0x3dd2d3e8, v28
	v_mul_f32_e32 v22, v22, v27
	v_fma_f32 v23, -v23, v28, s33
	v_mul_f32_e32 v25, 0x3dd2d3e8, v29
	v_exp_f32_e32 v22, v22
	v_mul_f32_e32 v23, v23, v28
	v_fma_f32 v25, -v25, v29, s33
	v_exp_f32_e32 v23, v23
	v_mul_f32_e32 v25, v25, v29
	v_exp_f32_e32 v25, v25
	v_add_f32_e32 v21, 1.0, v21
	v_rcp_f32_e32 v21, v21
	v_add_f32_e32 v22, 1.0, v22
	v_mul_f32_e32 v30, v19, v19
	v_rcp_f32_e32 v22, v22
	v_add_f32_e32 v23, 1.0, v23
	v_fmac_f32_e32 v30, v24, v24
	v_rcp_f32_e32 v23, v23
	v_add_f32_e32 v25, 1.0, v25
	v_fmac_f32_e32 v30, v18, v18
	v_rcp_f32_e32 v25, v25
	v_fmac_f32_e32 v30, v20, v20
	v_mul_f32_e32 v21, v21, v26
	v_fmac_f32_e32 v30, v21, v21
	v_mul_f32_e32 v22, v22, v27
	v_fmac_f32_e32 v30, v22, v22
	v_mul_f32_e32 v23, v23, v28
	v_fmac_f32_e32 v30, v23, v23
	v_mul_f32_e32 v25, v25, v29
	v_fmac_f32_e32 v30, v25, v25
	v_mov_b32_e32 v26, v30
	s_nop 1
	v_permlane32_swap_b32_e32 v26, v30
	s_waitcnt lgkmcnt(0)
	v_add_f32_e32 v26, v30, v26
	v_mov_b32_e32 v27, v26
	s_nop 1
	v_permlane16_swap_b32_e32 v27, v26
	s_waitcnt lgkmcnt(0)
	v_add_f32_e32 v26, v26, v27
	s_nop 1
	v_mov_b32_dpp v27, v26 row_ror:8 row_mask:0xf bank_mask:0xf
	s_waitcnt lgkmcnt(0)
	v_add_f32_e32 v26, v26, v27
	s_nop 1
	v_mov_b32_dpp v27, v26 row_shl:4 row_mask:0xf bank_mask:0x5
	v_mov_b32_dpp v27, v26 row_shr:4 row_mask:0xf bank_mask:0xa
	s_waitcnt lgkmcnt(0)
	v_add_f32_e32 v26, v26, v27
	s_nop 1
	v_mov_b32_dpp v27, v26 quad_perm:[2,3,0,1] row_mask:0xf bank_mask:0xf
	s_waitcnt lgkmcnt(0)
	v_add_f32_e32 v26, v26, v27
	s_nop 1
	v_mov_b32_dpp v27, v26 quad_perm:[1,0,3,2] row_mask:0xf bank_mask:0xf
	s_and_saveexec_b64 s[0:1], vcc
	s_cbranch_execz .LBB0_1284
	s_waitcnt lgkmcnt(0)
	v_add_f32_e32 v26, v26, v27
	v_fmamk_f32 v26, v26, 0x3b000000, v246
	s_mov_b32 s2, 0x800000
	v_cmp_gt_f32_e64 s[2:3], s2, v26
	v_mul_f32_e32 v27, 0x4b800000, v26
	s_nop 0
	v_cndmask_b32_e64 v26, v26, v27, s[2:3]
	v_rsq_f32_e32 v26, v26
	s_nop 0
	v_mul_f32_e32 v27, 0x45800000, v26
	v_cndmask_b32_e64 v34, v26, v27, s[2:3]
	v_mul_f32_e32 v18, v18, v34
	v_mul_f32_e32 v24, v24, v34
	v_mul_f32_e32 v19, v19, v34
	v_mul_f32_e32 v18, v18, v162
	v_cvt_pk_bf16_f32 v18, v18, s0
	ds_write_b16 v169, v18 offset:35382
	v_mul_f32_e32 v18, v20, v34
	v_mul_f32_e32 v18, v18, v163
	v_cvt_pk_bf16_f32 v18, v18, s0
	ds_write_b16 v169, v18 offset:35654
	v_mul_f32_e32 v18, v21, v34
	v_mul_f32_e32 v18, v18, v164
	v_cvt_pk_bf16_f32 v18, v18, s0
	ds_write_b16 v169, v18 offset:35926
	v_mul_f32_e32 v18, v22, v34
	v_mul_f32_e32 v18, v18, v165
	v_cvt_pk_bf16_f32 v18, v18, s0
	ds_write_b16 v169, v18 offset:36198
	v_mul_f32_e32 v18, v23, v34
	v_mul_f32_e32 v18, v18, v166
	v_cvt_pk_bf16_f32 v18, v18, s0
	ds_write_b16 v169, v18 offset:36470
	v_mul_f32_e32 v18, v25, v34
	v_mul_f32_e32 v24, v24, v160
	v_mul_f32_e32 v19, v19, v161
	v_mul_f32_e32 v18, v18, v167
	v_cvt_pk_bf16_f32 v24, v24, s0
	v_cvt_pk_bf16_f32 v19, v19, s0
	v_cvt_pk_bf16_f32 v18, v18, s0
	ds_write_b16 v169, v24 offset:34838
	ds_write_b16 v169, v19 offset:35110
	ds_write_b16 v169, v18 offset:36742
; __device__ __forceinline__ float bflo(unsigned w) { return __uint_as_float(w << 16); }
; __device__ __forceinline__ float bfhi(unsigned w) { return __uint_as_float(w & 0xffff0000u); }
; __device__ __forceinline__ unsigned short f2bf(float f) { return (unsigned short)(cvt_pk_bf16(f, 0.f) & 0xffffu); }
; __device__ __forceinline__ float gelu_tanh(float x) {
;     const float y = x * (-2.3022081986679503f - 0.10294324069457f * x * x);
;     return x * __builtin_amdgcn_rcpf(1.0f + __builtin_amdgcn_exp2f(y));
; }
; __device__ __forceinline__ void sgu_unit(const Params& p, int l, int un, LAS unsigned char* lds) {
;     ...
;     for (int qi = 0; qi < 16; ++qi) { const int q = wave * 16 + qi;
;         const u32x4 v = vv[qi]; float f[8] = {bflo(v.x), bfhi(v.x), bflo(v.y), bfhi(v.y), bflo(v.z), bfhi(v.z), bflo(v.w), bfhi(v.w)}; float ss = 0.f;
; #pragma unroll
;         for (int j = 0; j < 8; ++j) { f[j] = gelu_tanh(f[j]); ss += f[j] * f[j]; }
;         ss = wave_sum(ss); const float rinv = rsqrtf(ss * (1.0f / 512.0f) + EPS);
;         if ((lane >> 4) == h) { const int c0 = (lane & 15) * 8; const float* g = p.in[I_SGUNG] + l * 512 + h * 128 + c0;
; #pragma unroll
;             for (int j = 0; j < 8; ++j) Vl[(c0 + j) * 136 + q] = f2bf(f[j] * rinv * g[j]); } }
.LBB0_1284:
	s_or_b64 exec, exec, s[0:1]
	s_waitcnt vmcnt(3)
	v_lshlrev_b32_e32 v18, 16, v14
	v_lshlrev_b32_e32 v19, 16, v15
	v_and_b32_e32 v21, 0xffff0000, v15
	v_mul_f32_e32 v15, 0x3dd2d3e8, v18
	v_fma_f32 v15, -v15, v18, s33
	v_mul_f32_e32 v15, v15, v18
	v_exp_f32_e32 v15, v15
	v_and_b32_e32 v14, 0xffff0000, v14
	v_lshlrev_b32_e32 v22, 16, v16
	v_and_b32_e32 v23, 0xffff0000, v16
	v_add_f32_e32 v15, 1.0, v15
	v_rcp_f32_e32 v15, v15
	v_mul_f32_e32 v16, 0x3dd2d3e8, v21
	v_fma_f32 v16, -v16, v21, s33
	v_mul_f32_e32 v16, v16, v21
	v_mul_f32_e32 v20, v15, v18
	v_mul_f32_e32 v15, 0x3dd2d3e8, v14
	v_fma_f32 v15, -v15, v14, s33
	v_mul_f32_e32 v15, v15, v14
	v_exp_f32_e32 v15, v15
	v_exp_f32_e32 v16, v16
	v_lshlrev_b32_e32 v24, 16, v17
	v_and_b32_e32 v25, 0xffff0000, v17
	v_add_f32_e32 v15, 1.0, v15
	v_rcp_f32_e32 v15, v15
	v_add_f32_e32 v16, 1.0, v16
	v_rcp_f32_e32 v16, v16
	v_mul_f32_e32 v17, 0x3dd2d3e8, v22
	v_mul_f32_e32 v15, v15, v14
	v_mul_f32_e32 v14, 0x3dd2d3e8, v19
	v_fma_f32 v14, -v14, v19, s33
	v_mul_f32_e32 v14, v14, v19
	v_exp_f32_e32 v14, v14
	v_fma_f32 v17, -v17, v22, s33
	v_mul_f32_e32 v18, 0x3dd2d3e8, v23
	v_mul_f32_e32 v17, v17, v22
	v_add_f32_e32 v14, 1.0, v14
	v_rcp_f32_e32 v14, v14
	v_fma_f32 v18, -v18, v23, s33
	v_mul_f32_e32 v16, v16, v21
	v_exp_f32_e32 v17, v17
	v_mul_f32_e32 v14, v14, v19
	v_mul_f32_e32 v19, 0x3dd2d3e8, v24
	v_mul_f32_e32 v18, v18, v23
	v_fma_f32 v19, -v19, v24, s33
	v_mul_f32_e32 v21, 0x3dd2d3e8, v25
	v_exp_f32_e32 v18, v18
	v_mul_f32_e32 v19, v19, v24
	v_fma_f32 v21, -v21, v25, s33
	v_exp_f32_e32 v19, v19
	v_mul_f32_e32 v21, v21, v25
	v_exp_f32_e32 v21, v21
	v_add_f32_e32 v17, 1.0, v17
	v_rcp_f32_e32 v17, v17
	v_add_f32_e32 v18, 1.0, v18
	v_mul_f32_e32 v26, v15, v15
	v_rcp_f32_e32 v18, v18
	v_add_f32_e32 v19, 1.0, v19
	v_fmac_f32_e32 v26, v20, v20
	v_rcp_f32_e32 v19, v19
	v_add_f32_e32 v21, 1.0, v21
	v_fmac_f32_e32 v26, v14, v14
	v_rcp_f32_e32 v21, v21
	v_fmac_f32_e32 v26, v16, v16
	v_mul_f32_e32 v17, v17, v22
	v_fmac_f32_e32 v26, v17, v17
	v_mul_f32_e32 v18, v18, v23
	v_fmac_f32_e32 v26, v18, v18
	v_mul_f32_e32 v19, v19, v24
	v_fmac_f32_e32 v26, v19, v19
	v_mul_f32_e32 v21, v21, v25
	v_fmac_f32_e32 v26, v21, v21
	v_mov_b32_e32 v22, v26
	s_nop 1
	v_permlane32_swap_b32_e32 v22, v26
	s_waitcnt lgkmcnt(0)
	v_add_f32_e32 v22, v26, v22
	v_mov_b32_e32 v23, v22
	s_nop 1
	v_permlane16_swap_b32_e32 v23, v22
	s_waitcnt lgkmcnt(0)
	v_add_f32_e32 v22, v22, v23
	s_nop 1
	v_mov_b32_dpp v23, v22 row_ror:8 row_mask:0xf bank_mask:0xf
	s_waitcnt lgkmcnt(0)
	v_add_f32_e32 v22, v22, v23
	s_nop 1
	v_mov_b32_dpp v23, v22 row_shl:4 row_mask:0xf bank_mask:0x5
	v_mov_b32_dpp v23, v22 row_shr:4 row_mask:0xf bank_mask:0xa
	s_waitcnt lgkmcnt(0)
	v_add_f32_e32 v22, v22, v23
	s_nop 1
	v_mov_b32_dpp v23, v22 quad_perm:[2,3,0,1] row_mask:0xf bank_mask:0xf
	s_waitcnt lgkmcnt(0)
	v_add_f32_e32 v22, v22, v23
	s_nop 1
	v_mov_b32_dpp v23, v22 quad_perm:[1,0,3,2] row_mask:0xf bank_mask:0xf
	s_and_saveexec_b64 s[0:1], vcc
	s_cbranch_execz .LBB0_1286
	s_waitcnt lgkmcnt(0)
	v_add_f32_e32 v22, v22, v23
	v_fmamk_f32 v22, v22, 0x3b000000, v246
	s_mov_b32 s2, 0x800000
	v_cmp_gt_f32_e64 s[2:3], s2, v22
	v_mul_f32_e32 v23, 0x4b800000, v22
	s_nop 0
	v_cndmask_b32_e64 v22, v22, v23, s[2:3]
	v_rsq_f32_e32 v22, v22
	s_nop 0
	v_mul_f32_e32 v23, 0x45800000, v22
	v_cndmask_b32_e64 v30, v22, v23, s[2:3]
	v_mul_f32_e32 v14, v14, v30
	v_mul_f32_e32 v20, v20, v30
	v_mul_f32_e32 v15, v15, v30
	v_mul_f32_e32 v14, v14, v162
	v_cvt_pk_bf16_f32 v14, v14, s0
	ds_write_b16 v169, v14 offset:35384
	v_mul_f32_e32 v14, v16, v30
	v_mul_f32_e32 v14, v14, v163
	v_cvt_pk_bf16_f32 v14, v14, s0
	ds_write_b16 v169, v14 offset:35656
	v_mul_f32_e32 v14, v17, v30
	v_mul_f32_e32 v14, v14, v164
	v_cvt_pk_bf16_f32 v14, v14, s0
	ds_write_b16 v169, v14 offset:35928
	v_mul_f32_e32 v14, v18, v30
	v_mul_f32_e32 v14, v14, v165
	v_cvt_pk_bf16_f32 v14, v14, s0
	ds_write_b16 v169, v14 offset:36200
	v_mul_f32_e32 v14, v19, v30
	v_mul_f32_e32 v14, v14, v166
	v_cvt_pk_bf16_f32 v14, v14, s0
	ds_write_b16 v169, v14 offset:36472
	v_mul_f32_e32 v14, v21, v30
	v_mul_f32_e32 v20, v20, v160
	v_mul_f32_e32 v15, v15, v161
	v_mul_f32_e32 v14, v14, v167
	v_cvt_pk_bf16_f32 v20, v20, s0
	v_cvt_pk_bf16_f32 v15, v15, s0
	v_cvt_pk_bf16_f32 v14, v14, s0
	ds_write_b16 v169, v20 offset:34840
	ds_write_b16 v169, v15 offset:35112
	ds_write_b16 v169, v14 offset:36744
; __device__ __forceinline__ float bflo(unsigned w) { return __uint_as_float(w << 16); }
; __device__ __forceinline__ float bfhi(unsigned w) { return __uint_as_float(w & 0xffff0000u); }
; __device__ __forceinline__ unsigned short f2bf(float f) { return (unsigned short)(cvt_pk_bf16(f, 0.f) & 0xffffu); }
; __device__ __forceinline__ float gelu_tanh(float x) {
;     const float y = x * (-2.3022081986679503f - 0.10294324069457f * x * x);
;     return x * __builtin_amdgcn_rcpf(1.0f + __builtin_amdgcn_exp2f(y));
; }
; __device__ __forceinline__ void sgu_unit(const Params& p, int l, int un, LAS unsigned char* lds) {
;     ...
;     for (int qi = 0; qi < 16; ++qi) { const int q = wave * 16 + qi;
;         const u32x4 v = vv[qi]; float f[8] = {bflo(v.x), bfhi(v.x), bflo(v.y), bfhi(v.y), bflo(v.z), bfhi(v.z), bflo(v.w), bfhi(v.w)}; float ss = 0.f;
; #pragma unroll
;         for (int j = 0; j < 8; ++j) { f[j] = gelu_tanh(f[j]); ss += f[j] * f[j]; }
;         ss = wave_sum(ss); const float rinv = rsqrtf(ss * (1.0f / 512.0f) + EPS);
;         if ((lane >> 4) == h) { const int c0 = (lane & 15) * 8; const float* g = p.in[I_SGUNG] + l * 512 + h * 128 + c0;
; #pragma unroll
;             for (int j = 0; j < 8; ++j) Vl[(c0 + j) * 136 + q] = f2bf(f[j] * rinv * g[j]); } }
.LBB0_1286:
	s_or_b64 exec, exec, s[0:1]
	s_waitcnt vmcnt(2)
	v_lshlrev_b32_e32 v14, 16, v10
	v_lshlrev_b32_e32 v15, 16, v11
	v_and_b32_e32 v17, 0xffff0000, v11
	v_mul_f32_e32 v11, 0x3dd2d3e8, v14
	v_fma_f32 v11, -v11, v14, s33
	v_mul_f32_e32 v11, v11, v14
	v_exp_f32_e32 v11, v11
	v_and_b32_e32 v10, 0xffff0000, v10
	v_lshlrev_b32_e32 v18, 16, v12
	v_and_b32_e32 v19, 0xffff0000, v12
	v_add_f32_e32 v11, 1.0, v11
	v_rcp_f32_e32 v11, v11
	v_mul_f32_e32 v12, 0x3dd2d3e8, v17
	v_fma_f32 v12, -v12, v17, s33
	v_mul_f32_e32 v12, v12, v17
	v_mul_f32_e32 v16, v11, v14
	v_mul_f32_e32 v11, 0x3dd2d3e8, v10
	v_fma_f32 v11, -v11, v10, s33
	v_mul_f32_e32 v11, v11, v10
	v_exp_f32_e32 v11, v11
	v_exp_f32_e32 v12, v12
	v_lshlrev_b32_e32 v20, 16, v13
	v_and_b32_e32 v21, 0xffff0000, v13
	v_add_f32_e32 v11, 1.0, v11
	v_rcp_f32_e32 v11, v11
	v_add_f32_e32 v12, 1.0, v12
	v_rcp_f32_e32 v12, v12
	v_mul_f32_e32 v13, 0x3dd2d3e8, v18
	v_mul_f32_e32 v11, v11, v10
	v_mul_f32_e32 v10, 0x3dd2d3e8, v15
	v_fma_f32 v10, -v10, v15, s33
	v_mul_f32_e32 v10, v10, v15
	v_exp_f32_e32 v10, v10
	v_fma_f32 v13, -v13, v18, s33
	v_mul_f32_e32 v14, 0x3dd2d3e8, v19
	v_mul_f32_e32 v13, v13, v18
	v_add_f32_e32 v10, 1.0, v10
	v_rcp_f32_e32 v10, v10
	v_fma_f32 v14, -v14, v19, s33
	v_mul_f32_e32 v12, v12, v17
	v_exp_f32_e32 v13, v13
	v_mul_f32_e32 v10, v10, v15
	v_mul_f32_e32 v15, 0x3dd2d3e8, v20
	v_mul_f32_e32 v14, v14, v19
	v_fma_f32 v15, -v15, v20, s33
	v_mul_f32_e32 v17, 0x3dd2d3e8, v21
	v_exp_f32_e32 v14, v14
	v_mul_f32_e32 v15, v15, v20
	v_fma_f32 v17, -v17, v21, s33
	v_exp_f32_e32 v15, v15
	v_mul_f32_e32 v17, v17, v21
	v_exp_f32_e32 v17, v17
	v_add_f32_e32 v13, 1.0, v13
	v_rcp_f32_e32 v13, v13
	v_add_f32_e32 v14, 1.0, v14
	v_mul_f32_e32 v22, v11, v11
	v_rcp_f32_e32 v14, v14
	v_add_f32_e32 v15, 1.0, v15
	v_fmac_f32_e32 v22, v16, v16
	v_rcp_f32_e32 v15, v15
	v_add_f32_e32 v17, 1.0, v17
	v_fmac_f32_e32 v22, v10, v10
	v_rcp_f32_e32 v17, v17
	v_fmac_f32_e32 v22, v12, v12
	v_mul_f32_e32 v13, v13, v18
	v_fmac_f32_e32 v22, v13, v13
	v_mul_f32_e32 v14, v14, v19
	v_fmac_f32_e32 v22, v14, v14
	v_mul_f32_e32 v15, v15, v20
	v_fmac_f32_e32 v22, v15, v15
	v_mul_f32_e32 v17, v17, v21
	v_fmac_f32_e32 v22, v17, v17
	v_mov_b32_e32 v18, v22
	s_nop 1
	v_permlane32_swap_b32_e32 v18, v22
	s_waitcnt lgkmcnt(0)
	v_add_f32_e32 v18, v22, v18
	v_mov_b32_e32 v19, v18
	s_nop 1
	v_permlane16_swap_b32_e32 v19, v18
	s_waitcnt lgkmcnt(0)
	v_add_f32_e32 v18, v18, v19
	s_nop 1
	v_mov_b32_dpp v19, v18 row_ror:8 row_mask:0xf bank_mask:0xf
	s_waitcnt lgkmcnt(0)
	v_add_f32_e32 v18, v18, v19
	s_nop 1
	v_mov_b32_dpp v19, v18 row_shl:4 row_mask:0xf bank_mask:0x5
	v_mov_b32_dpp v19, v18 row_shr:4 row_mask:0xf bank_mask:0xa
	s_waitcnt lgkmcnt(0)
	v_add_f32_e32 v18, v18, v19
	s_nop 1
	v_mov_b32_dpp v19, v18 quad_perm:[2,3,0,1] row_mask:0xf bank_mask:0xf
	s_waitcnt lgkmcnt(0)
	v_add_f32_e32 v18, v18, v19
	s_nop 1
	v_mov_b32_dpp v19, v18 quad_perm:[1,0,3,2] row_mask:0xf bank_mask:0xf
	s_and_saveexec_b64 s[0:1], vcc
	s_cbranch_execz .LBB0_1288
	s_waitcnt lgkmcnt(0)
	v_add_f32_e32 v18, v18, v19
	v_fmamk_f32 v18, v18, 0x3b000000, v246
	s_mov_b32 s2, 0x800000
	v_cmp_gt_f32_e64 s[2:3], s2, v18
	v_mul_f32_e32 v19, 0x4b800000, v18
	s_nop 0
	v_cndmask_b32_e64 v18, v18, v19, s[2:3]
	v_rsq_f32_e32 v18, v18
	s_nop 0
	v_mul_f32_e32 v19, 0x45800000, v18
	v_cndmask_b32_e64 v26, v18, v19, s[2:3]
	v_mul_f32_e32 v10, v10, v26
	v_mul_f32_e32 v16, v16, v26
	v_mul_f32_e32 v11, v11, v26
	v_mul_f32_e32 v10, v10, v162
	v_cvt_pk_bf16_f32 v10, v10, s0
	ds_write_b16 v169, v10 offset:35386
	v_mul_f32_e32 v10, v12, v26
	v_mul_f32_e32 v10, v10, v163
	v_cvt_pk_bf16_f32 v10, v10, s0
	ds_write_b16 v169, v10 offset:35658
	v_mul_f32_e32 v10, v13, v26
	v_mul_f32_e32 v10, v10, v164
	v_cvt_pk_bf16_f32 v10, v10, s0
	ds_write_b16 v169, v10 offset:35930
	v_mul_f32_e32 v10, v14, v26
	v_mul_f32_e32 v10, v10, v165
	v_cvt_pk_bf16_f32 v10, v10, s0
	ds_write_b16 v169, v10 offset:36202
	v_mul_f32_e32 v10, v15, v26
	v_mul_f32_e32 v10, v10, v166
	v_cvt_pk_bf16_f32 v10, v10, s0
	ds_write_b16 v169, v10 offset:36474
	v_mul_f32_e32 v10, v17, v26
	v_mul_f32_e32 v16, v16, v160
	v_mul_f32_e32 v11, v11, v161
	v_mul_f32_e32 v10, v10, v167
	v_cvt_pk_bf16_f32 v16, v16, s0
	v_cvt_pk_bf16_f32 v11, v11, s0
	v_cvt_pk_bf16_f32 v10, v10, s0
	ds_write_b16 v169, v16 offset:34842
	ds_write_b16 v169, v11 offset:35114
	ds_write_b16 v169, v10 offset:36746
; __device__ __forceinline__ float bflo(unsigned w) { return __uint_as_float(w << 16); }
; __device__ __forceinline__ float bfhi(unsigned w) { return __uint_as_float(w & 0xffff0000u); }
; __device__ __forceinline__ unsigned short f2bf(float f) { return (unsigned short)(cvt_pk_bf16(f, 0.f) & 0xffffu); }
; __device__ __forceinline__ float gelu_tanh(float x) {
;     const float y = x * (-2.3022081986679503f - 0.10294324069457f * x * x);
;     return x * __builtin_amdgcn_rcpf(1.0f + __builtin_amdgcn_exp2f(y));
; }
; __device__ __forceinline__ void sgu_unit(const Params& p, int l, int un, LAS unsigned char* lds) {
;     ...
;     for (int qi = 0; qi < 16; ++qi) { const int q = wave * 16 + qi;
;         const u32x4 v = vv[qi]; float f[8] = {bflo(v.x), bfhi(v.x), bflo(v.y), bfhi(v.y), bflo(v.z), bfhi(v.z), bflo(v.w), bfhi(v.w)}; float ss = 0.f;
; #pragma unroll
;         for (int j = 0; j < 8; ++j) { f[j] = gelu_tanh(f[j]); ss += f[j] * f[j]; }
;         ss = wave_sum(ss); const float rinv = rsqrtf(ss * (1.0f / 512.0f) + EPS);
;         if ((lane >> 4) == h) { const int c0 = (lane & 15) * 8; const float* g = p.in[I_SGUNG] + l * 512 + h * 128 + c0;
; #pragma unroll
;             for (int j = 0; j < 8; ++j) Vl[(c0 + j) * 136 + q] = f2bf(f[j] * rinv * g[j]); } }
.LBB0_1288:
	s_or_b64 exec, exec, s[0:1]
	s_waitcnt vmcnt(1)
	v_lshlrev_b32_e32 v10, 16, v6
	v_lshlrev_b32_e32 v11, 16, v7
	v_and_b32_e32 v13, 0xffff0000, v7
	v_mul_f32_e32 v7, 0x3dd2d3e8, v10
	v_fma_f32 v7, -v7, v10, s33
	v_mul_f32_e32 v7, v7, v10
	v_exp_f32_e32 v7, v7
	v_and_b32_e32 v6, 0xffff0000, v6
	v_lshlrev_b32_e32 v14, 16, v8
	v_and_b32_e32 v15, 0xffff0000, v8
	v_add_f32_e32 v7, 1.0, v7
	v_rcp_f32_e32 v7, v7
	v_mul_f32_e32 v8, 0x3dd2d3e8, v13
	v_fma_f32 v8, -v8, v13, s33
	v_mul_f32_e32 v8, v8, v13
	v_mul_f32_e32 v12, v7, v10
	v_mul_f32_e32 v7, 0x3dd2d3e8, v6
	v_fma_f32 v7, -v7, v6, s33
	v_mul_f32_e32 v7, v7, v6
	v_exp_f32_e32 v7, v7
	v_exp_f32_e32 v8, v8
	v_lshlrev_b32_e32 v16, 16, v9
	v_and_b32_e32 v17, 0xffff0000, v9
	v_add_f32_e32 v7, 1.0, v7
	v_rcp_f32_e32 v7, v7
	v_add_f32_e32 v8, 1.0, v8
	v_rcp_f32_e32 v8, v8
	v_mul_f32_e32 v9, 0x3dd2d3e8, v14
	v_mul_f32_e32 v7, v7, v6
	v_mul_f32_e32 v6, 0x3dd2d3e8, v11
	v_fma_f32 v6, -v6, v11, s33
	v_mul_f32_e32 v6, v6, v11
	v_exp_f32_e32 v6, v6
	v_fma_f32 v9, -v9, v14, s33
	v_mul_f32_e32 v10, 0x3dd2d3e8, v15
	v_mul_f32_e32 v9, v9, v14
	v_add_f32_e32 v6, 1.0, v6
	v_rcp_f32_e32 v6, v6
	v_fma_f32 v10, -v10, v15, s33
	v_mul_f32_e32 v8, v8, v13
	v_exp_f32_e32 v9, v9
	v_mul_f32_e32 v6, v6, v11
	v_mul_f32_e32 v11, 0x3dd2d3e8, v16
	v_mul_f32_e32 v10, v10, v15
	v_fma_f32 v11, -v11, v16, s33
	v_mul_f32_e32 v13, 0x3dd2d3e8, v17
	v_exp_f32_e32 v10, v10
	v_mul_f32_e32 v11, v11, v16
	v_fma_f32 v13, -v13, v17, s33
	v_exp_f32_e32 v11, v11
	v_mul_f32_e32 v13, v13, v17
	v_exp_f32_e32 v13, v13
	v_add_f32_e32 v9, 1.0, v9
	v_rcp_f32_e32 v9, v9
	v_add_f32_e32 v10, 1.0, v10
	v_mul_f32_e32 v18, v7, v7
	v_rcp_f32_e32 v10, v10
	v_add_f32_e32 v11, 1.0, v11
	v_fmac_f32_e32 v18, v12, v12
	v_rcp_f32_e32 v11, v11
	v_add_f32_e32 v13, 1.0, v13
	v_fmac_f32_e32 v18, v6, v6
	v_rcp_f32_e32 v13, v13
	v_fmac_f32_e32 v18, v8, v8
	v_mul_f32_e32 v9, v9, v14
	v_fmac_f32_e32 v18, v9, v9
	v_mul_f32_e32 v10, v10, v15
	v_fmac_f32_e32 v18, v10, v10
	v_mul_f32_e32 v11, v11, v16
	v_fmac_f32_e32 v18, v11, v11
	v_mul_f32_e32 v13, v13, v17
	v_fmac_f32_e32 v18, v13, v13
	v_mov_b32_e32 v14, v18
	s_nop 1
	v_permlane32_swap_b32_e32 v14, v18
	s_waitcnt lgkmcnt(0)
	v_add_f32_e32 v14, v18, v14
	v_mov_b32_e32 v15, v14
	s_nop 1
	v_permlane16_swap_b32_e32 v15, v14
	s_waitcnt lgkmcnt(0)
	v_add_f32_e32 v14, v14, v15
	s_nop 1
	v_mov_b32_dpp v15, v14 row_ror:8 row_mask:0xf bank_mask:0xf
	s_waitcnt lgkmcnt(0)
	v_add_f32_e32 v14, v14, v15
	s_nop 1
	v_mov_b32_dpp v15, v14 row_shl:4 row_mask:0xf bank_mask:0x5
	v_mov_b32_dpp v15, v14 row_shr:4 row_mask:0xf bank_mask:0xa
	s_waitcnt lgkmcnt(0)
	v_add_f32_e32 v14, v14, v15
	s_nop 1
	v_mov_b32_dpp v15, v14 quad_perm:[2,3,0,1] row_mask:0xf bank_mask:0xf
	s_waitcnt lgkmcnt(0)
	v_add_f32_e32 v14, v14, v15
	s_nop 1
	v_mov_b32_dpp v15, v14 quad_perm:[1,0,3,2] row_mask:0xf bank_mask:0xf
	s_and_saveexec_b64 s[0:1], vcc
	s_cbranch_execz .LBB0_1290
	s_waitcnt lgkmcnt(0)
	v_add_f32_e32 v14, v14, v15
	v_fmamk_f32 v14, v14, 0x3b000000, v246
	s_mov_b32 s2, 0x800000
	v_cmp_gt_f32_e64 s[2:3], s2, v14
	v_mul_f32_e32 v15, 0x4b800000, v14
	s_nop 0
	v_cndmask_b32_e64 v14, v14, v15, s[2:3]
	v_rsq_f32_e32 v14, v14
	s_nop 0
	v_mul_f32_e32 v15, 0x45800000, v14
	v_cndmask_b32_e64 v22, v14, v15, s[2:3]
	v_mul_f32_e32 v6, v6, v22
	v_mul_f32_e32 v12, v12, v22
	v_mul_f32_e32 v7, v7, v22
	v_mul_f32_e32 v6, v6, v162
	v_cvt_pk_bf16_f32 v6, v6, s0
	ds_write_b16 v169, v6 offset:35388
	v_mul_f32_e32 v6, v8, v22
	v_mul_f32_e32 v6, v6, v163
	v_cvt_pk_bf16_f32 v6, v6, s0
	ds_write_b16 v169, v6 offset:35660
	v_mul_f32_e32 v6, v9, v22
	v_mul_f32_e32 v6, v6, v164
	v_cvt_pk_bf16_f32 v6, v6, s0
	ds_write_b16 v169, v6 offset:35932
	v_mul_f32_e32 v6, v10, v22
	v_mul_f32_e32 v6, v6, v165
	v_cvt_pk_bf16_f32 v6, v6, s0
	ds_write_b16 v169, v6 offset:36204
	v_mul_f32_e32 v6, v11, v22
	v_mul_f32_e32 v6, v6, v166
	v_cvt_pk_bf16_f32 v6, v6, s0
	ds_write_b16 v169, v6 offset:36476
	v_mul_f32_e32 v6, v13, v22
	v_mul_f32_e32 v12, v12, v160
	v_mul_f32_e32 v7, v7, v161
	v_mul_f32_e32 v6, v6, v167
	v_cvt_pk_bf16_f32 v12, v12, s0
	v_cvt_pk_bf16_f32 v7, v7, s0
	v_cvt_pk_bf16_f32 v6, v6, s0
	ds_write_b16 v169, v12 offset:34844
	ds_write_b16 v169, v7 offset:35116
	ds_write_b16 v169, v6 offset:36748
; __device__ __forceinline__ float bflo(unsigned w) { return __uint_as_float(w << 16); }
; __device__ __forceinline__ float bfhi(unsigned w) { return __uint_as_float(w & 0xffff0000u); }
; __device__ __forceinline__ unsigned short f2bf(float f) { return (unsigned short)(cvt_pk_bf16(f, 0.f) & 0xffffu); }
; __device__ __forceinline__ float gelu_tanh(float x) {
;     const float y = x * (-2.3022081986679503f - 0.10294324069457f * x * x);
;     return x * __builtin_amdgcn_rcpf(1.0f + __builtin_amdgcn_exp2f(y));
; }
; __device__ __forceinline__ void sgu_unit(const Params& p, int l, int un, LAS unsigned char* lds) {
;     ...
;     for (int qi = 0; qi < 16; ++qi) { const int q = wave * 16 + qi;
;         const u32x4 v = vv[qi]; float f[8] = {bflo(v.x), bfhi(v.x), bflo(v.y), bfhi(v.y), bflo(v.z), bfhi(v.z), bflo(v.w), bfhi(v.w)}; float ss = 0.f;
; #pragma unroll
;         for (int j = 0; j < 8; ++j) { f[j] = gelu_tanh(f[j]); ss += f[j] * f[j]; }
;         ss = wave_sum(ss); const float rinv = rsqrtf(ss * (1.0f / 512.0f) + EPS);
;         if ((lane >> 4) == h) { const int c0 = (lane & 15) * 8; const float* g = p.in[I_SGUNG] + l * 512 + h * 128 + c0;
; #pragma unroll
;             for (int j = 0; j < 8; ++j) Vl[(c0 + j) * 136 + q] = f2bf(f[j] * rinv * g[j]); } }
.LBB0_1290:
	s_or_b64 exec, exec, s[0:1]
	s_waitcnt vmcnt(0)
	v_lshlrev_b32_e32 v6, 16, v2
	v_lshlrev_b32_e32 v7, 16, v3
	v_and_b32_e32 v9, 0xffff0000, v3
	v_mul_f32_e32 v3, 0x3dd2d3e8, v6
	v_fma_f32 v3, -v3, v6, s33
	v_mul_f32_e32 v3, v3, v6
	v_exp_f32_e32 v3, v3
	v_and_b32_e32 v2, 0xffff0000, v2
	v_lshlrev_b32_e32 v10, 16, v4
	v_and_b32_e32 v11, 0xffff0000, v4
	v_add_f32_e32 v3, 1.0, v3
	v_rcp_f32_e32 v3, v3
	v_mul_f32_e32 v4, 0x3dd2d3e8, v9
	v_fma_f32 v4, -v4, v9, s33
	v_mul_f32_e32 v4, v4, v9
	v_mul_f32_e32 v8, v3, v6
	v_mul_f32_e32 v3, 0x3dd2d3e8, v2
	v_fma_f32 v3, -v3, v2, s33
	v_mul_f32_e32 v3, v3, v2
	v_exp_f32_e32 v3, v3
	v_exp_f32_e32 v4, v4
	v_lshlrev_b32_e32 v12, 16, v5
	v_and_b32_e32 v13, 0xffff0000, v5
	v_add_f32_e32 v3, 1.0, v3
	v_rcp_f32_e32 v3, v3
	v_add_f32_e32 v4, 1.0, v4
	v_rcp_f32_e32 v4, v4
	v_mul_f32_e32 v5, 0x3dd2d3e8, v10
	v_mul_f32_e32 v3, v3, v2
	v_mul_f32_e32 v2, 0x3dd2d3e8, v7
	v_fma_f32 v2, -v2, v7, s33
	v_mul_f32_e32 v2, v2, v7
	v_exp_f32_e32 v2, v2
	v_fma_f32 v5, -v5, v10, s33
	v_mul_f32_e32 v6, 0x3dd2d3e8, v11
	v_mul_f32_e32 v5, v5, v10
	v_add_f32_e32 v2, 1.0, v2
	v_rcp_f32_e32 v2, v2
	v_fma_f32 v6, -v6, v11, s33
	v_mul_f32_e32 v4, v4, v9
	v_exp_f32_e32 v5, v5
	v_mul_f32_e32 v2, v2, v7
	v_mul_f32_e32 v7, 0x3dd2d3e8, v12
	v_mul_f32_e32 v6, v6, v11
	v_fma_f32 v7, -v7, v12, s33
	v_mul_f32_e32 v9, 0x3dd2d3e8, v13
	v_exp_f32_e32 v6, v6
	v_mul_f32_e32 v7, v7, v12
	v_fma_f32 v9, -v9, v13, s33
	v_exp_f32_e32 v7, v7
	v_mul_f32_e32 v9, v9, v13
	v_exp_f32_e32 v9, v9
	v_add_f32_e32 v5, 1.0, v5
	v_rcp_f32_e32 v5, v5
	v_add_f32_e32 v6, 1.0, v6
	v_mul_f32_e32 v14, v3, v3
	v_rcp_f32_e32 v6, v6
	v_add_f32_e32 v7, 1.0, v7
	v_fmac_f32_e32 v14, v8, v8
	v_rcp_f32_e32 v7, v7
	v_add_f32_e32 v9, 1.0, v9
	v_fmac_f32_e32 v14, v2, v2
	v_rcp_f32_e32 v9, v9
	v_fmac_f32_e32 v14, v4, v4
	v_mul_f32_e32 v5, v5, v10
	v_fmac_f32_e32 v14, v5, v5
	v_mul_f32_e32 v6, v6, v11
	v_fmac_f32_e32 v14, v6, v6
	v_mul_f32_e32 v7, v7, v12
	v_fmac_f32_e32 v14, v7, v7
	v_mul_f32_e32 v9, v9, v13
	v_fmac_f32_e32 v14, v9, v9
	v_mov_b32_e32 v10, v14
	s_nop 1
	v_permlane32_swap_b32_e32 v10, v14
	s_waitcnt lgkmcnt(0)
	v_add_f32_e32 v10, v14, v10
	v_mov_b32_e32 v11, v10
	s_nop 1
	v_permlane16_swap_b32_e32 v11, v10
	s_waitcnt lgkmcnt(0)
	v_add_f32_e32 v10, v10, v11
	s_nop 1
	v_mov_b32_dpp v11, v10 row_ror:8 row_mask:0xf bank_mask:0xf
	s_waitcnt lgkmcnt(0)
	v_add_f32_e32 v10, v10, v11
	s_nop 1
	v_mov_b32_dpp v11, v10 row_shl:4 row_mask:0xf bank_mask:0x5
	v_mov_b32_dpp v11, v10 row_shr:4 row_mask:0xf bank_mask:0xa
	s_waitcnt lgkmcnt(0)
	v_add_f32_e32 v10, v10, v11
	s_nop 1
	v_mov_b32_dpp v11, v10 quad_perm:[2,3,0,1] row_mask:0xf bank_mask:0xf
	s_waitcnt lgkmcnt(0)
	v_add_f32_e32 v10, v10, v11
	s_nop 1
	v_mov_b32_dpp v11, v10 quad_perm:[1,0,3,2] row_mask:0xf bank_mask:0xf
	s_and_saveexec_b64 s[0:1], vcc
	s_cbranch_execz .LBB0_1292
	s_waitcnt lgkmcnt(0)
	v_add_f32_e32 v10, v10, v11
	v_fmamk_f32 v10, v10, 0x3b000000, v246
	s_mov_b32 s2, 0x800000
	v_cmp_gt_f32_e32 vcc, s2, v10
	v_mul_f32_e32 v11, 0x4b800000, v10
	s_nop 0
	v_cndmask_b32_e32 v10, v10, v11, vcc
	v_rsq_f32_e32 v10, v10
	s_nop 0
	v_mul_f32_e32 v11, 0x45800000, v10
	v_cndmask_b32_e32 v18, v10, v11, vcc
	v_mul_f32_e32 v2, v2, v18
	v_mul_f32_e32 v8, v8, v18
	v_mul_f32_e32 v3, v3, v18
	v_mul_f32_e32 v2, v2, v162
	v_cvt_pk_bf16_f32 v2, v2, s0
	ds_write_b16 v169, v2 offset:35390
	v_mul_f32_e32 v2, v4, v18
	v_mul_f32_e32 v2, v2, v163
	v_cvt_pk_bf16_f32 v2, v2, s0
	ds_write_b16 v169, v2 offset:35662
	v_mul_f32_e32 v2, v5, v18
	v_mul_f32_e32 v2, v2, v164
	v_cvt_pk_bf16_f32 v2, v2, s0
	ds_write_b16 v169, v2 offset:35934
	v_mul_f32_e32 v2, v6, v18
	v_mul_f32_e32 v2, v2, v165
	v_cvt_pk_bf16_f32 v2, v2, s0
	ds_write_b16 v169, v2 offset:36206
	v_mul_f32_e32 v2, v7, v18
	v_mul_f32_e32 v2, v2, v166
	v_cvt_pk_bf16_f32 v2, v2, s0
	ds_write_b16 v169, v2 offset:36478
	v_mul_f32_e32 v2, v9, v18
	v_mul_f32_e32 v8, v8, v160
	v_mul_f32_e32 v3, v3, v161
	v_mul_f32_e32 v2, v2, v167
	v_cvt_pk_bf16_f32 v8, v8, s0
	v_cvt_pk_bf16_f32 v3, v3, s0
	v_cvt_pk_bf16_f32 v2, v2, s0
	ds_write_b16 v169, v8 offset:34846
	ds_write_b16 v169, v3 offset:35118
	ds_write_b16 v169, v2 offset:36750

; __device__ __forceinline__ void sgu_unit(const Params& p, int l, int un, LAS unsigned char* lds) {
;     ...
;     const float* Wg = p.in[I_SGUW] + ((size_t)l * 4 + h) * 128 * 128;
;     f32x4 wq[8]; u32x4 vv[16];
; #pragma unroll
;     for (int i = 0; i < 8; ++i) wq[i] = *(const f32x4*)(Wg + (i * 512 + tid) * 4);
; #pragma unroll
;     for (int qi = 0; qi < 16; ++qi) vv[qi] = *(const u32x4*)(P + (size_t)(row0 + wave * 16 + qi) * INP + C_SGU_V + lane * 8);
; __global__ void __launch_bounds__(512, 2) fwd(Params p) {
;     ...
;             if (c < (l == 0 ? 72 : 64) || G != 256) pg8::gemm_phase(lds, pg8::Desc{512, 512, 512}, S, E);
;             else { const int un = (l == 0 ? 128 + (c - 72) : 160 + (c - 64)); if (un < (l == 0 ? B_SGU : 256)) sgu_unit(p, l, un, lds); }
.LBB0_1393:
	s_andn2_b64 vcc, exec, s[0:1]
	s_cbranch_vccnz .LBB0_1501
	v_readlane_b32 s0, v252, 5
	v_readlane_b32 s1, v252, 6
	s_lshl_b32 s4, s0, 9
	v_readlane_b32 s0, v252, 20
	v_readlane_b32 s1, v252, 21
	s_and_b64 s[0:1], s[0:1], exec
	s_cselect_b32 s0, 0x48, 64
	s_cmp_ge_i32 s92, s0
	v_readlane_b32 s12, v255, 40
	s_cselect_b64 s[2:3], -1, 0
	v_readlane_b32 s13, v255, 41
	s_and_b64 s[2:3], s[12:13], s[2:3]
	s_mov_b64 s[0:1], -1
	s_and_b64 vcc, exec, s[2:3]
	s_cbranch_vccz .LBB0_1430
	v_readlane_b32 s2, v252, 20
	v_readlane_b32 s3, v252, 21
	s_and_b64 s[0:1], s[2:3], exec
	s_cselect_b32 s0, 56, 0x60
	s_add_i32 s0, s0, s92
	s_and_b64 s[2:3], s[2:3], exec
	s_movk_i32 s1, 0x120
	s_cselect_b32 s1, s1, 0x100
	s_cmp_ge_u32 s0, s1
	s_cbranch_scc1 .LBB0_1429
	v_readlane_b32 s44, v251, 16
	s_lshl_b32 s12, s0, 5
	v_readlane_b32 s0, v253, 39
	v_readlane_b32 s48, v251, 20
	v_readlane_b32 s49, v251, 21
	s_or_b32 s40, s4, s0
	s_mov_b32 s41, s5
	v_readlane_b32 s50, v251, 22
	v_readlane_b32 s51, v251, 23
	v_readlane_b32 s52, v251, 24
	v_readlane_b32 s53, v251, 25
	v_readlane_b32 s54, v251, 26
	v_readlane_b32 s55, v251, 27
	s_mov_b64 s[16:17], s[48:49]
	s_lshl_b64 s[0:1], s[40:41], 9
	s_mov_b64 s[18:19], s[50:51]
	s_waitcnt vmcnt(0)
	v_mov_b32_e32 v64, v0
	s_add_u32 s2, s18, s0
	s_addc_u32 s3, s19, s1
	v_lshlrev_b32_e32 v2, 2, v64
	v_ashrrev_i32_e32 v3, 31, v2
	v_add_u32_e32 v62, 0x800, v2
	s_mov_b64 s[14:15], 0
	v_lshl_add_u64 v[4:5], v[2:3], 2, s[2:3]
	v_ashrrev_i32_e32 v63, 31, v62
	v_lshl_add_u64 v[6:7], v[62:63], 2, s[2:3]
	global_load_dwordx4 v[66:69], v[4:5], off
	global_load_dwordx4 v[70:73], v[6:7], off
	v_add_u32_e32 v102, 0x1000, v2
	v_ashrrev_i32_e32 v103, 31, v102
	v_add_u32_e32 v104, 0x1800, v2
	v_lshl_add_u64 v[4:5], v[102:103], 2, s[2:3]
	v_ashrrev_i32_e32 v105, 31, v104
	v_lshl_add_u64 v[6:7], v[104:105], 2, s[2:3]
	global_load_dwordx4 v[74:77], v[4:5], off
	global_load_dwordx4 v[78:81], v[6:7], off
	s_and_b32 s12, s12, 0x7fffff80
	s_lshl_b64 s[0:1], s[4:5], 2
	v_readlane_b32 s13, v253, 41
	v_add_u32_e32 v106, 0x2000, v2
	s_add_u32 s0, s13, s0
	v_readlane_b32 s13, v253, 42
	v_ashrrev_i32_e32 v107, 31, v106
	v_add_u32_e32 v108, 0x2800, v2
	s_addc_u32 s1, s13, s1
	v_lshl_add_u64 v[4:5], v[106:107], 2, s[2:3]
	v_ashrrev_i32_e32 v109, 31, v108
	s_add_u32 s36, s84, s14
	v_lshl_add_u64 v[6:7], v[108:109], 2, s[2:3]
	global_load_dwordx4 v[82:85], v[4:5], off
	global_load_dwordx4 v[86:89], v[6:7], off
	s_addc_u32 s37, s85, s15
	v_add_u32_e32 v110, 0x3000, v2
	v_add_u32_e32 v112, 0x3800, v2
	s_add_u32 s38, s36, 0x1f1b8000
	v_ashrrev_i32_e32 v111, 31, v110
	v_ashrrev_i32_e32 v113, 31, v112
	v_ashrrev_i32_e32 v103, 6, v64
	s_addc_u32 s39, s37, 0
	v_lshl_add_u64 v[4:5], v[110:111], 2, s[2:3]
	v_lshl_add_u64 v[2:3], v[112:113], 2, s[2:3]
	v_lshlrev_b32_e32 v65, 4, v103
	v_and_b32_e32 v8, 63, v64
	global_load_dwordx4 v[90:93], v[4:5], off
	global_load_dwordx4 v[94:97], v[2:3], off
	v_add_u32_e32 v9, s12, v65
	v_mov_b64_e32 v[2:3], s[38:39]
	s_movk_i32 s13, 0x1e00
	v_mad_i64_i32 v[4:5], s[2:3], v9, s13, v[2:3]
	v_lshlrev_b32_e32 v206, 4, v8
	v_or_b32_e32 v6, 1, v9
	v_lshl_add_u64 v[4:5], v[4:5], 0, v[206:207]
	v_mad_i64_i32 v[6:7], s[2:3], v6, s13, v[2:3]
	v_lshl_add_u64 v[6:7], v[6:7], 0, v[206:207]
	global_load_dwordx4 v[98:101], v[4:5], off offset:1024
	global_load_dwordx4 v[58:61], v[6:7], off offset:1024
	v_or_b32_e32 v4, 2, v9
	v_or_b32_e32 v6, 3, v9
	v_mad_i64_i32 v[4:5], s[2:3], v4, s13, v[2:3]
	v_mad_i64_i32 v[6:7], s[2:3], v6, s13, v[2:3]
	v_lshl_add_u64 v[4:5], v[4:5], 0, v[206:207]
	v_lshl_add_u64 v[6:7], v[6:7], 0, v[206:207]
	global_load_dwordx4 v[54:57], v[4:5], off offset:1024
	global_load_dwordx4 v[50:53], v[6:7], off offset:1024
	v_or_b32_e32 v4, 4, v9
	v_or_b32_e32 v6, 5, v9
	v_mad_i64_i32 v[4:5], s[2:3], v4, s13, v[2:3]
	v_mad_i64_i32 v[6:7], s[2:3], v6, s13, v[2:3]
	v_lshl_add_u64 v[4:5], v[4:5], 0, v[206:207]
	v_lshl_add_u64 v[6:7], v[6:7], 0, v[206:207]
	global_load_dwordx4 v[46:49], v[4:5], off offset:1024
	global_load_dwordx4 v[42:45], v[6:7], off offset:1024
	v_or_b32_e32 v4, 6, v9
	v_or_b32_e32 v6, 7, v9
	v_mad_i64_i32 v[4:5], s[2:3], v4, s13, v[2:3]
	v_mad_i64_i32 v[6:7], s[2:3], v6, s13, v[2:3]
	v_lshl_add_u64 v[4:5], v[4:5], 0, v[206:207]
	v_lshl_add_u64 v[6:7], v[6:7], 0, v[206:207]
	global_load_dwordx4 v[38:41], v[4:5], off offset:1024
	global_load_dwordx4 v[34:37], v[6:7], off offset:1024
	v_or_b32_e32 v4, 8, v9
	v_or_b32_e32 v6, 9, v9
	v_mad_i64_i32 v[4:5], s[2:3], v4, s13, v[2:3]
	v_mad_i64_i32 v[6:7], s[2:3], v6, s13, v[2:3]
	v_lshl_add_u64 v[4:5], v[4:5], 0, v[206:207]
	v_lshl_add_u64 v[6:7], v[6:7], 0, v[206:207]
	global_load_dwordx4 v[30:33], v[4:5], off offset:1024
	global_load_dwordx4 v[26:29], v[6:7], off offset:1024
	v_or_b32_e32 v4, 10, v9
	v_or_b32_e32 v6, 11, v9
	v_mad_i64_i32 v[4:5], s[2:3], v4, s13, v[2:3]
	v_mad_i64_i32 v[6:7], s[2:3], v6, s13, v[2:3]
	v_lshl_add_u64 v[4:5], v[4:5], 0, v[206:207]
	v_lshl_add_u64 v[6:7], v[6:7], 0, v[206:207]
	global_load_dwordx4 v[22:25], v[4:5], off offset:1024
	global_load_dwordx4 v[18:21], v[6:7], off offset:1024
	v_or_b32_e32 v4, 12, v9
	v_or_b32_e32 v6, 13, v9
	v_mad_i64_i32 v[4:5], s[2:3], v4, s13, v[2:3]
	v_mad_i64_i32 v[6:7], s[2:3], v6, s13, v[2:3]
	v_lshl_add_u64 v[4:5], v[4:5], 0, v[206:207]
	v_lshl_add_u64 v[6:7], v[6:7], 0, v[206:207]
	v_lshlrev_b32_e32 v105, 3, v64
	global_load_dwordx4 v[14:17], v[4:5], off offset:1024
	global_load_dwordx4 v[10:13], v[6:7], off offset:1024
	v_or_b32_e32 v4, 14, v9
	v_or_b32_e32 v6, 15, v9
	v_and_b32_e32 v63, 0xf8, v105
	v_mad_i64_i32 v[4:5], s[2:3], v4, s13, v[2:3]
	v_mad_i64_i32 v[2:3], s[2:3], v6, s13, v[2:3]
	v_add_u32_e32 v114, 0, v63
	v_bfe_i32 v63, v64, 5, 25
	s_movk_i32 s13, 0x110
	v_lshl_add_u64 v[4:5], v[4:5], 0, v[206:207]
	v_lshl_add_u64 v[2:3], v[2:3], 0, v[206:207]
	s_waitcnt vmcnt(21)
; #define LAS __attribute__((address_space(3)))
; __device__ __forceinline__ unsigned cvt_pk_bf16(float lo, float hi) { const f32x2 v = {lo, hi}; const bf16x2_t b = __builtin_convertvector(v, bf16x2_t); return __builtin_bit_cast(unsigned, b); }
; __device__ __forceinline__ float bflo(unsigned w) { return __uint_as_float(w << 16); }
; __device__ __forceinline__ float bfhi(unsigned w) { return __uint_as_float(w & 0xffff0000u); }
; __device__ __forceinline__ float wave_sum(float v) {
; #pragma unroll
;     for (int o = 32; o >= 1; o >>= 1) v += __shfl_xor(v, o);
;     return v;
; __device__ __forceinline__ void sgu_unit(const Params& p, int l, int un, LAS unsigned char* lds) {
;     ...
;     for (int i = 0; i < 8; ++i) { const int e4 = (i * 512 + tid) * 4, r = e4 >> 7, c = e4 & 127; const f32x4 v = wq[i];
;         u32x2 w; w.x = cvt_pk_bf16(v[0], v[1]); w.y = cvt_pk_bf16(v[2], v[3]); *(LAS u32x2*)(Wl + r * 136 + c) = w; }
; #pragma unroll
;     for (int qi = 0; qi < 16; ++qi) { const int q = wave * 16 + qi;
;         const u32x4 v = vv[qi]; float f[8] = {bflo(v.x), bfhi(v.x), bflo(v.y), bfhi(v.y), bflo(v.z), bfhi(v.z), bflo(v.w), bfhi(v.w)}; float ss = 0.f;
; #pragma unroll
;         for (int j = 0; j < 8; ++j) { f[j] = gelu_tanh(f[j]); ss += f[j] * f[j]; }
;         ss = wave_sum(ss); const float rinv = rsqrtf(ss * (1.0f / 512.0f) + EPS);
	v_cvt_pk_bf16_f32 v66, v66, v67
	v_cvt_pk_bf16_f32 v67, v68, v69
	v_mad_u64_u32 v[68:69], s[2:3], v63, s13, v[114:115]
	global_load_dwordx4 v[6:9], v[4:5], off offset:1024
	s_nop 0
	global_load_dwordx4 v[2:5], v[2:3], off offset:1024
	ds_write_b64 v68, v[66:67]
	v_ashrrev_i32_e32 v66, 7, v62
	s_waitcnt vmcnt(22)
	v_cvt_pk_bf16_f32 v62, v70, v71
	v_cvt_pk_bf16_f32 v63, v72, v73
	v_mad_u64_u32 v[66:67], s[2:3], v66, s13, v[114:115]
	ds_write_b64 v66, v[62:63]
	v_ashrrev_i32_e32 v66, 7, v102
	s_waitcnt vmcnt(21)
	v_cvt_pk_bf16_f32 v62, v74, v75
	v_cvt_pk_bf16_f32 v63, v76, v77
	v_mad_u64_u32 v[66:67], s[2:3], v66, s13, v[114:115]
	ds_write_b64 v66, v[62:63]
	v_ashrrev_i32_e32 v66, 7, v104
	s_waitcnt vmcnt(20)
	v_cvt_pk_bf16_f32 v62, v78, v79
	v_cvt_pk_bf16_f32 v63, v80, v81
	v_mad_u64_u32 v[66:67], s[2:3], v66, s13, v[114:115]
	ds_write_b64 v66, v[62:63]
	v_ashrrev_i32_e32 v66, 7, v106
	s_waitcnt vmcnt(19)
	v_cvt_pk_bf16_f32 v62, v82, v83
	v_cvt_pk_bf16_f32 v63, v84, v85
	v_mad_u64_u32 v[66:67], s[2:3], v66, s13, v[114:115]
	ds_write_b64 v66, v[62:63]
	v_ashrrev_i32_e32 v66, 7, v108
	s_waitcnt vmcnt(18)
	v_cvt_pk_bf16_f32 v62, v86, v87
	v_cvt_pk_bf16_f32 v63, v88, v89
	v_mad_u64_u32 v[66:67], s[2:3], v66, s13, v[114:115]
	ds_write_b64 v66, v[62:63]
	v_ashrrev_i32_e32 v66, 7, v110
	s_waitcnt vmcnt(17)
	v_cvt_pk_bf16_f32 v62, v90, v91
	v_cvt_pk_bf16_f32 v63, v92, v93
	v_mad_u64_u32 v[66:67], s[2:3], v66, s13, v[114:115]
	ds_write_b64 v66, v[62:63]
	v_ashrrev_i32_e32 v66, 7, v112
	v_mad_u64_u32 v[66:67], s[2:3], v66, s13, v[114:115]
	s_waitcnt vmcnt(15)
	v_and_b32_e32 v67, 0xffff0000, v98
	v_mul_f32_e32 v73, 0x3dd2d3e8, v67
	v_fma_f32 v73, -v73, v67, s33
	v_mul_f32_e32 v73, v73, v67
	v_exp_f32_e32 v73, v73
	v_cvt_pk_bf16_f32 v62, v94, v95
	v_cvt_pk_bf16_f32 v63, v96, v97
	ds_write_b64 v66, v[62:63]
	v_lshlrev_b32_e32 v66, 16, v98
	v_add_f32_e32 v73, 1.0, v73
	v_mul_f32_e32 v72, 0x3dd2d3e8, v66
	v_rcp_f32_e32 v73, v73
	v_fma_f32 v72, -v72, v66, s33
	v_mul_f32_e32 v72, v72, v66
	v_lshlrev_b32_e32 v69, 16, v99
	v_exp_f32_e32 v72, v72
	v_mul_f32_e32 v79, v73, v67
	v_mul_f32_e32 v67, 0x3dd2d3e8, v69
	v_fma_f32 v67, -v67, v69, s33
	v_mul_f32_e32 v67, v67, v69
	v_add_f32_e32 v72, 1.0, v72
	v_exp_f32_e32 v67, v67
	v_rcp_f32_e32 v72, v72
	v_lshlrev_b32_e32 v71, 16, v100
	v_and_b32_e32 v70, 0xffff0000, v99
	v_add_f32_e32 v67, 1.0, v67
	v_mul_f32_e32 v73, 0x3dd2d3e8, v71
	v_mul_f32_e32 v81, v72, v66
	v_mul_f32_e32 v72, 0x3dd2d3e8, v70
	v_rcp_f32_e32 v67, v67
	v_fma_f32 v73, -v73, v71, s33
	v_fma_f32 v72, -v72, v70, s33
	v_mul_f32_e32 v73, v73, v71
	v_mul_f32_e32 v72, v72, v70
	v_exp_f32_e32 v73, v73
	v_and_b32_e32 v74, 0xffff0000, v100
	v_exp_f32_e32 v72, v72
	v_mul_f32_e32 v80, v67, v69
	v_mul_f32_e32 v69, 0x3dd2d3e8, v74
	v_fma_f32 v69, -v69, v74, s33
	v_add_f32_e32 v67, 1.0, v73
	v_mul_f32_e32 v69, v69, v74
	v_add_f32_e32 v72, 1.0, v72
	v_rcp_f32_e32 v67, v67
	v_exp_f32_e32 v69, v69
	v_rcp_f32_e32 v72, v72
	v_lshlrev_b32_e32 v75, 16, v101
	v_and_b32_e32 v82, 0xffff0000, v101
	v_mul_f32_e32 v76, v67, v71
	v_add_f32_e32 v67, 1.0, v69
	v_mul_f32_e32 v69, 0x3dd2d3e8, v75
	v_mul_f32_e32 v78, v72, v70
	v_fma_f32 v69, -v69, v75, s33
	v_mul_f32_e32 v70, 0x3dd2d3e8, v82
	v_mul_f32_e32 v69, v69, v75
	v_fma_f32 v70, -v70, v82, s33
	v_rcp_f32_e32 v67, v67
	v_exp_f32_e32 v69, v69
	v_mul_f32_e32 v70, v70, v82
	v_exp_f32_e32 v70, v70
	v_mul_f32_e32 v66, v79, v79
	v_mul_f32_e32 v77, v67, v74
	v_add_f32_e32 v67, 1.0, v69
	v_fmac_f32_e32 v66, v81, v81
	v_rcp_f32_e32 v67, v67
	v_add_f32_e32 v69, 1.0, v70
	v_fmac_f32_e32 v66, v80, v80
	v_rcp_f32_e32 v69, v69
	v_and_b32_e32 v62, 64, v249
	v_fmac_f32_e32 v66, v78, v78
	v_add_u32_e32 v62, 64, v62
	v_xor_b32_e32 v63, 32, v249
	v_fmac_f32_e32 v66, v76, v76
	v_cmp_lt_i32_e32 vcc, v63, v62
	v_fmac_f32_e32 v66, v77, v77
	v_mul_f32_e32 v75, v67, v75
	v_cndmask_b32_e32 v63, v249, v63, vcc
	v_fmac_f32_e32 v66, v75, v75
	v_mul_f32_e32 v74, v69, v82
	v_lshlrev_b32_e32 v68, 2, v63
	v_fmac_f32_e32 v66, v74, v74
	v_mov_b32_e32 v67, v66
	s_nop 1
	v_permlane32_swap_b32_e32 v67, v66
	v_xor_b32_e32 v63, 16, v249
	v_cmp_lt_i32_e32 vcc, v63, v62
	v_and_b32_e32 v84, 0x78, v105
	v_readlane_b32 s2, v253, 40
	v_cndmask_b32_e32 v63, v249, v63, vcc
	v_lshlrev_b32_e32 v69, 2, v63
	s_waitcnt lgkmcnt(0)
	v_add_f32_e32 v66, v66, v67
	v_mov_b32_e32 v67, v66
	s_nop 1
	v_permlane16_swap_b32_e32 v67, v66
	v_xor_b32_e32 v63, 8, v249
	v_cmp_lt_i32_e32 vcc, v63, v62
	v_lshlrev_b32_e32 v206, 2, v84
	v_readlane_b32 s45, v251, 17
	v_cndmask_b32_e32 v63, v249, v63, vcc
	v_lshlrev_b32_e32 v70, 2, v63
	s_waitcnt lgkmcnt(0)
	v_add_f32_e32 v66, v66, v67
	s_nop 1
	v_mov_b32_dpp v67, v66 row_ror:8 row_mask:0xf bank_mask:0xf
	v_xor_b32_e32 v63, 4, v249
	v_cmp_lt_i32_e32 vcc, v63, v62
	v_readlane_b32 s46, v251, 18
	v_readlane_b32 s47, v251, 19
	v_cndmask_b32_e32 v63, v249, v63, vcc
	v_lshlrev_b32_e32 v71, 2, v63
	s_waitcnt lgkmcnt(0)
	v_add_f32_e32 v66, v66, v67
	v_xor_b32_e32 v63, 2, v249
	s_nop 1
	v_mov_b32_dpp v67, v66 row_shl:4 row_mask:0xf bank_mask:0x5
	v_mov_b32_dpp v67, v66 row_shr:4 row_mask:0xf bank_mask:0xa
	v_cmp_lt_i32_e32 vcc, v63, v62
	v_readlane_b32 s56, v251, 28
	v_readlane_b32 s57, v251, 29
	v_cndmask_b32_e32 v63, v249, v63, vcc
	v_lshlrev_b32_e32 v72, 2, v63
	v_xor_b32_e32 v63, 1, v249
	v_cmp_lt_i32_e32 vcc, v63, v62
	v_readlane_b32 s58, v251, 30
	v_readlane_b32 s59, v251, 31
	v_cndmask_b32_e32 v62, v249, v63, vcc
	s_waitcnt lgkmcnt(0)
	v_add_f32_e32 v63, v66, v67
	s_nop 1
	v_mov_b32_dpp v67, v63 quad_perm:[2,3,0,1] row_mask:0xf bank_mask:0xf
	v_lshlrev_b32_e32 v73, 2, v62
	v_bfe_u32 v66, v64, 4, 2
	v_cmp_eq_u32_e32 vcc, s2, v66
	s_mov_b64 s[20:21], s[52:53]
	s_waitcnt lgkmcnt(0)
	v_add_f32_e32 v82, v63, v67
	s_nop 1
	v_mov_b32_dpp v83, v82 quad_perm:[1,0,3,2] row_mask:0xf bank_mask:0xf
	v_lshl_add_u32 v67, v103, 5, 0
	v_lshl_add_u64 v[62:63], s[0:1], 0, v[206:207]
	v_mad_u32_u24 v67, v84, s13, v67
	v_lshrrev_b32_e32 v170, 6, v0
	v_lshlrev_b32_e32 v170, 1, v170
	v_and_b32_e32 v171, 15, v0
	v_xor_b32_e32 v168, v170, v171
	v_sub_u32_e32 v168, v168, v170
	v_lshl_add_u32 v168, v168, 4, v67
	v_or_b32_e32 v170, 1, v170
	v_xor_b32_e32 v169, v170, v171
	v_sub_u32_e32 v169, v169, v170
	v_lshl_add_u32 v169, v169, 4, v67
	s_mov_b64 s[22:23], s[54:55]
	s_and_saveexec_b64 s[0:1], vcc
	s_cbranch_execz .LBB0_1398
; __device__ __forceinline__ unsigned short f2bf(float f) { return (unsigned short)(cvt_pk_bf16(f, 0.f) & 0xffffu); }
; __device__ __forceinline__ void sgu_unit(const Params& p, int l, int un, LAS unsigned char* lds) {
;     ...
;         ss = wave_sum(ss); const float rinv = rsqrtf(ss * (1.0f / 512.0f) + EPS);
;         if ((lane >> 4) == h) { const int c0 = (lane & 15) * 8; const float* g = p.in[I_SGUNG] + l * 512 + h * 128 + c0;
; #pragma unroll
;             for (int j = 0; j < 8; ++j) Vl[(c0 + j) * 136 + q] = f2bf(f[j] * rinv * g[j]); } }
	s_waitcnt lgkmcnt(0)
	v_add_f32_e32 v82, v82, v83
	v_fmamk_f32 v82, v82, 0x3b000000, v246
	s_mov_b32 s2, 0x800000
	v_cmp_gt_f32_e64 s[2:3], s2, v82
	v_mul_f32_e32 v83, 0x4b800000, v82
	s_nop 0
	v_cndmask_b32_e64 v82, v82, v83, s[2:3]
	v_rsq_f32_e32 v82, v82
	s_nop 0
	v_mul_f32_e32 v83, 0x45800000, v82
	v_cndmask_b32_e64 v90, v82, v83, s[2:3]
	global_load_dwordx4 v[82:85], v[62:63], off offset:16
	global_load_dwordx4 v[86:89], v[62:63], off
	v_mul_f32_e32 v79, v79, v90
	v_mul_f32_e32 v76, v76, v90
	v_mul_f32_e32 v81, v81, v90
	v_mul_f32_e32 v78, v78, v90
	v_mul_f32_e32 v75, v75, v90
	v_mul_f32_e32 v74, v74, v90
	s_waitcnt vmcnt(1)
	v_mul_f32_e32 v76, v76, v82
	s_waitcnt vmcnt(0)
	v_mov_b32_e32 v160, v86
	v_mov_b32_e32 v161, v87
	v_mov_b32_e32 v162, v88
	v_mov_b32_e32 v163, v89
	v_mov_b32_e32 v164, v82
	v_mov_b32_e32 v165, v83
	v_mov_b32_e32 v166, v84
	v_mov_b32_e32 v167, v85
	v_mul_f32_e32 v79, v79, v87
	v_cvt_pk_bf16_f32 v79, v79, s0
	v_cvt_pk_bf16_f32 v76, v76, s0
	ds_write_b16 v168, v79 offset:35088
	v_mul_f32_e32 v79, v80, v90
	ds_write_b16 v168, v76 offset:35904
	v_mul_f32_e32 v76, v77, v90
	v_mul_f32_e32 v81, v81, v86
	v_mul_f32_e32 v79, v79, v88
	v_mul_f32_e32 v78, v78, v89
	v_mul_f32_e32 v76, v76, v83
	v_mul_f32_e32 v75, v75, v84
	v_mul_f32_e32 v74, v74, v85
	v_cvt_pk_bf16_f32 v81, v81, s0
	v_cvt_pk_bf16_f32 v79, v79, s0
	v_cvt_pk_bf16_f32 v78, v78, s0
	v_cvt_pk_bf16_f32 v76, v76, s0
	v_cvt_pk_bf16_f32 v75, v75, s0
	v_cvt_pk_bf16_f32 v74, v74, s0
	ds_write_b16 v168, v81 offset:34816
	ds_write_b16 v168, v79 offset:35360
	ds_write_b16 v168, v78 offset:35632
	ds_write_b16 v168, v76 offset:36176
	ds_write_b16 v168, v75 offset:36448
	ds_write_b16 v168, v74 offset:36720
